# expert phase: 16 id reads and 8 partial reads batched before their consumers; lane^16 / lane^32 exchanges by v_permlane16/32_swap instead of ds_bpermute where followed by add/max
# baseline (speedup 1.0000x reference)
;     __device__ __forceinline__ void operator()(const f32x4 (&acc)[2][2][4][2], const Unit& u, int wr, int wc, int fr, int fq) const {
;     ...
;                         float s = (v0[0] * v0[0] + v0[1] * v0[1]) + (v0[2] * v0[2] + v0[3] * v0[3]) + (v1[0] * v1[0] + v1[1] * v1[1]) + (v1[2] * v1[2] + v1[3] * v1[3]);
;                         s += __shfl_xor(s, 16); s += __shfl_xor(s, 32);
;                         const int head = (u.pn & 3) * 2 + bj;
;                         if (fq == 0) ssq[(size_t)((kind * 8 + head) * 4 + wc) * MT + row] = s;
.LBB0_232:
	s_andn2_b64 vcc, exec, s[2:3]
	s_lshl_b32 s8, s4, 3
	s_cbranch_vccnz .LBB0_236
	v_mul_f32_e32 v149, v125, v125
	v_mul_f32_e32 v150, v127, v127
	v_fmac_f32_e32 v149, v124, v124
	v_fmac_f32_e32 v150, v126, v126
	v_add_f32_e32 v149, v149, v150
	v_mul_f32_e32 v150, v121, v121
	v_fmac_f32_e32 v150, v120, v120
	v_add_f32_e32 v149, v150, v149
	v_mul_f32_e32 v150, v123, v123
	v_fmac_f32_e32 v150, v122, v122
	v_add_f32_e32 v149, v150, v149
	v_mov_b32_e32 v150, v149
	s_nop 1
	v_permlane16_swap_b32_e32 v150, v149
	s_waitcnt lgkmcnt(0)
	v_add_f32_e32 v149, v149, v150
	ds_bpermute_b32 v150, v158, v149
	s_and_saveexec_b64 s[2:3], s[34:35]
	s_cbranch_execz .LBB0_235
	s_lshl_b32 s4, s66, 1
	s_and_b32 s4, s4, 6
	s_or_b32 s4, s4, s8
	s_lshl_b32 s4, s4, 2
	s_or_b32 s4, s4, s27
	s_ashr_i32 s5, s4, 31
	s_lshl_b64 s[4:5], s[4:5], 16
	s_add_u32 s4, s88, s4
	s_addc_u32 s5, s89, s5
	s_waitcnt lgkmcnt(0)
	v_add_f32_e32 v149, v149, v150
	v_lshl_add_u64 v[150:151], v[142:143], 2, s[4:5]
	global_store_dword v[150:151], v149, off

;     __device__ __forceinline__ void operator()(const f32x4 (&acc)[2][2][4][2], const Unit& u, int wr, int wc, int fr, int fq) const {
;     ...
;                         float s = (v0[0] * v0[0] + v0[1] * v0[1]) + (v0[2] * v0[2] + v0[3] * v0[3]) + (v1[0] * v1[0] + v1[1] * v1[1]) + (v1[2] * v1[2] + v1[3] * v1[3]);
;                         s += __shfl_xor(s, 16); s += __shfl_xor(s, 32);
;                         const int head = (u.pn & 3) * 2 + bj;
;                         if (fq == 0) ssq[(size_t)((kind * 8 + head) * 4 + wc) * MT + row] = s;
.LBB0_242:
	s_andn2_b64 vcc, exec, s[0:1]
	s_cbranch_vccnz .LBB0_246
	v_mul_f32_e32 v124, v117, v117
	v_mul_f32_e32 v125, v119, v119
	v_fmac_f32_e32 v124, v116, v116
	v_fmac_f32_e32 v125, v118, v118
	v_add_f32_e32 v124, v124, v125
	v_mul_f32_e32 v125, v113, v113
	v_fmac_f32_e32 v125, v112, v112
	v_add_f32_e32 v124, v125, v124
	v_mul_f32_e32 v125, v115, v115
	v_fmac_f32_e32 v125, v114, v114
	v_add_f32_e32 v124, v125, v124
	v_mov_b32_e32 v125, v124
	s_nop 1
	v_permlane16_swap_b32_e32 v125, v124
	s_waitcnt lgkmcnt(0)
	v_add_f32_e32 v124, v124, v125
	ds_bpermute_b32 v125, v158, v124
	s_and_saveexec_b64 s[0:1], s[34:35]
	s_cbranch_execz .LBB0_245
	s_lshl_b32 s2, s66, 1
	s_and_b32 s2, s2, 6
	s_or_b32 s2, s2, s8
	s_lshl_b32 s2, s2, 2
	s_or_b32 s2, s2, s64
	s_ashr_i32 s3, s2, 31
	s_lshl_b64 s[2:3], s[2:3], 16
	s_add_u32 s2, s88, s2
	s_addc_u32 s3, s89, s3
	s_waitcnt lgkmcnt(0)
	v_add_f32_e32 v126, v124, v125
	v_lshl_add_u64 v[124:125], v[142:143], 2, s[2:3]
	global_store_dword v[124:125], v126, off

;     __device__ __forceinline__ void operator()(const f32x4 (&acc)[2][2][4][2], const Unit& u, int wr, int wc, int fr, int fq) const {
;     ...
;                         float s = (v0[0] * v0[0] + v0[1] * v0[1]) + (v0[2] * v0[2] + v0[3] * v0[3]) + (v1[0] * v1[0] + v1[1] * v1[1]) + (v1[2] * v1[2] + v1[3] * v1[3]);
;                         s += __shfl_xor(s, 16); s += __shfl_xor(s, 32);
;                         const int head = (u.pn & 3) * 2 + bj;
;                         if (fq == 0) ssq[(size_t)((kind * 8 + head) * 4 + wc) * MT + row] = s;
.LBB0_252:
	s_andn2_b64 vcc, exec, s[0:1]
	s_cbranch_vccnz .LBB0_256
	v_mul_f32_e32 v113, v109, v109
	v_mul_f32_e32 v116, v111, v111
	v_fmac_f32_e32 v113, v108, v108
	v_fmac_f32_e32 v116, v110, v110
	v_add_f32_e32 v113, v113, v116
	v_mul_f32_e32 v116, v105, v105
	v_fmac_f32_e32 v116, v104, v104
	v_add_f32_e32 v113, v116, v113
	v_mul_f32_e32 v116, v107, v107
	v_fmac_f32_e32 v116, v106, v106
	v_add_f32_e32 v113, v116, v113
	v_mov_b32_e32 v116, v113
	s_nop 1
	v_permlane16_swap_b32_e32 v116, v113
	s_waitcnt lgkmcnt(0)
	v_add_f32_e32 v113, v113, v116
	ds_bpermute_b32 v116, v158, v113
	s_and_saveexec_b64 s[0:1], s[34:35]
	s_cbranch_execz .LBB0_255
	s_lshl_b32 s2, s66, 1
	s_and_b32 s2, s2, 6
	s_or_b32 s2, s2, s8
	s_lshl_b32 s2, s2, 2
	s_or_b32 s2, s2, s27
	s_ashr_i32 s3, s2, 31
	s_lshl_b64 s[2:3], s[2:3], 16
	s_add_u32 s2, s88, s2
	s_addc_u32 s3, s89, s3
	s_waitcnt lgkmcnt(0)
	v_add_f32_e32 v113, v113, v116
	v_lshl_add_u64 v[116:117], v[142:143], 2, s[2:3]
	global_store_dword v[116:117], v113, off offset:64

;     __device__ __forceinline__ void operator()(const f32x4 (&acc)[2][2][4][2], const Unit& u, int wr, int wc, int fr, int fq) const {
;     ...
;                         float s = (v0[0] * v0[0] + v0[1] * v0[1]) + (v0[2] * v0[2] + v0[3] * v0[3]) + (v1[0] * v1[0] + v1[1] * v1[1]) + (v1[2] * v1[2] + v1[3] * v1[3]);
;                         s += __shfl_xor(s, 16); s += __shfl_xor(s, 32);
;                         const int head = (u.pn & 3) * 2 + bj;
;                         if (fq == 0) ssq[(size_t)((kind * 8 + head) * 4 + wc) * MT + row] = s;
.LBB0_262:
	s_andn2_b64 vcc, exec, s[0:1]
	s_cbranch_vccnz .LBB0_266
	v_mul_f32_e32 v106, v101, v101
	v_mul_f32_e32 v107, v103, v103
	v_fmac_f32_e32 v106, v100, v100
	v_fmac_f32_e32 v107, v102, v102
	v_add_f32_e32 v106, v106, v107
	v_mul_f32_e32 v107, v97, v97
	v_fmac_f32_e32 v107, v96, v96
	v_add_f32_e32 v106, v107, v106
	v_mul_f32_e32 v107, v99, v99
	v_fmac_f32_e32 v107, v98, v98
	v_add_f32_e32 v106, v107, v106
	v_mov_b32_e32 v107, v106
	s_nop 1
	v_permlane16_swap_b32_e32 v107, v106
	s_waitcnt lgkmcnt(0)
	v_add_f32_e32 v106, v106, v107
	ds_bpermute_b32 v107, v158, v106
	s_and_saveexec_b64 s[0:1], s[34:35]
	s_cbranch_execz .LBB0_265
	s_lshl_b32 s2, s66, 1
	s_and_b32 s2, s2, 6
	s_or_b32 s2, s2, s8
	s_lshl_b32 s2, s2, 2
	s_or_b32 s2, s2, s64
	s_ashr_i32 s3, s2, 31
	s_lshl_b64 s[2:3], s[2:3], 16
	s_add_u32 s2, s88, s2
	s_addc_u32 s3, s89, s3
	s_waitcnt lgkmcnt(0)
	v_add_f32_e32 v108, v106, v107
	v_lshl_add_u64 v[106:107], v[142:143], 2, s[2:3]
	global_store_dword v[106:107], v108, off offset:64

;     __device__ __forceinline__ void operator()(const f32x4 (&acc)[2][2][4][2], const Unit& u, int wr, int wc, int fr, int fq) const {
;     ...
;                         float s = (v0[0] * v0[0] + v0[1] * v0[1]) + (v0[2] * v0[2] + v0[3] * v0[3]) + (v1[0] * v1[0] + v1[1] * v1[1]) + (v1[2] * v1[2] + v1[3] * v1[3]);
;                         s += __shfl_xor(s, 16); s += __shfl_xor(s, 32);
;                         const int head = (u.pn & 3) * 2 + bj;
;                         if (fq == 0) ssq[(size_t)((kind * 8 + head) * 4 + wc) * MT + row] = s;
.LBB0_272:
	s_andn2_b64 vcc, exec, s[0:1]
	s_cbranch_vccnz .LBB0_276
	v_mul_f32_e32 v97, v93, v93
	v_mul_f32_e32 v100, v95, v95
	v_fmac_f32_e32 v97, v92, v92
	v_fmac_f32_e32 v100, v94, v94
	v_add_f32_e32 v97, v97, v100
	v_mul_f32_e32 v100, v89, v89
	v_fmac_f32_e32 v100, v88, v88
	v_add_f32_e32 v97, v100, v97
	v_mul_f32_e32 v100, v91, v91
	v_fmac_f32_e32 v100, v90, v90
	v_add_f32_e32 v97, v100, v97
	v_mov_b32_e32 v100, v97
	s_nop 1
	v_permlane16_swap_b32_e32 v100, v97
	s_waitcnt lgkmcnt(0)
	v_add_f32_e32 v97, v97, v100
	ds_bpermute_b32 v100, v158, v97
	s_and_saveexec_b64 s[0:1], s[34:35]
	s_cbranch_execz .LBB0_275
	s_lshl_b32 s2, s66, 1
	s_and_b32 s2, s2, 6
	s_or_b32 s2, s2, s8
	s_lshl_b32 s2, s2, 2
	s_or_b32 s2, s2, s27
	s_ashr_i32 s3, s2, 31
	s_lshl_b64 s[2:3], s[2:3], 16
	s_add_u32 s2, s88, s2
	s_addc_u32 s3, s89, s3
	s_waitcnt lgkmcnt(0)
	v_add_f32_e32 v97, v97, v100
	v_lshl_add_u64 v[100:101], v[142:143], 2, s[2:3]
	global_store_dword v[100:101], v97, off offset:128

;     __device__ __forceinline__ void operator()(const f32x4 (&acc)[2][2][4][2], const Unit& u, int wr, int wc, int fr, int fq) const {
;     ...
;                         float s = (v0[0] * v0[0] + v0[1] * v0[1]) + (v0[2] * v0[2] + v0[3] * v0[3]) + (v1[0] * v1[0] + v1[1] * v1[1]) + (v1[2] * v1[2] + v1[3] * v1[3]);
;                         s += __shfl_xor(s, 16); s += __shfl_xor(s, 32);
;                         const int head = (u.pn & 3) * 2 + bj;
;                         if (fq == 0) ssq[(size_t)((kind * 8 + head) * 4 + wc) * MT + row] = s;
.LBB0_282:
	s_andn2_b64 vcc, exec, s[0:1]
	s_cbranch_vccnz .LBB0_286
	v_mul_f32_e32 v90, v85, v85
	v_mul_f32_e32 v91, v87, v87
	v_fmac_f32_e32 v90, v84, v84
	v_fmac_f32_e32 v91, v86, v86
	v_add_f32_e32 v90, v90, v91
	v_mul_f32_e32 v91, v81, v81
	v_fmac_f32_e32 v91, v80, v80
	v_add_f32_e32 v90, v91, v90
	v_mul_f32_e32 v91, v83, v83
	v_fmac_f32_e32 v91, v82, v82
	v_add_f32_e32 v90, v91, v90
	v_mov_b32_e32 v91, v90
	s_nop 1
	v_permlane16_swap_b32_e32 v91, v90
	s_waitcnt lgkmcnt(0)
	v_add_f32_e32 v90, v90, v91
	ds_bpermute_b32 v91, v158, v90
	s_and_saveexec_b64 s[0:1], s[34:35]
	s_cbranch_execz .LBB0_285
	s_lshl_b32 s2, s66, 1
	s_and_b32 s2, s2, 6
	s_or_b32 s2, s2, s8
	s_lshl_b32 s2, s2, 2
	s_or_b32 s2, s2, s64
	s_ashr_i32 s3, s2, 31
	s_lshl_b64 s[2:3], s[2:3], 16
	s_add_u32 s2, s88, s2
	s_addc_u32 s3, s89, s3
	s_waitcnt lgkmcnt(0)
	v_add_f32_e32 v92, v90, v91
	v_lshl_add_u64 v[90:91], v[142:143], 2, s[2:3]
	global_store_dword v[90:91], v92, off offset:128

;     __device__ __forceinline__ void operator()(const f32x4 (&acc)[2][2][4][2], const Unit& u, int wr, int wc, int fr, int fq) const {
;     ...
;                         float s = (v0[0] * v0[0] + v0[1] * v0[1]) + (v0[2] * v0[2] + v0[3] * v0[3]) + (v1[0] * v1[0] + v1[1] * v1[1]) + (v1[2] * v1[2] + v1[3] * v1[3]);
;                         s += __shfl_xor(s, 16); s += __shfl_xor(s, 32);
;                         const int head = (u.pn & 3) * 2 + bj;
;                         if (fq == 0) ssq[(size_t)((kind * 8 + head) * 4 + wc) * MT + row] = s;
.LBB0_292:
	s_andn2_b64 vcc, exec, s[0:1]
	s_cbranch_vccnz .LBB0_296
	v_mul_f32_e32 v81, v77, v77
	v_mul_f32_e32 v84, v79, v79
	v_fmac_f32_e32 v81, v76, v76
	v_fmac_f32_e32 v84, v78, v78
	v_add_f32_e32 v81, v81, v84
	v_mul_f32_e32 v84, v73, v73
	v_fmac_f32_e32 v84, v72, v72
	v_add_f32_e32 v81, v84, v81
	v_mul_f32_e32 v84, v75, v75
	v_fmac_f32_e32 v84, v74, v74
	v_add_f32_e32 v81, v84, v81
	v_mov_b32_e32 v84, v81
	s_nop 1
	v_permlane16_swap_b32_e32 v84, v81
	s_waitcnt lgkmcnt(0)
	v_add_f32_e32 v81, v81, v84
	ds_bpermute_b32 v84, v158, v81
	s_and_saveexec_b64 s[0:1], s[34:35]
	s_cbranch_execz .LBB0_295
	s_lshl_b32 s2, s66, 1
	s_and_b32 s2, s2, 6
	s_or_b32 s2, s2, s8
	s_lshl_b32 s2, s2, 2
	s_or_b32 s2, s2, s27
	s_ashr_i32 s3, s2, 31
	s_lshl_b64 s[2:3], s[2:3], 16
	s_add_u32 s2, s88, s2
	s_addc_u32 s3, s89, s3
	s_waitcnt lgkmcnt(0)
	v_add_f32_e32 v81, v81, v84
	v_lshl_add_u64 v[84:85], v[142:143], 2, s[2:3]
	global_store_dword v[84:85], v81, off offset:192

;     __device__ __forceinline__ void operator()(const f32x4 (&acc)[2][2][4][2], const Unit& u, int wr, int wc, int fr, int fq) const {
;     ...
;                         float s = (v0[0] * v0[0] + v0[1] * v0[1]) + (v0[2] * v0[2] + v0[3] * v0[3]) + (v1[0] * v1[0] + v1[1] * v1[1]) + (v1[2] * v1[2] + v1[3] * v1[3]);
;                         s += __shfl_xor(s, 16); s += __shfl_xor(s, 32);
;                         const int head = (u.pn & 3) * 2 + bj;
;                         if (fq == 0) ssq[(size_t)((kind * 8 + head) * 4 + wc) * MT + row] = s;
.LBB0_302:
	s_andn2_b64 vcc, exec, s[0:1]
	s_cbranch_vccnz .LBB0_306
	v_mul_f32_e32 v74, v69, v69
	v_mul_f32_e32 v75, v71, v71
	v_fmac_f32_e32 v74, v68, v68
	v_fmac_f32_e32 v75, v70, v70
	v_add_f32_e32 v74, v74, v75
	v_mul_f32_e32 v75, v65, v65
	v_fmac_f32_e32 v75, v64, v64
	v_add_f32_e32 v74, v75, v74
	v_mul_f32_e32 v75, v67, v67
	v_fmac_f32_e32 v75, v66, v66
	v_add_f32_e32 v74, v75, v74
	v_mov_b32_e32 v75, v74
	s_nop 1
	v_permlane16_swap_b32_e32 v75, v74
	s_waitcnt lgkmcnt(0)
	v_add_f32_e32 v74, v74, v75
	ds_bpermute_b32 v75, v158, v74
	s_and_saveexec_b64 s[0:1], s[34:35]
	s_cbranch_execz .LBB0_305
	s_lshl_b32 s2, s66, 1
	s_and_b32 s2, s2, 6
	s_or_b32 s2, s2, s8
	s_lshl_b32 s2, s2, 2
	s_or_b32 s2, s2, s64
	s_ashr_i32 s3, s2, 31
	s_lshl_b64 s[2:3], s[2:3], 16
	s_add_u32 s2, s88, s2
	s_addc_u32 s3, s89, s3
	s_waitcnt lgkmcnt(0)
	v_add_f32_e32 v76, v74, v75
	v_lshl_add_u64 v[74:75], v[142:143], 2, s[2:3]
	global_store_dword v[74:75], v76, off offset:192

;     __device__ __forceinline__ void operator()(const f32x4 (&acc)[2][2][4][2], const Unit& u, int wr, int wc, int fr, int fq) const {
;     ...
;                         float s = (v0[0] * v0[0] + v0[1] * v0[1]) + (v0[2] * v0[2] + v0[3] * v0[3]) + (v1[0] * v1[0] + v1[1] * v1[1]) + (v1[2] * v1[2] + v1[3] * v1[3]);
;                         s += __shfl_xor(s, 16); s += __shfl_xor(s, 32);
;                         const int head = (u.pn & 3) * 2 + bj;
;                         if (fq == 0) ssq[(size_t)((kind * 8 + head) * 4 + wc) * MT + row] = s;
.LBB0_312:
	s_andn2_b64 vcc, exec, s[0:1]
	s_cbranch_vccnz .LBB0_316
	v_mul_f32_e32 v65, v61, v61
	v_mul_f32_e32 v66, v63, v63
	v_fmac_f32_e32 v65, v60, v60
	v_fmac_f32_e32 v66, v62, v62
	v_add_f32_e32 v65, v65, v66
	v_mul_f32_e32 v66, v57, v57
	v_fmac_f32_e32 v66, v56, v56
	v_add_f32_e32 v65, v66, v65
	v_mul_f32_e32 v66, v59, v59
	v_fmac_f32_e32 v66, v58, v58
	v_add_f32_e32 v65, v66, v65
	v_mov_b32_e32 v66, v65
	s_nop 1
	v_permlane16_swap_b32_e32 v66, v65
	s_waitcnt lgkmcnt(0)
	v_add_f32_e32 v65, v65, v66
	ds_bpermute_b32 v66, v158, v65
	s_and_saveexec_b64 s[0:1], s[34:35]
	s_cbranch_execz .LBB0_315
	s_lshl_b32 s2, s66, 1
	s_and_b32 s2, s2, 6
	s_or_b32 s2, s2, s8
	s_lshl_b32 s2, s2, 2
	s_or_b32 s2, s2, s27
	s_ashr_i32 s3, s2, 31
	s_lshl_b64 s[2:3], s[2:3], 16
	s_add_u32 s2, s88, s2
	s_addc_u32 s3, s89, s3
	s_waitcnt lgkmcnt(0)
	v_add_f32_e32 v65, v65, v66
	v_lshl_add_u64 v[66:67], v[142:143], 2, s[2:3]
	global_store_dword v[66:67], v65, off offset:512

;     __device__ __forceinline__ void operator()(const f32x4 (&acc)[2][2][4][2], const Unit& u, int wr, int wc, int fr, int fq) const {
;     ...
;                         float s = (v0[0] * v0[0] + v0[1] * v0[1]) + (v0[2] * v0[2] + v0[3] * v0[3]) + (v1[0] * v1[0] + v1[1] * v1[1]) + (v1[2] * v1[2] + v1[3] * v1[3]);
;                         s += __shfl_xor(s, 16); s += __shfl_xor(s, 32);
;                         const int head = (u.pn & 3) * 2 + bj;
;                         if (fq == 0) ssq[(size_t)((kind * 8 + head) * 4 + wc) * MT + row] = s;
.LBB0_322:
	s_andn2_b64 vcc, exec, s[0:1]
	s_cbranch_vccnz .LBB0_326
	v_mul_f32_e32 v58, v53, v53
	v_mul_f32_e32 v59, v55, v55
	v_fmac_f32_e32 v58, v52, v52
	v_fmac_f32_e32 v59, v54, v54
	v_add_f32_e32 v58, v58, v59
	v_mul_f32_e32 v59, v49, v49
	v_fmac_f32_e32 v59, v48, v48
	v_add_f32_e32 v58, v59, v58
	v_mul_f32_e32 v59, v51, v51
	v_fmac_f32_e32 v59, v50, v50
	v_add_f32_e32 v58, v59, v58
	v_mov_b32_e32 v59, v58
	s_nop 1
	v_permlane16_swap_b32_e32 v59, v58
	s_waitcnt lgkmcnt(0)
	v_add_f32_e32 v58, v58, v59
	ds_bpermute_b32 v59, v158, v58
	s_and_saveexec_b64 s[0:1], s[34:35]
	s_cbranch_execz .LBB0_325
	s_lshl_b32 s2, s66, 1
	s_and_b32 s2, s2, 6
	s_or_b32 s2, s2, s8
	s_lshl_b32 s2, s2, 2
	s_or_b32 s2, s2, s64
	s_ashr_i32 s3, s2, 31
	s_lshl_b64 s[2:3], s[2:3], 16
	s_add_u32 s2, s88, s2
	s_addc_u32 s3, s89, s3
	s_waitcnt lgkmcnt(0)
	v_add_f32_e32 v60, v58, v59
	v_lshl_add_u64 v[58:59], v[142:143], 2, s[2:3]
	global_store_dword v[58:59], v60, off offset:512

;     __device__ __forceinline__ void operator()(const f32x4 (&acc)[2][2][4][2], const Unit& u, int wr, int wc, int fr, int fq) const {
;     ...
;                         float s = (v0[0] * v0[0] + v0[1] * v0[1]) + (v0[2] * v0[2] + v0[3] * v0[3]) + (v1[0] * v1[0] + v1[1] * v1[1]) + (v1[2] * v1[2] + v1[3] * v1[3]);
;                         s += __shfl_xor(s, 16); s += __shfl_xor(s, 32);
;                         const int head = (u.pn & 3) * 2 + bj;
;                         if (fq == 0) ssq[(size_t)((kind * 8 + head) * 4 + wc) * MT + row] = s;
.LBB0_332:
	s_andn2_b64 vcc, exec, s[0:1]
	s_cbranch_vccnz .LBB0_336
	v_mul_f32_e32 v49, v45, v45
	v_mul_f32_e32 v50, v47, v47
	v_fmac_f32_e32 v49, v44, v44
	v_fmac_f32_e32 v50, v46, v46
	v_add_f32_e32 v49, v49, v50
	v_mul_f32_e32 v50, v41, v41
	v_fmac_f32_e32 v50, v40, v40
	v_add_f32_e32 v49, v50, v49
	v_mul_f32_e32 v50, v43, v43
	v_fmac_f32_e32 v50, v42, v42
	v_add_f32_e32 v49, v50, v49
	v_mov_b32_e32 v50, v49
	s_nop 1
	v_permlane16_swap_b32_e32 v50, v49
	s_waitcnt lgkmcnt(0)
	v_add_f32_e32 v49, v49, v50
	ds_bpermute_b32 v50, v158, v49
	s_and_saveexec_b64 s[0:1], s[34:35]
	s_cbranch_execz .LBB0_335
	s_lshl_b32 s2, s66, 1
	s_and_b32 s2, s2, 6
	s_or_b32 s2, s2, s8
	s_lshl_b32 s2, s2, 2
	s_or_b32 s2, s2, s27
	s_ashr_i32 s3, s2, 31
	s_lshl_b64 s[2:3], s[2:3], 16
	s_add_u32 s2, s88, s2
	s_addc_u32 s3, s89, s3
	s_waitcnt lgkmcnt(0)
	v_add_f32_e32 v49, v49, v50
	v_lshl_add_u64 v[50:51], v[142:143], 2, s[2:3]
	global_store_dword v[50:51], v49, off offset:576

;     __device__ __forceinline__ void operator()(const f32x4 (&acc)[2][2][4][2], const Unit& u, int wr, int wc, int fr, int fq) const {
;     ...
;                         float s = (v0[0] * v0[0] + v0[1] * v0[1]) + (v0[2] * v0[2] + v0[3] * v0[3]) + (v1[0] * v1[0] + v1[1] * v1[1]) + (v1[2] * v1[2] + v1[3] * v1[3]);
;                         s += __shfl_xor(s, 16); s += __shfl_xor(s, 32);
;                         const int head = (u.pn & 3) * 2 + bj;
;                         if (fq == 0) ssq[(size_t)((kind * 8 + head) * 4 + wc) * MT + row] = s;
.LBB0_342:
	s_andn2_b64 vcc, exec, s[0:1]
	s_cbranch_vccnz .LBB0_346
	v_mul_f32_e32 v42, v37, v37
	v_mul_f32_e32 v43, v39, v39
	v_fmac_f32_e32 v42, v36, v36
	v_fmac_f32_e32 v43, v38, v38
	v_add_f32_e32 v42, v42, v43
	v_mul_f32_e32 v43, v33, v33
	v_fmac_f32_e32 v43, v32, v32
	v_add_f32_e32 v42, v43, v42
	v_mul_f32_e32 v43, v35, v35
	v_fmac_f32_e32 v43, v34, v34
	v_add_f32_e32 v42, v43, v42
	v_mov_b32_e32 v43, v42
	s_nop 1
	v_permlane16_swap_b32_e32 v43, v42
	s_waitcnt lgkmcnt(0)
	v_add_f32_e32 v42, v42, v43
	ds_bpermute_b32 v43, v158, v42
	s_and_saveexec_b64 s[0:1], s[34:35]
	s_cbranch_execz .LBB0_345
	s_lshl_b32 s2, s66, 1
	s_and_b32 s2, s2, 6
	s_or_b32 s2, s2, s8
	s_lshl_b32 s2, s2, 2
	s_or_b32 s2, s2, s64
	s_ashr_i32 s3, s2, 31
	s_lshl_b64 s[2:3], s[2:3], 16
	s_add_u32 s2, s88, s2
	s_addc_u32 s3, s89, s3
	s_waitcnt lgkmcnt(0)
	v_add_f32_e32 v44, v42, v43
	v_lshl_add_u64 v[42:43], v[142:143], 2, s[2:3]
	global_store_dword v[42:43], v44, off offset:576

;     __device__ __forceinline__ void operator()(const f32x4 (&acc)[2][2][4][2], const Unit& u, int wr, int wc, int fr, int fq) const {
;     ...
;                         float s = (v0[0] * v0[0] + v0[1] * v0[1]) + (v0[2] * v0[2] + v0[3] * v0[3]) + (v1[0] * v1[0] + v1[1] * v1[1]) + (v1[2] * v1[2] + v1[3] * v1[3]);
;                         s += __shfl_xor(s, 16); s += __shfl_xor(s, 32);
;                         const int head = (u.pn & 3) * 2 + bj;
;                         if (fq == 0) ssq[(size_t)((kind * 8 + head) * 4 + wc) * MT + row] = s;
.LBB0_352:
	s_andn2_b64 vcc, exec, s[0:1]
	s_cbranch_vccnz .LBB0_356
	v_mul_f32_e32 v33, v29, v29
	v_mul_f32_e32 v34, v31, v31
	v_fmac_f32_e32 v33, v28, v28
	v_fmac_f32_e32 v34, v30, v30
	v_add_f32_e32 v33, v33, v34
	v_mul_f32_e32 v34, v25, v25
	v_fmac_f32_e32 v34, v24, v24
	v_add_f32_e32 v33, v34, v33
	v_mul_f32_e32 v34, v27, v27
	v_fmac_f32_e32 v34, v26, v26
	v_add_f32_e32 v33, v34, v33
	v_mov_b32_e32 v34, v33
	s_nop 1
	v_permlane16_swap_b32_e32 v34, v33
	s_waitcnt lgkmcnt(0)
	v_add_f32_e32 v33, v33, v34
	ds_bpermute_b32 v34, v158, v33
	s_and_saveexec_b64 s[0:1], s[34:35]
	s_cbranch_execz .LBB0_355
	s_lshl_b32 s2, s66, 1
	s_and_b32 s2, s2, 6
	s_or_b32 s2, s2, s8
	s_lshl_b32 s2, s2, 2
	s_or_b32 s2, s2, s27
	s_ashr_i32 s3, s2, 31
	s_lshl_b64 s[2:3], s[2:3], 16
	s_add_u32 s2, s88, s2
	s_addc_u32 s3, s89, s3
	s_waitcnt lgkmcnt(0)
	v_add_f32_e32 v33, v33, v34
	v_lshl_add_u64 v[34:35], v[142:143], 2, s[2:3]
	global_store_dword v[34:35], v33, off offset:640

;     __device__ __forceinline__ void operator()(const f32x4 (&acc)[2][2][4][2], const Unit& u, int wr, int wc, int fr, int fq) const {
;     ...
;                         float s = (v0[0] * v0[0] + v0[1] * v0[1]) + (v0[2] * v0[2] + v0[3] * v0[3]) + (v1[0] * v1[0] + v1[1] * v1[1]) + (v1[2] * v1[2] + v1[3] * v1[3]);
;                         s += __shfl_xor(s, 16); s += __shfl_xor(s, 32);
;                         const int head = (u.pn & 3) * 2 + bj;
;                         if (fq == 0) ssq[(size_t)((kind * 8 + head) * 4 + wc) * MT + row] = s;
.LBB0_362:
	s_andn2_b64 vcc, exec, s[0:1]
	s_cbranch_vccnz .LBB0_366
	v_mul_f32_e32 v26, v21, v21
	v_mul_f32_e32 v27, v23, v23
	v_fmac_f32_e32 v26, v20, v20
	v_fmac_f32_e32 v27, v22, v22
	v_add_f32_e32 v26, v26, v27
	v_mul_f32_e32 v27, v17, v17
	v_fmac_f32_e32 v27, v16, v16
	v_add_f32_e32 v26, v27, v26
	v_mul_f32_e32 v27, v19, v19
	v_fmac_f32_e32 v27, v18, v18
	v_add_f32_e32 v26, v27, v26
	v_mov_b32_e32 v27, v26
	s_nop 1
	v_permlane16_swap_b32_e32 v27, v26
	s_waitcnt lgkmcnt(0)
	v_add_f32_e32 v26, v26, v27
	ds_bpermute_b32 v27, v158, v26
	s_and_saveexec_b64 s[0:1], s[34:35]
	s_cbranch_execz .LBB0_365
	s_lshl_b32 s2, s66, 1
	s_and_b32 s2, s2, 6
	s_or_b32 s2, s2, s8
	s_lshl_b32 s2, s2, 2
	s_or_b32 s2, s2, s64
	s_ashr_i32 s3, s2, 31
	s_lshl_b64 s[2:3], s[2:3], 16
	s_add_u32 s2, s88, s2
	s_addc_u32 s3, s89, s3
	s_waitcnt lgkmcnt(0)
	v_add_f32_e32 v28, v26, v27
	v_lshl_add_u64 v[26:27], v[142:143], 2, s[2:3]
	global_store_dword v[26:27], v28, off offset:640

;     __device__ __forceinline__ void operator()(const f32x4 (&acc)[2][2][4][2], const Unit& u, int wr, int wc, int fr, int fq) const {
;     ...
;                         float s = (v0[0] * v0[0] + v0[1] * v0[1]) + (v0[2] * v0[2] + v0[3] * v0[3]) + (v1[0] * v1[0] + v1[1] * v1[1]) + (v1[2] * v1[2] + v1[3] * v1[3]);
;                         s += __shfl_xor(s, 16); s += __shfl_xor(s, 32);
;                         const int head = (u.pn & 3) * 2 + bj;
;                         if (fq == 0) ssq[(size_t)((kind * 8 + head) * 4 + wc) * MT + row] = s;
.LBB0_372:
	s_andn2_b64 vcc, exec, s[0:1]
	s_cbranch_vccnz .LBB0_376
	v_mul_f32_e32 v17, v13, v13
	v_mul_f32_e32 v18, v15, v15
	v_fmac_f32_e32 v17, v12, v12
	v_fmac_f32_e32 v18, v14, v14
	v_add_f32_e32 v17, v17, v18
	v_mul_f32_e32 v18, v9, v9
	v_fmac_f32_e32 v18, v8, v8
	v_add_f32_e32 v17, v18, v17
	v_mul_f32_e32 v18, v11, v11
	v_fmac_f32_e32 v18, v10, v10
	v_add_f32_e32 v17, v18, v17
	v_mov_b32_e32 v18, v17
	s_nop 1
	v_permlane16_swap_b32_e32 v18, v17
	s_waitcnt lgkmcnt(0)
	v_add_f32_e32 v17, v17, v18
	ds_bpermute_b32 v18, v158, v17
	s_and_saveexec_b64 s[0:1], s[34:35]
	s_cbranch_execz .LBB0_375
	s_lshl_b32 s2, s66, 1
	s_and_b32 s2, s2, 6
	s_or_b32 s2, s2, s8
	s_lshl_b32 s2, s2, 2
	s_or_b32 s2, s2, s27
	s_ashr_i32 s3, s2, 31
	s_lshl_b64 s[2:3], s[2:3], 16
	s_add_u32 s2, s88, s2
	s_addc_u32 s3, s89, s3
	s_waitcnt lgkmcnt(0)
	v_add_f32_e32 v17, v17, v18
	v_lshl_add_u64 v[18:19], v[142:143], 2, s[2:3]
	global_store_dword v[18:19], v17, off offset:704

;     __device__ __forceinline__ void operator()(const f32x4 (&acc)[2][2][4][2], const Unit& u, int wr, int wc, int fr, int fq) const {
;     ...
;                         float s = (v0[0] * v0[0] + v0[1] * v0[1]) + (v0[2] * v0[2] + v0[3] * v0[3]) + (v1[0] * v1[0] + v1[1] * v1[1]) + (v1[2] * v1[2] + v1[3] * v1[3]);
;                         s += __shfl_xor(s, 16); s += __shfl_xor(s, 32);
;                         const int head = (u.pn & 3) * 2 + bj;
;                         if (fq == 0) ssq[(size_t)((kind * 8 + head) * 4 + wc) * MT + row] = s;
.LBB0_382:
	s_andn2_b64 vcc, exec, s[0:1]
	s_cbranch_vccnz .LBB0_386
	v_mul_f32_e32 v10, v5, v5
	v_mul_f32_e32 v11, v7, v7
	v_fmac_f32_e32 v10, v4, v4
	v_fmac_f32_e32 v11, v6, v6
	v_add_f32_e32 v10, v10, v11
	v_mul_f32_e32 v11, v1, v1
	v_fmac_f32_e32 v11, v0, v0
	v_add_f32_e32 v10, v11, v10
	v_mul_f32_e32 v11, v3, v3
	v_fmac_f32_e32 v11, v2, v2
	v_add_f32_e32 v10, v11, v10
	v_mov_b32_e32 v11, v10
	s_nop 1
	v_permlane16_swap_b32_e32 v11, v10
	s_waitcnt lgkmcnt(0)
	v_add_f32_e32 v10, v10, v11
	ds_bpermute_b32 v11, v158, v10
	s_and_saveexec_b64 s[0:1], s[34:35]
	s_cbranch_execz .LBB0_385
	s_lshl_b32 s2, s66, 1
	s_and_b32 s2, s2, 6
	s_or_b32 s2, s2, s8
	s_lshl_b32 s2, s2, 2
	s_or_b32 s2, s2, s64
	s_ashr_i32 s3, s2, 31
	s_lshl_b64 s[2:3], s[2:3], 16
	s_add_u32 s2, s88, s2
	s_addc_u32 s3, s89, s3
	s_waitcnt lgkmcnt(0)
	v_add_f32_e32 v12, v10, v11
	v_lshl_add_u64 v[10:11], v[142:143], 2, s[2:3]
	global_store_dword v[10:11], v12, off offset:704

; __device__ __forceinline__ float rq_sum(float v) { v += __shfl_xor(v, 16); v += __shfl_xor(v, 32); return v; }
; __device__ __forceinline__ float frsq(float x) { return __builtin_amdgcn_rsqf(x); }
; __device__ __forceinline__ void attn_wg_task(const Frame& F, int l, int task) {
;     ...
;     for (int qb = 0; qb < 2; ++qb) {
;         const int tq = tq0 + qb * 16;
;         const float inv = 1.0f / rq_sum(l_run[qb]);
;         float ss = 0.f;
; #pragma unroll
;         for (int db = 0; db < 8; ++db) { O[qb][db] *= inv; ss += (O[qb][db][0] * O[qb][db][0] + O[qb][db][1] * O[qb][db][1]) + (O[qb][db][2] * O[qb][db][2] + O[qb][db][3] * O[qb][db][3]); }
;         const float rstd = frsq(rq_sum(ss) * (1.f / HD) + EPS);
; #pragma unroll
;         for (int db = 0; db < 8; ++db) {
;             const int d0 = h * HD + db * 16 + rq * 4;
;             const f32x4 g4 = ld_f4(F.attn_g + l * 1024 + d0);
.LBB0_517:
	v_mov_b32_e32 v64, v151
	v_lshl_or_b32 v82, v204, 2, s17
	v_readlane_b32 s2, v251, 53
	v_readlane_b32 s3, v251, 54
	s_nop 1
	v_permlane16_swap_b32_e32 v64, v151
	s_waitcnt lgkmcnt(0)
	v_add_f32_e32 v64, v151, v64
	ds_bpermute_b32 v65, v203, v64
	s_barrier
	s_waitcnt lgkmcnt(0)
	v_lshlrev_b32_e32 v184, 1, v82
	v_readlane_b32 s4, v253, 59
	v_add_f32_e32 v64, v64, v65
	v_div_scale_f32 v65, s[0:1], v64, v64, 1.0
	v_rcp_f32_e32 v66, v65
	v_readlane_b32 s5, v253, 60
	v_fma_f32 v67, -v65, v66, 1.0
	v_fmac_f32_e32 v66, v67, v66
	v_div_scale_f32 v67, vcc, 1.0, v64, 1.0
	v_mul_f32_e32 v68, v67, v66
	v_fma_f32 v69, -v65, v68, v67
	v_fmac_f32_e32 v68, v69, v66
	v_fma_f32 v65, -v65, v68, v67
	v_div_fmas_f32 v65, v65, v66, v68
	v_div_fixup_f32 v84, v65, v64, 1.0
	v_pk_mul_f32 v[80:81], v[32:33], v[84:85] op_sel_hi:[1,0]
	v_pk_mul_f32 v[76:77], v[36:37], v[84:85] op_sel_hi:[1,0]
	v_pk_mul_f32 v[78:79], v[34:35], v[84:85] op_sel_hi:[1,0]
	v_pk_mul_f32 v[74:75], v[38:39], v[84:85] op_sel_hi:[1,0]
	v_mov_b32_e32 v34, v81
	v_mov_b32_e32 v35, v77
	v_mov_b32_e32 v32, v80
	v_mov_b32_e32 v33, v76
	v_pk_mul_f32 v[34:35], v[34:35], v[34:35]
	v_mov_b32_e32 v36, v79
	v_mov_b32_e32 v37, v75
	v_pk_fma_f32 v[32:33], v[32:33], v[32:33], v[34:35]
	v_mov_b32_e32 v34, v78
	v_mov_b32_e32 v35, v74
	v_pk_mul_f32 v[36:37], v[36:37], v[36:37]
	v_pk_mul_f32 v[72:73], v[40:41], v[84:85] op_sel_hi:[1,0]
	v_pk_fma_f32 v[34:35], v[34:35], v[34:35], v[36:37]
	v_pk_mul_f32 v[70:71], v[42:43], v[84:85] op_sel_hi:[1,0]
	v_pk_add_f32 v[32:33], v[32:33], v[34:35]
	v_pk_mul_f32 v[34:35], v[70:71], v[70:71]
	v_pk_add_f32 v[32:33], v[32:33], v[32:33] op_sel_hi:[0,1]
	v_pk_mul_f32 v[36:37], v[72:73], v[72:73]
	v_pk_mul_f32 v[68:69], v[44:45], v[84:85] op_sel_hi:[1,0]
	v_pk_mov_b32 v[38:39], v[36:37], v[34:35] op_sel:[1,0]
	v_mov_b32_e32 v37, v35
	v_pk_mul_f32 v[66:67], v[46:47], v[84:85] op_sel_hi:[1,0]
	v_mul_f32_e32 v32, v68, v68
	v_pk_add_f32 v[34:35], v[38:39], v[36:37]
	v_pk_fma_f32 v[36:37], v[68:69], v[68:69], v[32:33] op_sel_hi:[1,1,0]
	v_mul_f32_e32 v32, v66, v66
	v_pk_add_f32 v[34:35], v[34:35], v[34:35] op_sel_hi:[0,1]
	v_pk_fma_f32 v[38:39], v[66:67], v[66:67], v[32:33] op_sel_hi:[1,1,0]
	v_pk_mul_f32 v[50:51], v[50:51], v[84:85] op_sel_hi:[1,0]
	v_pk_mul_f32 v[64:65], v[48:49], v[84:85] op_sel_hi:[1,0]
	v_mul_f32_e32 v34, v50, v50
	v_mul_f32_e32 v36, v64, v64
	v_mul_f32_e32 v38, v65, v65
	v_mul_f32_e32 v32, v51, v51
	v_pk_add_f32 v[36:37], v[36:37], v[38:39]
	v_pk_add_f32 v[32:33], v[34:35], v[32:33]
	v_pk_mul_f32 v[48:49], v[52:53], v[84:85] op_sel_hi:[1,0]
	v_pk_add_f32 v[32:33], v[36:37], v[32:33]
	v_pk_mul_f32 v[46:47], v[54:55], v[84:85] op_sel_hi:[1,0]
	v_pk_add_f32 v[32:33], v[32:33], v[32:33] op_sel_hi:[0,1]
	v_pk_mul_f32 v[34:35], v[46:47], v[46:47]
	v_pk_mul_f32 v[36:37], v[48:49], v[48:49]
	v_pk_mul_f32 v[44:45], v[56:57], v[84:85] op_sel_hi:[1,0]
	v_pk_mov_b32 v[38:39], v[36:37], v[34:35] op_sel:[1,0]
	v_mov_b32_e32 v37, v35
	v_pk_mul_f32 v[42:43], v[58:59], v[84:85] op_sel_hi:[1,0]
	v_mul_f32_e32 v32, v44, v44
	v_pk_add_f32 v[34:35], v[38:39], v[36:37]
	v_pk_fma_f32 v[40:41], v[44:45], v[44:45], v[32:33] op_sel_hi:[1,1,0]
	v_mul_f32_e32 v32, v42, v42
	v_pk_add_f32 v[34:35], v[34:35], v[34:35] op_sel_hi:[0,1]
	v_pk_fma_f32 v[52:53], v[42:43], v[42:43], v[32:33] op_sel_hi:[1,1,0]
	v_pk_mul_f32 v[36:37], v[62:63], v[84:85] op_sel_hi:[1,0]
	v_pk_mul_f32 v[38:39], v[60:61], v[84:85] op_sel_hi:[1,0]
	v_mul_f32_e32 v34, v36, v36
	v_mul_f32_e32 v40, v38, v38
	v_mul_f32_e32 v52, v39, v39
	v_mul_f32_e32 v32, v37, v37
	v_pk_add_f32 v[40:41], v[40:41], v[52:53]
	v_pk_add_f32 v[32:33], v[34:35], v[32:33]
	v_lshlrev_b32_e32 v54, 2, v82
	global_load_dwordx4 v[96:99], v54, s[42:43]
	global_load_dwordx4 v[100:103], v54, s[42:43] offset:64
	global_load_dwordx4 v[104:107], v54, s[42:43] offset:128
	global_load_dwordx4 v[108:111], v54, s[42:43] offset:192
	global_load_dwordx4 v[112:115], v54, s[42:43] offset:256
	global_load_dwordx4 v[116:119], v54, s[42:43] offset:320
	global_load_dwordx4 v[120:123], v54, s[42:43] offset:384
	global_load_dwordx4 v[124:127], v54, s[42:43] offset:448
	v_pk_add_f32 v[32:33], v[40:41], v[32:33]
	v_mov_b32_e32 v56, v80
	v_add_f32_e32 v32, v32, v33
	v_mov_b32_e32 v33, v32
	v_mov_b32_e32 v57, v78
	v_mov_b32_e32 v78, v81
	s_nop 1
	v_permlane16_swap_b32_e32 v33, v32
	s_waitcnt lgkmcnt(0)
	v_add_f32_e32 v32, v32, v33
	v_mov_b32_e32 v33, v32
	s_nop 1
	v_permlane32_swap_b32_e32 v33, v32
	s_waitcnt lgkmcnt(0)
	v_add_f32_e32 v32, v32, v33
	v_fmamk_f32 v32, v32, 0x3c000000, v214
	v_rsq_f32_e32 v40, v32
	v_lshlrev_b64 v[32:33], 12, v[152:153]
	v_lshl_add_u64 v[52:53], s[2:3], 0, v[32:33]
	s_waitcnt vmcnt(0)
; __device__ __forceinline__ unsigned pk2(float lo, float hi) { return f2bf(lo) | (f2bf(hi) << 16); }
; __device__ __forceinline__ void attn_wg_task(const Frame& F, int l, int task) {
;     ...
; #pragma unroll
;         for (int db = 0; db < 8; ++db) {
;             const int d0 = h * HD + db * 16 + rq * 4;
;             const f32x4 g4 = ld_f4(F.attn_g + l * 1024 + d0);
;             u32x2 o; o.x = pk2(O[qb][db][0] * rstd * g4[0], O[qb][db][1] * rstd * g4[1]); o.y = pk2(O[qb][db][2] * rstd * g4[2], O[qb][db][3] * rstd * g4[3]);
;             st_u2(MIX + (size_t)tq * D + d0, o);
;         }
	v_mov_b32_e32 v32, v96
	v_mov_b32_e32 v33, v97
	v_mov_b32_e32 v34, v98
	v_mov_b32_e32 v35, v99
	v_pk_mul_f32 v[56:57], v[56:57], v[40:41] op_sel_hi:[1,0]
	v_mov_b32_e32 v58, v32
	v_mov_b32_e32 v59, v34
	v_pk_mul_f32 v[56:57], v[58:59], v[56:57]
	v_pk_mul_f32 v[58:59], v[78:79], v[40:41] op_sel_hi:[1,0]
	v_mov_b32_e32 v34, v33
	v_pk_mul_f32 v[32:33], v[34:35], v[58:59]
	v_and_b32_sdwa v35, v56, v213 dst_sel:DWORD dst_unused:UNUSED_PAD src0_sel:WORD_1 src1_sel:DWORD
	v_add3_u32 v41, v56, v35, s76
	v_and_b32_sdwa v35, v33, v213 dst_sel:DWORD dst_unused:UNUSED_PAD src0_sel:WORD_1 src1_sel:DWORD
	v_and_b32_sdwa v55, v32, v213 dst_sel:DWORD dst_unused:UNUSED_PAD src0_sel:WORD_1 src1_sel:DWORD
	v_and_b32_sdwa v34, v57, v213 dst_sel:DWORD dst_unused:UNUSED_PAD src0_sel:WORD_1 src1_sel:DWORD
	v_add3_u32 v33, v33, v35, s76
	v_add3_u32 v32, v32, v55, s76
	v_add3_u32 v34, v57, v34, s76
	v_and_b32_e32 v33, 0xffff0000, v33
	v_and_b32_e32 v32, 0xffff0000, v32
	v_or_b32_sdwa v35, v33, v34 dst_sel:DWORD dst_unused:UNUSED_PAD src0_sel:DWORD src1_sel:WORD_1
	v_or_b32_sdwa v34, v32, v41 dst_sel:DWORD dst_unused:UNUSED_PAD src0_sel:DWORD src1_sel:WORD_1
	v_lshl_add_u64 v[32:33], v[52:53], 0, v[184:185]
	global_store_dwordx2 v[32:33], v[34:35], off
	v_mov_b32_e32 v56, v100
	v_mov_b32_e32 v57, v101
	v_mov_b32_e32 v58, v102
	v_mov_b32_e32 v59, v103
	v_mov_b32_e32 v34, v76
	v_mov_b32_e32 v35, v74
	v_pk_mul_f32 v[34:35], v[34:35], v[40:41] op_sel_hi:[1,0]
	v_mov_b32_e32 v74, v77
	v_mov_b32_e32 v52, v56
	v_mov_b32_e32 v53, v58
	v_pk_mul_f32 v[34:35], v[52:53], v[34:35]
	v_pk_mul_f32 v[52:53], v[74:75], v[40:41] op_sel_hi:[1,0]
	v_mov_b32_e32 v58, v57
	v_pk_mul_f32 v[52:53], v[58:59], v[52:53]
	v_and_b32_sdwa v41, v35, v213 dst_sel:DWORD dst_unused:UNUSED_PAD src0_sel:WORD_1 src1_sel:DWORD
	v_and_b32_sdwa v55, v34, v213 dst_sel:DWORD dst_unused:UNUSED_PAD src0_sel:WORD_1 src1_sel:DWORD
	v_add3_u32 v34, v34, v55, s76
	v_add3_u32 v35, v35, v41, s76
	v_and_b32_sdwa v41, v53, v213 dst_sel:DWORD dst_unused:UNUSED_PAD src0_sel:WORD_1 src1_sel:DWORD
	v_and_b32_sdwa v55, v52, v213 dst_sel:DWORD dst_unused:UNUSED_PAD src0_sel:WORD_1 src1_sel:DWORD
	v_add3_u32 v41, v53, v41, s76
	v_add3_u32 v52, v52, v55, s76
	v_and_b32_e32 v41, 0xffff0000, v41
	v_and_b32_e32 v52, 0xffff0000, v52
	v_or_b32_sdwa v35, v41, v35 dst_sel:DWORD dst_unused:UNUSED_PAD src0_sel:DWORD src1_sel:WORD_1
	v_or_b32_sdwa v34, v52, v34 dst_sel:DWORD dst_unused:UNUSED_PAD src0_sel:DWORD src1_sel:WORD_1
	global_store_dwordx2 v[32:33], v[34:35], off offset:32
	v_mov_b32_e32 v56, v104
	v_mov_b32_e32 v57, v105
	v_mov_b32_e32 v58, v106
	v_mov_b32_e32 v59, v107
	v_mov_b32_e32 v34, v72
	v_mov_b32_e32 v35, v70
	v_pk_mul_f32 v[34:35], v[34:35], v[40:41] op_sel_hi:[1,0]
	v_mov_b32_e32 v70, v73
	v_mov_b32_e32 v52, v56
	v_mov_b32_e32 v53, v58
	v_pk_mul_f32 v[34:35], v[52:53], v[34:35]
	v_pk_mul_f32 v[52:53], v[70:71], v[40:41] op_sel_hi:[1,0]
	v_mov_b32_e32 v58, v57
	v_pk_mul_f32 v[52:53], v[58:59], v[52:53]
	v_and_b32_sdwa v41, v35, v213 dst_sel:DWORD dst_unused:UNUSED_PAD src0_sel:WORD_1 src1_sel:DWORD
	v_and_b32_sdwa v55, v34, v213 dst_sel:DWORD dst_unused:UNUSED_PAD src0_sel:WORD_1 src1_sel:DWORD
	v_add3_u32 v34, v34, v55, s76
	v_add3_u32 v35, v35, v41, s76
	v_and_b32_sdwa v41, v53, v213 dst_sel:DWORD dst_unused:UNUSED_PAD src0_sel:WORD_1 src1_sel:DWORD
	v_and_b32_sdwa v55, v52, v213 dst_sel:DWORD dst_unused:UNUSED_PAD src0_sel:WORD_1 src1_sel:DWORD
	v_add3_u32 v41, v53, v41, s76
	v_add3_u32 v52, v52, v55, s76
	v_and_b32_e32 v41, 0xffff0000, v41
	v_and_b32_e32 v52, 0xffff0000, v52
	v_or_b32_sdwa v35, v41, v35 dst_sel:DWORD dst_unused:UNUSED_PAD src0_sel:DWORD src1_sel:WORD_1
	v_or_b32_sdwa v34, v52, v34 dst_sel:DWORD dst_unused:UNUSED_PAD src0_sel:DWORD src1_sel:WORD_1
	global_store_dwordx2 v[32:33], v[34:35], off offset:64
	v_mov_b32_e32 v56, v108
	v_mov_b32_e32 v57, v109
	v_mov_b32_e32 v58, v110
	v_mov_b32_e32 v59, v111
	v_mov_b32_e32 v34, v68
	v_mov_b32_e32 v35, v66
	v_pk_mul_f32 v[34:35], v[34:35], v[40:41] op_sel_hi:[1,0]
	v_mov_b32_e32 v66, v69
	v_mov_b32_e32 v52, v56
	v_mov_b32_e32 v53, v58
	v_pk_mul_f32 v[34:35], v[52:53], v[34:35]
	v_pk_mul_f32 v[52:53], v[66:67], v[40:41] op_sel_hi:[1,0]
	v_mov_b32_e32 v58, v57
	v_pk_mul_f32 v[52:53], v[58:59], v[52:53]
	v_and_b32_sdwa v41, v35, v213 dst_sel:DWORD dst_unused:UNUSED_PAD src0_sel:WORD_1 src1_sel:DWORD
	v_and_b32_sdwa v55, v34, v213 dst_sel:DWORD dst_unused:UNUSED_PAD src0_sel:WORD_1 src1_sel:DWORD
	v_add3_u32 v34, v34, v55, s76
	v_add3_u32 v35, v35, v41, s76
	v_and_b32_sdwa v41, v53, v213 dst_sel:DWORD dst_unused:UNUSED_PAD src0_sel:WORD_1 src1_sel:DWORD
	v_and_b32_sdwa v55, v52, v213 dst_sel:DWORD dst_unused:UNUSED_PAD src0_sel:WORD_1 src1_sel:DWORD
	v_add3_u32 v41, v53, v41, s76
	v_add3_u32 v52, v52, v55, s76
	v_and_b32_e32 v41, 0xffff0000, v41
	v_and_b32_e32 v52, 0xffff0000, v52
	v_or_b32_sdwa v35, v41, v35 dst_sel:DWORD dst_unused:UNUSED_PAD src0_sel:DWORD src1_sel:WORD_1
	v_or_b32_sdwa v34, v52, v34 dst_sel:DWORD dst_unused:UNUSED_PAD src0_sel:DWORD src1_sel:WORD_1
	global_store_dwordx2 v[32:33], v[34:35], off offset:96
	v_mov_b32_e32 v56, v112
	v_mov_b32_e32 v57, v113
	v_mov_b32_e32 v58, v114
	v_mov_b32_e32 v59, v115
	v_mov_b32_e32 v34, v64
	v_mov_b32_e32 v35, v50
	v_pk_mul_f32 v[34:35], v[34:35], v[40:41] op_sel_hi:[1,0]
	v_mov_b32_e32 v50, v65
	v_pk_mul_f32 v[50:51], v[50:51], v[40:41] op_sel_hi:[1,0]
	v_mov_b32_e32 v52, v56
	v_mov_b32_e32 v53, v58
	v_pk_mul_f32 v[34:35], v[52:53], v[34:35]
	v_mov_b32_e32 v58, v57
	v_pk_mul_f32 v[50:51], v[58:59], v[50:51]
	v_and_b32_sdwa v41, v35, v213 dst_sel:DWORD dst_unused:UNUSED_PAD src0_sel:WORD_1 src1_sel:DWORD
; __device__ __forceinline__ unsigned pk2(float lo, float hi) { return f2bf(lo) | (f2bf(hi) << 16); }
; __device__ __forceinline__ float rq_sum(float v) { v += __shfl_xor(v, 16); v += __shfl_xor(v, 32); return v; }
; __device__ __forceinline__ float frsq(float x) { return __builtin_amdgcn_rsqf(x); }
; __device__ __forceinline__ void attn_wg_task(const Frame& F, int l, int task) {
;     ...
;     for (int qb = 0; qb < 2; ++qb) {
;         const int tq = tq0 + qb * 16;
;         const float inv = 1.0f / rq_sum(l_run[qb]);
;         float ss = 0.f;
; #pragma unroll
;         for (int db = 0; db < 8; ++db) { O[qb][db] *= inv; ss += (O[qb][db][0] * O[qb][db][0] + O[qb][db][1] * O[qb][db][1]) + (O[qb][db][2] * O[qb][db][2] + O[qb][db][3] * O[qb][db][3]); }
;         const float rstd = frsq(rq_sum(ss) * (1.f / HD) + EPS);
; #pragma unroll
;         for (int db = 0; db < 8; ++db) {
;             const int d0 = h * HD + db * 16 + rq * 4;
;             const f32x4 g4 = ld_f4(F.attn_g + l * 1024 + d0);
;             u32x2 o; o.x = pk2(O[qb][db][0] * rstd * g4[0], O[qb][db][1] * rstd * g4[1]); o.y = pk2(O[qb][db][2] * rstd * g4[2], O[qb][db][3] * rstd * g4[3]);
;             st_u2(MIX + (size_t)tq * D + d0, o);
;         }
	v_and_b32_sdwa v52, v34, v213 dst_sel:DWORD dst_unused:UNUSED_PAD src0_sel:WORD_1 src1_sel:DWORD
	v_add3_u32 v34, v34, v52, s76
	v_add3_u32 v35, v35, v41, s76
	v_and_b32_sdwa v41, v51, v213 dst_sel:DWORD dst_unused:UNUSED_PAD src0_sel:WORD_1 src1_sel:DWORD
	v_and_b32_sdwa v52, v50, v213 dst_sel:DWORD dst_unused:UNUSED_PAD src0_sel:WORD_1 src1_sel:DWORD
	v_add3_u32 v41, v51, v41, s76
	v_add3_u32 v50, v50, v52, s76
	v_and_b32_e32 v41, 0xffff0000, v41
	v_and_b32_e32 v50, 0xffff0000, v50
	v_or_b32_sdwa v35, v41, v35 dst_sel:DWORD dst_unused:UNUSED_PAD src0_sel:DWORD src1_sel:WORD_1
	v_or_b32_sdwa v34, v50, v34 dst_sel:DWORD dst_unused:UNUSED_PAD src0_sel:DWORD src1_sel:WORD_1
	global_store_dwordx2 v[32:33], v[34:35], off offset:128
	v_mov_b32_e32 v50, v116
	v_mov_b32_e32 v51, v117
	v_mov_b32_e32 v52, v118
	v_mov_b32_e32 v53, v119
	v_mov_b32_e32 v34, v48
	v_mov_b32_e32 v35, v46
	v_pk_mul_f32 v[34:35], v[34:35], v[40:41] op_sel_hi:[1,0]
	v_mov_b32_e32 v46, v49
	v_pk_mul_f32 v[46:47], v[46:47], v[40:41] op_sel_hi:[1,0]
	v_mov_b32_e32 v56, v50
	v_mov_b32_e32 v57, v52
	v_pk_mul_f32 v[34:35], v[56:57], v[34:35]
	v_mov_b32_e32 v52, v51
	v_pk_mul_f32 v[46:47], v[52:53], v[46:47]
	v_and_b32_sdwa v41, v35, v213 dst_sel:DWORD dst_unused:UNUSED_PAD src0_sel:WORD_1 src1_sel:DWORD
	v_and_b32_sdwa v48, v34, v213 dst_sel:DWORD dst_unused:UNUSED_PAD src0_sel:WORD_1 src1_sel:DWORD
	v_add3_u32 v34, v34, v48, s76
	v_add3_u32 v35, v35, v41, s76
	v_and_b32_sdwa v41, v47, v213 dst_sel:DWORD dst_unused:UNUSED_PAD src0_sel:WORD_1 src1_sel:DWORD
	v_and_b32_sdwa v48, v46, v213 dst_sel:DWORD dst_unused:UNUSED_PAD src0_sel:WORD_1 src1_sel:DWORD
	v_add3_u32 v41, v47, v41, s76
	v_add3_u32 v46, v46, v48, s76
	v_and_b32_e32 v41, 0xffff0000, v41
	v_and_b32_e32 v46, 0xffff0000, v46
	v_or_b32_sdwa v35, v41, v35 dst_sel:DWORD dst_unused:UNUSED_PAD src0_sel:DWORD src1_sel:WORD_1
	v_or_b32_sdwa v34, v46, v34 dst_sel:DWORD dst_unused:UNUSED_PAD src0_sel:DWORD src1_sel:WORD_1
	global_store_dwordx2 v[32:33], v[34:35], off offset:160
	v_mov_b32_e32 v46, v120
	v_mov_b32_e32 v47, v121
	v_mov_b32_e32 v48, v122
	v_mov_b32_e32 v49, v123
	v_mov_b32_e32 v34, v44
	v_mov_b32_e32 v35, v42
	v_pk_mul_f32 v[34:35], v[34:35], v[40:41] op_sel_hi:[1,0]
	v_mov_b32_e32 v42, v45
	v_pk_mul_f32 v[42:43], v[42:43], v[40:41] op_sel_hi:[1,0]
	v_mov_b32_e32 v50, v46
	v_mov_b32_e32 v51, v48
	v_pk_mul_f32 v[34:35], v[50:51], v[34:35]
	v_mov_b32_e32 v48, v47
	v_pk_mul_f32 v[42:43], v[48:49], v[42:43]
	v_and_b32_sdwa v41, v35, v213 dst_sel:DWORD dst_unused:UNUSED_PAD src0_sel:WORD_1 src1_sel:DWORD
	v_and_b32_sdwa v44, v34, v213 dst_sel:DWORD dst_unused:UNUSED_PAD src0_sel:WORD_1 src1_sel:DWORD
	v_add3_u32 v34, v34, v44, s76
	v_add3_u32 v35, v35, v41, s76
	v_and_b32_sdwa v41, v43, v213 dst_sel:DWORD dst_unused:UNUSED_PAD src0_sel:WORD_1 src1_sel:DWORD
	v_and_b32_sdwa v44, v42, v213 dst_sel:DWORD dst_unused:UNUSED_PAD src0_sel:WORD_1 src1_sel:DWORD
	v_add3_u32 v41, v43, v41, s76
	v_add3_u32 v42, v42, v44, s76
	v_and_b32_e32 v41, 0xffff0000, v41
	v_and_b32_e32 v42, 0xffff0000, v42
	v_or_b32_sdwa v35, v41, v35 dst_sel:DWORD dst_unused:UNUSED_PAD src0_sel:DWORD src1_sel:WORD_1
	v_or_b32_sdwa v34, v42, v34 dst_sel:DWORD dst_unused:UNUSED_PAD src0_sel:DWORD src1_sel:WORD_1
	global_store_dwordx2 v[32:33], v[34:35], off offset:192
	v_mov_b32_e32 v42, v124
	v_mov_b32_e32 v43, v125
	v_mov_b32_e32 v44, v126
	v_mov_b32_e32 v45, v127
	v_mov_b32_e32 v34, v38
	v_mov_b32_e32 v35, v36
	v_pk_mul_f32 v[34:35], v[34:35], v[40:41] op_sel_hi:[1,0]
	v_mov_b32_e32 v36, v39
	v_pk_mul_f32 v[36:37], v[36:37], v[40:41] op_sel_hi:[1,0]
	v_mov_b32_e32 v46, v42
	v_mov_b32_e32 v47, v44
	v_pk_mul_f32 v[34:35], v[46:47], v[34:35]
	v_mov_b32_e32 v44, v43
	v_pk_mul_f32 v[36:37], v[44:45], v[36:37]
	v_and_b32_sdwa v38, v35, v213 dst_sel:DWORD dst_unused:UNUSED_PAD src0_sel:WORD_1 src1_sel:DWORD
	v_and_b32_sdwa v39, v34, v213 dst_sel:DWORD dst_unused:UNUSED_PAD src0_sel:WORD_1 src1_sel:DWORD
	v_add3_u32 v34, v34, v39, s76
	v_add3_u32 v35, v35, v38, s76
	v_and_b32_sdwa v38, v37, v213 dst_sel:DWORD dst_unused:UNUSED_PAD src0_sel:WORD_1 src1_sel:DWORD
	v_and_b32_sdwa v39, v36, v213 dst_sel:DWORD dst_unused:UNUSED_PAD src0_sel:WORD_1 src1_sel:DWORD
	v_add3_u32 v37, v37, v38, s76
	v_add3_u32 v36, v36, v39, s76
	v_and_b32_e32 v37, 0xffff0000, v37
	v_and_b32_e32 v36, 0xffff0000, v36
	v_or_b32_sdwa v35, v37, v35 dst_sel:DWORD dst_unused:UNUSED_PAD src0_sel:DWORD src1_sel:WORD_1
	v_or_b32_sdwa v34, v36, v34 dst_sel:DWORD dst_unused:UNUSED_PAD src0_sel:DWORD src1_sel:WORD_1
	global_store_dwordx2 v[32:33], v[34:35], off offset:224
	v_mov_b32_e32 v32, v150
	s_nop 1
	v_permlane16_swap_b32_e32 v32, v150
	s_waitcnt lgkmcnt(0)
	v_add_f32_e32 v32, v150, v32
	v_mov_b32_e32 v33, v32
	s_nop 1
	v_permlane32_swap_b32_e32 v33, v32
	s_waitcnt lgkmcnt(0)
; __device__ __forceinline__ unsigned pk2(float lo, float hi) { return f2bf(lo) | (f2bf(hi) << 16); }
; __device__ __forceinline__ float rq_sum(float v) { v += __shfl_xor(v, 16); v += __shfl_xor(v, 32); return v; }
; __device__ __forceinline__ float frsq(float x) { return __builtin_amdgcn_rsqf(x); }
; __device__ __forceinline__ void attn_wg_task(const Frame& F, int l, int task) {
;     ...
;         const float inv = 1.0f / rq_sum(l_run[qb]);
;         float ss = 0.f;
; #pragma unroll
;         for (int db = 0; db < 8; ++db) { O[qb][db] *= inv; ss += (O[qb][db][0] * O[qb][db][0] + O[qb][db][1] * O[qb][db][1]) + (O[qb][db][2] * O[qb][db][2] + O[qb][db][3] * O[qb][db][3]); }
;         const float rstd = frsq(rq_sum(ss) * (1.f / HD) + EPS);
; #pragma unroll
;         for (int db = 0; db < 8; ++db) {
;             const int d0 = h * HD + db * 16 + rq * 4;
;             const f32x4 g4 = ld_f4(F.attn_g + l * 1024 + d0);
;             u32x2 o; o.x = pk2(O[qb][db][0] * rstd * g4[0], O[qb][db][1] * rstd * g4[1]); o.y = pk2(O[qb][db][2] * rstd * g4[2], O[qb][db][3] * rstd * g4[3]);
;             st_u2(MIX + (size_t)tq * D + d0, o);
;         }
	v_add_f32_e32 v32, v32, v33
	v_div_scale_f32 v33, s[0:1], v32, v32, 1.0
	v_rcp_f32_e32 v34, v33
	s_nop 0
	v_fma_f32 v35, -v33, v34, 1.0
	v_fmac_f32_e32 v34, v35, v34
	v_div_scale_f32 v35, vcc, 1.0, v32, 1.0
	v_mul_f32_e32 v36, v35, v34
	v_fma_f32 v37, -v33, v36, v35
	v_fmac_f32_e32 v36, v37, v34
	v_fma_f32 v33, -v33, v36, v35
	v_div_fmas_f32 v33, v33, v34, v36
	v_div_fixup_f32 v48, v33, v32, 1.0
	v_pk_mul_f32 v[46:47], v[4:5], v[48:49] op_sel_hi:[1,0]
	v_pk_mul_f32 v[42:43], v[8:9], v[48:49] op_sel_hi:[1,0]
	v_pk_mul_f32 v[44:45], v[6:7], v[48:49] op_sel_hi:[1,0]
	v_pk_mul_f32 v[36:37], v[10:11], v[48:49] op_sel_hi:[1,0]
	v_mov_b32_e32 v6, v47
	v_mov_b32_e32 v7, v43
	v_mov_b32_e32 v4, v46
	v_mov_b32_e32 v5, v42
	v_pk_mul_f32 v[6:7], v[6:7], v[6:7]
	v_mov_b32_e32 v8, v45
	v_mov_b32_e32 v9, v37
	v_pk_fma_f32 v[4:5], v[4:5], v[4:5], v[6:7]
	v_mov_b32_e32 v6, v44
	v_mov_b32_e32 v7, v36
	v_pk_mul_f32 v[8:9], v[8:9], v[8:9]
	v_pk_mul_f32 v[40:41], v[0:1], v[48:49] op_sel_hi:[1,0]
	v_pk_mul_f32 v[38:39], v[2:3], v[48:49] op_sel_hi:[1,0]
	v_pk_fma_f32 v[6:7], v[6:7], v[6:7], v[8:9]
	v_pk_mul_f32 v[0:1], v[38:39], v[38:39]
	v_pk_mul_f32 v[2:3], v[40:41], v[40:41]
	v_pk_add_f32 v[4:5], v[4:5], v[6:7]
	v_pk_mov_b32 v[6:7], v[2:3], v[0:1] op_sel:[1,0]
	v_mov_b32_e32 v3, v1
	v_pk_add_f32 v[0:1], v[6:7], v[2:3]
	v_pk_mul_f32 v[34:35], v[12:13], v[48:49] op_sel_hi:[1,0]
	v_pk_add_f32 v[0:1], v[0:1], v[0:1] op_sel_hi:[0,1]
	v_pk_mul_f32 v[32:33], v[14:15], v[48:49] op_sel_hi:[1,0]
	v_mul_f32_e32 v0, v34, v34
	v_pk_fma_f32 v[2:3], v[34:35], v[34:35], v[0:1] op_sel_hi:[1,1,0]
	v_mul_f32_e32 v0, v32, v32
	v_pk_add_f32 v[4:5], v[4:5], v[4:5] op_sel_hi:[0,1]
	v_pk_fma_f32 v[6:7], v[32:33], v[32:33], v[0:1] op_sel_hi:[1,1,0]
	v_pk_mul_f32 v[14:15], v[18:19], v[48:49] op_sel_hi:[1,0]
	v_pk_mul_f32 v[16:17], v[16:17], v[48:49] op_sel_hi:[1,0]
	v_mul_f32_e32 v0, v14, v14
	v_mul_f32_e32 v2, v16, v16
	v_mul_f32_e32 v6, v17, v17
	v_mul_f32_e32 v4, v15, v15
	v_pk_add_f32 v[2:3], v[2:3], v[6:7]
	v_pk_add_f32 v[0:1], v[0:1], v[4:5]
	v_pk_mul_f32 v[12:13], v[20:21], v[48:49] op_sel_hi:[1,0]
	v_pk_add_f32 v[0:1], v[2:3], v[0:1]
	v_pk_mul_f32 v[10:11], v[22:23], v[48:49] op_sel_hi:[1,0]
	v_pk_add_f32 v[4:5], v[0:1], v[0:1] op_sel_hi:[0,1]
	v_pk_mul_f32 v[0:1], v[10:11], v[10:11]
	v_pk_mul_f32 v[2:3], v[12:13], v[12:13]
	v_pk_mul_f32 v[8:9], v[24:25], v[48:49] op_sel_hi:[1,0]
	v_pk_mov_b32 v[6:7], v[2:3], v[0:1] op_sel:[1,0]
	v_mov_b32_e32 v3, v1
	v_pk_add_f32 v[0:1], v[6:7], v[2:3]
	v_pk_mul_f32 v[6:7], v[26:27], v[48:49] op_sel_hi:[1,0]
	v_pk_add_f32 v[18:19], v[0:1], v[0:1] op_sel_hi:[0,1]
	v_mul_f32_e32 v0, v8, v8
	v_pk_fma_f32 v[20:21], v[8:9], v[8:9], v[0:1] op_sel_hi:[1,1,0]
	v_mul_f32_e32 v0, v6, v6
	v_pk_fma_f32 v[22:23], v[6:7], v[6:7], v[0:1] op_sel_hi:[1,1,0]
	v_pk_mul_f32 v[0:1], v[30:31], v[48:49] op_sel_hi:[1,0]
	v_pk_mul_f32 v[2:3], v[28:29], v[48:49] op_sel_hi:[1,0]
	v_mul_f32_e32 v18, v0, v0
	v_mul_f32_e32 v20, v2, v2
	v_mul_f32_e32 v22, v3, v3
	v_mul_f32_e32 v4, v1, v1
	v_pk_add_f32 v[20:21], v[20:21], v[22:23]
	v_pk_add_f32 v[4:5], v[18:19], v[4:5]
	v_mov_b32_e32 v24, v46
	v_pk_add_f32 v[4:5], v[20:21], v[4:5]
	v_mov_b32_e32 v20, v96
	v_mov_b32_e32 v21, v97
	v_mov_b32_e32 v22, v98
	v_mov_b32_e32 v23, v99
	v_add_f32_e32 v4, v4, v5
	v_mov_b32_e32 v5, v4
	v_mov_b32_e32 v25, v44
	v_mov_b32_e32 v44, v47
	v_lshlrev_b64 v[18:19], 12, v[148:149]
	v_lshl_add_u64 v[18:19], s[2:3], 0, v[18:19]
	s_nop 1
	v_permlane16_swap_b32_e32 v5, v4
	s_waitcnt lgkmcnt(0)
	v_add_f32_e32 v4, v4, v5
	v_mov_b32_e32 v5, v4
	v_lshl_add_u64 v[18:19], v[18:19], 0, v[184:185]
	s_add_i32 s2, s16, 1
	s_cmp_lt_u32 s16, 2
	s_cselect_b64 s[0:1], -1, 0
	s_nop 1
	v_permlane32_swap_b32_e32 v5, v4
	s_waitcnt lgkmcnt(0)
	v_add_f32_e32 v4, v4, v5
	v_fmamk_f32 v4, v4, 0x3c000000, v214
	v_rsq_f32_e32 v4, v4
	s_and_b64 s[0:1], s[4:5], s[0:1]
	s_andn2_b64 vcc, exec, s[0:1]
	s_mov_b32 s16, s2
	v_pk_mul_f32 v[24:25], v[24:25], v[4:5] op_sel_hi:[1,0]
	v_mov_b32_e32 v26, v20
	v_mov_b32_e32 v27, v22
	v_pk_mul_f32 v[24:25], v[26:27], v[24:25]
	v_pk_mul_f32 v[26:27], v[44:45], v[4:5] op_sel_hi:[1,0]
	v_mov_b32_e32 v22, v21
	v_pk_mul_f32 v[20:21], v[22:23], v[26:27]
	v_and_b32_sdwa v22, v24, v213 dst_sel:DWORD dst_unused:UNUSED_PAD src0_sel:WORD_1 src1_sel:DWORD
	v_add3_u32 v22, v24, v22, s76
	v_and_b32_sdwa v23, v21, v213 dst_sel:DWORD dst_unused:UNUSED_PAD src0_sel:WORD_1 src1_sel:DWORD
	v_and_b32_sdwa v24, v20, v213 dst_sel:DWORD dst_unused:UNUSED_PAD src0_sel:WORD_1 src1_sel:DWORD
	v_and_b32_sdwa v5, v25, v213 dst_sel:DWORD dst_unused:UNUSED_PAD src0_sel:WORD_1 src1_sel:DWORD
	v_add3_u32 v21, v21, v23, s76
	v_add3_u32 v20, v20, v24, s76
	v_add3_u32 v5, v25, v5, s76
	v_and_b32_e32 v21, 0xffff0000, v21
	v_and_b32_e32 v20, 0xffff0000, v20
	v_or_b32_sdwa v21, v21, v5 dst_sel:DWORD dst_unused:UNUSED_PAD src0_sel:DWORD src1_sel:WORD_1
	v_or_b32_sdwa v20, v20, v22 dst_sel:DWORD dst_unused:UNUSED_PAD src0_sel:DWORD src1_sel:WORD_1
	global_store_dwordx2 v[18:19], v[20:21], off
	v_mov_b32_e32 v20, v100
	v_mov_b32_e32 v21, v101
	v_mov_b32_e32 v22, v102
	v_mov_b32_e32 v23, v103
	v_mov_b32_e32 v24, v42
	v_mov_b32_e32 v25, v36
	v_pk_mul_f32 v[24:25], v[24:25], v[4:5] op_sel_hi:[1,0]
	v_mov_b32_e32 v36, v43
	v_mov_b32_e32 v26, v20
	v_mov_b32_e32 v27, v22
	v_pk_mul_f32 v[24:25], v[26:27], v[24:25]
	v_pk_mul_f32 v[26:27], v[36:37], v[4:5] op_sel_hi:[1,0]
	v_mov_b32_e32 v22, v21
	v_pk_mul_f32 v[20:21], v[22:23], v[26:27]
	v_and_b32_sdwa v22, v24, v213 dst_sel:DWORD dst_unused:UNUSED_PAD src0_sel:WORD_1 src1_sel:DWORD
	v_add3_u32 v22, v24, v22, s76
	v_and_b32_sdwa v23, v21, v213 dst_sel:DWORD dst_unused:UNUSED_PAD src0_sel:WORD_1 src1_sel:DWORD
; __device__ __forceinline__ unsigned pk2(float lo, float hi) { return f2bf(lo) | (f2bf(hi) << 16); }
; __device__ __forceinline__ void attn_wg_task(const Frame& F, int l, int task) {
;     ...
; #pragma unroll
;         for (int db = 0; db < 8; ++db) {
;             const int d0 = h * HD + db * 16 + rq * 4;
;             const f32x4 g4 = ld_f4(F.attn_g + l * 1024 + d0);
;             u32x2 o; o.x = pk2(O[qb][db][0] * rstd * g4[0], O[qb][db][1] * rstd * g4[1]); o.y = pk2(O[qb][db][2] * rstd * g4[2], O[qb][db][3] * rstd * g4[3]);
;             st_u2(MIX + (size_t)tq * D + d0, o);
;         }
	v_and_b32_sdwa v24, v20, v213 dst_sel:DWORD dst_unused:UNUSED_PAD src0_sel:WORD_1 src1_sel:DWORD
	v_and_b32_sdwa v5, v25, v213 dst_sel:DWORD dst_unused:UNUSED_PAD src0_sel:WORD_1 src1_sel:DWORD
	v_add3_u32 v21, v21, v23, s76
	v_add3_u32 v20, v20, v24, s76
	v_add3_u32 v5, v25, v5, s76
	v_and_b32_e32 v21, 0xffff0000, v21
	v_and_b32_e32 v20, 0xffff0000, v20
	v_or_b32_sdwa v21, v21, v5 dst_sel:DWORD dst_unused:UNUSED_PAD src0_sel:DWORD src1_sel:WORD_1
	v_or_b32_sdwa v20, v20, v22 dst_sel:DWORD dst_unused:UNUSED_PAD src0_sel:DWORD src1_sel:WORD_1
	global_store_dwordx2 v[18:19], v[20:21], off offset:32
	v_mov_b32_e32 v20, v104
	v_mov_b32_e32 v21, v105
	v_mov_b32_e32 v22, v106
	v_mov_b32_e32 v23, v107
	v_mov_b32_e32 v24, v40
	v_mov_b32_e32 v25, v38
	v_pk_mul_f32 v[24:25], v[24:25], v[4:5] op_sel_hi:[1,0]
	v_mov_b32_e32 v38, v41
	v_mov_b32_e32 v26, v20
	v_mov_b32_e32 v27, v22
	v_pk_mul_f32 v[24:25], v[26:27], v[24:25]
	v_pk_mul_f32 v[26:27], v[38:39], v[4:5] op_sel_hi:[1,0]
	v_mov_b32_e32 v22, v21
	v_pk_mul_f32 v[20:21], v[22:23], v[26:27]
	v_and_b32_sdwa v22, v24, v213 dst_sel:DWORD dst_unused:UNUSED_PAD src0_sel:WORD_1 src1_sel:DWORD
	v_add3_u32 v22, v24, v22, s76
	v_and_b32_sdwa v23, v21, v213 dst_sel:DWORD dst_unused:UNUSED_PAD src0_sel:WORD_1 src1_sel:DWORD
	v_and_b32_sdwa v24, v20, v213 dst_sel:DWORD dst_unused:UNUSED_PAD src0_sel:WORD_1 src1_sel:DWORD
	v_and_b32_sdwa v5, v25, v213 dst_sel:DWORD dst_unused:UNUSED_PAD src0_sel:WORD_1 src1_sel:DWORD
	v_add3_u32 v21, v21, v23, s76
	v_add3_u32 v20, v20, v24, s76
	v_add3_u32 v5, v25, v5, s76
	v_and_b32_e32 v21, 0xffff0000, v21
	v_and_b32_e32 v20, 0xffff0000, v20
	v_or_b32_sdwa v21, v21, v5 dst_sel:DWORD dst_unused:UNUSED_PAD src0_sel:DWORD src1_sel:WORD_1
	v_or_b32_sdwa v20, v20, v22 dst_sel:DWORD dst_unused:UNUSED_PAD src0_sel:DWORD src1_sel:WORD_1
	global_store_dwordx2 v[18:19], v[20:21], off offset:64
	v_mov_b32_e32 v20, v108
	v_mov_b32_e32 v21, v109
	v_mov_b32_e32 v22, v110
	v_mov_b32_e32 v23, v111
	v_mov_b32_e32 v24, v34
	v_mov_b32_e32 v25, v32
	v_pk_mul_f32 v[24:25], v[24:25], v[4:5] op_sel_hi:[1,0]
	v_mov_b32_e32 v32, v35
	v_mov_b32_e32 v26, v20
	v_mov_b32_e32 v27, v22
	v_pk_mul_f32 v[24:25], v[26:27], v[24:25]
	v_pk_mul_f32 v[26:27], v[32:33], v[4:5] op_sel_hi:[1,0]
	v_mov_b32_e32 v22, v21
	v_pk_mul_f32 v[20:21], v[22:23], v[26:27]
	v_and_b32_sdwa v22, v24, v213 dst_sel:DWORD dst_unused:UNUSED_PAD src0_sel:WORD_1 src1_sel:DWORD
	v_add3_u32 v22, v24, v22, s76
	v_and_b32_sdwa v23, v21, v213 dst_sel:DWORD dst_unused:UNUSED_PAD src0_sel:WORD_1 src1_sel:DWORD
	v_and_b32_sdwa v24, v20, v213 dst_sel:DWORD dst_unused:UNUSED_PAD src0_sel:WORD_1 src1_sel:DWORD
	v_and_b32_sdwa v5, v25, v213 dst_sel:DWORD dst_unused:UNUSED_PAD src0_sel:WORD_1 src1_sel:DWORD
	v_add3_u32 v21, v21, v23, s76
	v_add3_u32 v20, v20, v24, s76
	v_add3_u32 v5, v25, v5, s76
	v_and_b32_e32 v21, 0xffff0000, v21
	v_and_b32_e32 v20, 0xffff0000, v20
	v_or_b32_sdwa v21, v21, v5 dst_sel:DWORD dst_unused:UNUSED_PAD src0_sel:DWORD src1_sel:WORD_1
	v_or_b32_sdwa v20, v20, v22 dst_sel:DWORD dst_unused:UNUSED_PAD src0_sel:DWORD src1_sel:WORD_1
	global_store_dwordx2 v[18:19], v[20:21], off offset:96
	v_mov_b32_e32 v20, v112
	v_mov_b32_e32 v21, v113
	v_mov_b32_e32 v22, v114
	v_mov_b32_e32 v23, v115
	v_mov_b32_e32 v25, v14
	v_mov_b32_e32 v14, v17
	v_mov_b32_e32 v24, v16
	v_pk_mul_f32 v[14:15], v[14:15], v[4:5] op_sel_hi:[1,0]
	v_pk_mul_f32 v[24:25], v[24:25], v[4:5] op_sel_hi:[1,0]
	v_mov_b32_e32 v27, v22
	v_mov_b32_e32 v22, v21
	v_mov_b32_e32 v26, v20
	v_pk_mul_f32 v[14:15], v[22:23], v[14:15]
	v_pk_mul_f32 v[24:25], v[26:27], v[24:25]
	v_and_b32_sdwa v17, v15, v213 dst_sel:DWORD dst_unused:UNUSED_PAD src0_sel:WORD_1 src1_sel:DWORD
	v_and_b32_sdwa v20, v14, v213 dst_sel:DWORD dst_unused:UNUSED_PAD src0_sel:WORD_1 src1_sel:DWORD
	v_and_b32_sdwa v5, v25, v213 dst_sel:DWORD dst_unused:UNUSED_PAD src0_sel:WORD_1 src1_sel:DWORD
	v_and_b32_sdwa v16, v24, v213 dst_sel:DWORD dst_unused:UNUSED_PAD src0_sel:WORD_1 src1_sel:DWORD
	v_add3_u32 v15, v15, v17, s76
	v_add3_u32 v14, v14, v20, s76
	v_add3_u32 v16, v24, v16, s76
	v_add3_u32 v5, v25, v5, s76
; __device__ __forceinline__ unsigned pk2(float lo, float hi) { return f2bf(lo) | (f2bf(hi) << 16); }
; __device__ __forceinline__ void attn_wg_task(const Frame& F, int l, int task) {
;     ...
; #pragma unroll
;         for (int db = 0; db < 8; ++db) {
;             const int d0 = h * HD + db * 16 + rq * 4;
;             const f32x4 g4 = ld_f4(F.attn_g + l * 1024 + d0);
;             u32x2 o; o.x = pk2(O[qb][db][0] * rstd * g4[0], O[qb][db][1] * rstd * g4[1]); o.y = pk2(O[qb][db][2] * rstd * g4[2], O[qb][db][3] * rstd * g4[3]);
;             st_u2(MIX + (size_t)tq * D + d0, o);
;         }
	v_and_b32_e32 v15, 0xffff0000, v15
	v_and_b32_e32 v14, 0xffff0000, v14
	v_or_b32_sdwa v15, v15, v5 dst_sel:DWORD dst_unused:UNUSED_PAD src0_sel:DWORD src1_sel:WORD_1
	v_or_b32_sdwa v14, v14, v16 dst_sel:DWORD dst_unused:UNUSED_PAD src0_sel:DWORD src1_sel:WORD_1
	global_store_dwordx2 v[18:19], v[14:15], off offset:128
	v_mov_b32_e32 v14, v116
	v_mov_b32_e32 v15, v117
	v_mov_b32_e32 v16, v118
	v_mov_b32_e32 v17, v119
	v_mov_b32_e32 v21, v10
	v_mov_b32_e32 v10, v13
	v_mov_b32_e32 v20, v12
	v_pk_mul_f32 v[10:11], v[10:11], v[4:5] op_sel_hi:[1,0]
	v_pk_mul_f32 v[20:21], v[20:21], v[4:5] op_sel_hi:[1,0]
	v_mov_b32_e32 v23, v16
	v_mov_b32_e32 v16, v15
	v_mov_b32_e32 v22, v14
	v_pk_mul_f32 v[10:11], v[16:17], v[10:11]
	v_pk_mul_f32 v[20:21], v[22:23], v[20:21]
	v_and_b32_sdwa v13, v11, v213 dst_sel:DWORD dst_unused:UNUSED_PAD src0_sel:WORD_1 src1_sel:DWORD
	v_and_b32_sdwa v14, v10, v213 dst_sel:DWORD dst_unused:UNUSED_PAD src0_sel:WORD_1 src1_sel:DWORD
	v_and_b32_sdwa v5, v21, v213 dst_sel:DWORD dst_unused:UNUSED_PAD src0_sel:WORD_1 src1_sel:DWORD
	v_and_b32_sdwa v12, v20, v213 dst_sel:DWORD dst_unused:UNUSED_PAD src0_sel:WORD_1 src1_sel:DWORD
	v_add3_u32 v11, v11, v13, s76
	v_add3_u32 v10, v10, v14, s76
	v_add3_u32 v12, v20, v12, s76
	v_add3_u32 v5, v21, v5, s76
	v_and_b32_e32 v11, 0xffff0000, v11
	v_and_b32_e32 v10, 0xffff0000, v10
	v_or_b32_sdwa v11, v11, v5 dst_sel:DWORD dst_unused:UNUSED_PAD src0_sel:DWORD src1_sel:WORD_1
	v_or_b32_sdwa v10, v10, v12 dst_sel:DWORD dst_unused:UNUSED_PAD src0_sel:DWORD src1_sel:WORD_1
	global_store_dwordx2 v[18:19], v[10:11], off offset:160
	v_mov_b32_e32 v10, v120
	v_mov_b32_e32 v11, v121
	v_mov_b32_e32 v12, v122
	v_mov_b32_e32 v13, v123
	v_mov_b32_e32 v15, v6
	v_mov_b32_e32 v6, v9
	v_mov_b32_e32 v14, v8
	v_pk_mul_f32 v[6:7], v[6:7], v[4:5] op_sel_hi:[1,0]
	v_pk_mul_f32 v[14:15], v[14:15], v[4:5] op_sel_hi:[1,0]
	v_mov_b32_e32 v17, v12
	v_mov_b32_e32 v12, v11
	v_mov_b32_e32 v16, v10
	v_pk_mul_f32 v[6:7], v[12:13], v[6:7]
	v_pk_mul_f32 v[14:15], v[16:17], v[14:15]
	v_and_b32_sdwa v9, v7, v213 dst_sel:DWORD dst_unused:UNUSED_PAD src0_sel:WORD_1 src1_sel:DWORD
	v_and_b32_sdwa v10, v6, v213 dst_sel:DWORD dst_unused:UNUSED_PAD src0_sel:WORD_1 src1_sel:DWORD
	v_and_b32_sdwa v5, v15, v213 dst_sel:DWORD dst_unused:UNUSED_PAD src0_sel:WORD_1 src1_sel:DWORD
	v_and_b32_sdwa v8, v14, v213 dst_sel:DWORD dst_unused:UNUSED_PAD src0_sel:WORD_1 src1_sel:DWORD
	v_add3_u32 v7, v7, v9, s76
	v_add3_u32 v6, v6, v10, s76
	v_add3_u32 v8, v14, v8, s76
	v_add3_u32 v5, v15, v5, s76
	v_and_b32_e32 v7, 0xffff0000, v7
	v_and_b32_e32 v6, 0xffff0000, v6
	v_or_b32_sdwa v7, v7, v5 dst_sel:DWORD dst_unused:UNUSED_PAD src0_sel:DWORD src1_sel:WORD_1
	v_or_b32_sdwa v6, v6, v8 dst_sel:DWORD dst_unused:UNUSED_PAD src0_sel:DWORD src1_sel:WORD_1
	global_store_dwordx2 v[18:19], v[6:7], off offset:192
	v_mov_b32_e32 v6, v124
	v_mov_b32_e32 v7, v125
	v_mov_b32_e32 v8, v126
	v_mov_b32_e32 v9, v127
	v_mov_b32_e32 v11, v0
	v_mov_b32_e32 v0, v3
	v_mov_b32_e32 v10, v2
	v_pk_mul_f32 v[0:1], v[0:1], v[4:5] op_sel_hi:[1,0]
	v_pk_mul_f32 v[10:11], v[10:11], v[4:5] op_sel_hi:[1,0]
	v_mov_b32_e32 v13, v8
	v_mov_b32_e32 v8, v7
	v_mov_b32_e32 v12, v6
	v_pk_mul_f32 v[0:1], v[8:9], v[0:1]
	v_pk_mul_f32 v[10:11], v[12:13], v[10:11]
	v_and_b32_sdwa v4, v1, v213 dst_sel:DWORD dst_unused:UNUSED_PAD src0_sel:WORD_1 src1_sel:DWORD
	v_and_b32_sdwa v5, v0, v213 dst_sel:DWORD dst_unused:UNUSED_PAD src0_sel:WORD_1 src1_sel:DWORD
	v_and_b32_sdwa v2, v11, v213 dst_sel:DWORD dst_unused:UNUSED_PAD src0_sel:WORD_1 src1_sel:DWORD
	v_and_b32_sdwa v3, v10, v213 dst_sel:DWORD dst_unused:UNUSED_PAD src0_sel:WORD_1 src1_sel:DWORD
	v_add3_u32 v1, v1, v4, s76
	v_add3_u32 v0, v0, v5, s76
	v_add3_u32 v3, v10, v3, s76
	v_add3_u32 v2, v11, v2, s76
	v_and_b32_e32 v1, 0xffff0000, v1
	v_and_b32_e32 v0, 0xffff0000, v0
	v_or_b32_sdwa v1, v1, v2 dst_sel:DWORD dst_unused:UNUSED_PAD src0_sel:DWORD src1_sel:WORD_1
	v_or_b32_sdwa v0, v0, v3 dst_sel:DWORD dst_unused:UNUSED_PAD src0_sel:DWORD src1_sel:WORD_1
	global_store_dwordx2 v[18:19], v[0:1], off offset:224
	s_cbranch_vccnz .LBB0_577

; __device__ __forceinline__ float rq_max(float v) { v = fmaxf(v, __shfl_xor(v, 16)); v = fmaxf(v, __shfl_xor(v, 32)); return v; }
; __device__ __forceinline__ float fexp2(float x) { return __builtin_amdgcn_exp2f(x); }
; __device__ __forceinline__ void attn_wg_task(const Frame& F, int l, int task) {
;     ...
;             for (int qb = 0; qb < 2; ++qb) {
;                 const float mxr = rq_max(mx[qb]);
;                 const float mn = fmaxf(m_run[qb], mxr); alpha[qb] = fexp2(m_run[qb] - mn);
;                 moved = moved || (mn > m_run[qb]);
;                 float ps = 0.f;
; #pragma unroll
;                 for (int g = 0; g < 2; ++g) {
; #pragma unroll
;                     for (int ab = 0; ab < 2; ++ab)
; #pragma unroll
;                         for (int e = 0; e < 4; ++e) { const float p = fexp2(sa[qb][g][ab][e] - mn); sa[qb][g][ab][e] = p; ps += p; }
;                     Pf[qb][g] = pack8(sa[qb][g][0], sa[qb][g][1]);
;                 }
;                 l_run[qb] = l_run[qb] * alpha[qb] + ps; m_run[qb] = mn;
;             }
;             if (__any(moved)) {
; #pragma unroll
;                 for (int qb = 0; qb < 2; ++qb)
; #pragma unroll
;                     for (int db = 0; db < 8; ++db) O[qb][db] *= alpha[qb];
;             }
.LBB0_533:
	s_nop 4
	ds_bpermute_b32 v112, v202, v234
	v_max_f32_e32 v113, v234, v234
	s_waitcnt lgkmcnt(0)
	v_max_f32_e32 v112, v112, v112
	v_max_f32_e32 v112, v113, v112
	v_mov_b32_e32 v113, v112
	s_nop 1
	v_permlane32_swap_b32_e32 v113, v112
	s_waitcnt lgkmcnt(0)
	v_max3_f32 v130, v233, v112, v113
	v_sub_f32_e32 v112, v233, v130
	v_exp_f32_e32 v129, v112
	ds_bpermute_b32 v112, v202, v184
	v_max_f32_e32 v113, v184, v184
	v_cmp_gt_f32_e32 vcc, v130, v233
	s_waitcnt lgkmcnt(0)
	v_max_f32_e32 v112, v112, v112
	v_max_f32_e32 v112, v113, v112
	v_mov_b32_e32 v113, v112
	s_nop 1
	v_permlane32_swap_b32_e32 v113, v112
	s_waitcnt lgkmcnt(0)
	v_max3_f32 v131, v232, v112, v113
	v_sub_f32_e32 v112, v232, v131
	v_exp_f32_e32 v128, v112
	v_cmp_gt_f32_e64 s[36:37], v131, v232
	s_or_b64 vcc, vcc, s[36:37]
	s_cbranch_vccz .LBB0_535
	v_mov_b32_e32 v112, v129
	v_pk_mul_f32 v[34:35], v[34:35], v[112:113] op_sel_hi:[1,0]
	v_pk_mul_f32 v[32:33], v[32:33], v[112:113] op_sel_hi:[1,0]
	v_pk_mul_f32 v[38:39], v[38:39], v[112:113] op_sel_hi:[1,0]
	v_pk_mul_f32 v[36:37], v[36:37], v[112:113] op_sel_hi:[1,0]
	v_pk_mul_f32 v[42:43], v[42:43], v[112:113] op_sel_hi:[1,0]
	v_pk_mul_f32 v[40:41], v[40:41], v[112:113] op_sel_hi:[1,0]
	v_pk_mul_f32 v[46:47], v[46:47], v[112:113] op_sel_hi:[1,0]
	v_pk_mul_f32 v[44:45], v[44:45], v[112:113] op_sel_hi:[1,0]
	v_pk_mul_f32 v[50:51], v[50:51], v[112:113] op_sel_hi:[1,0]
	v_pk_mul_f32 v[48:49], v[48:49], v[112:113] op_sel_hi:[1,0]
	v_pk_mul_f32 v[54:55], v[54:55], v[112:113] op_sel_hi:[1,0]
	v_pk_mul_f32 v[52:53], v[52:53], v[112:113] op_sel_hi:[1,0]
	v_pk_mul_f32 v[58:59], v[58:59], v[112:113] op_sel_hi:[1,0]
	v_pk_mul_f32 v[56:57], v[56:57], v[112:113] op_sel_hi:[1,0]
	v_pk_mul_f32 v[62:63], v[62:63], v[112:113] op_sel_hi:[1,0]
	v_pk_mul_f32 v[60:61], v[60:61], v[112:113] op_sel_hi:[1,0]
	v_pk_mul_f32 v[6:7], v[6:7], v[128:129] op_sel_hi:[1,0]
	v_pk_mul_f32 v[4:5], v[4:5], v[128:129] op_sel_hi:[1,0]
	v_pk_mul_f32 v[10:11], v[10:11], v[128:129] op_sel_hi:[1,0]
	v_pk_mul_f32 v[8:9], v[8:9], v[128:129] op_sel_hi:[1,0]
	v_pk_mul_f32 v[2:3], v[2:3], v[128:129] op_sel_hi:[1,0]
	v_pk_mul_f32 v[0:1], v[0:1], v[128:129] op_sel_hi:[1,0]
	v_pk_mul_f32 v[14:15], v[14:15], v[128:129] op_sel_hi:[1,0]
	v_pk_mul_f32 v[12:13], v[12:13], v[128:129] op_sel_hi:[1,0]
	v_pk_mul_f32 v[18:19], v[18:19], v[128:129] op_sel_hi:[1,0]
	v_pk_mul_f32 v[16:17], v[16:17], v[128:129] op_sel_hi:[1,0]
	v_pk_mul_f32 v[22:23], v[22:23], v[128:129] op_sel_hi:[1,0]
	v_pk_mul_f32 v[20:21], v[20:21], v[128:129] op_sel_hi:[1,0]
	v_pk_mul_f32 v[26:27], v[26:27], v[128:129] op_sel_hi:[1,0]
	v_pk_mul_f32 v[24:25], v[24:25], v[128:129] op_sel_hi:[1,0]
	v_pk_mul_f32 v[30:31], v[30:31], v[128:129] op_sel_hi:[1,0]
	v_pk_mul_f32 v[28:29], v[28:29], v[128:129] op_sel_hi:[1,0]

; __device__ __forceinline__ float rq_max(float v) { v = fmaxf(v, __shfl_xor(v, 16)); v = fmaxf(v, __shfl_xor(v, 32)); return v; }
; __device__ __forceinline__ float fexp2(float x) { return __builtin_amdgcn_exp2f(x); }
; __device__ __forceinline__ void attn_wg_task(const Frame& F, int l, int task) {
;     ...
;             for (int qb = 0; qb < 2; ++qb) {
;                 const float mxr = rq_max(mx[qb]);
;                 const float mn = fmaxf(m_run[qb], mxr); alpha[qb] = fexp2(m_run[qb] - mn);
;                 moved = moved || (mn > m_run[qb]);
;                 float ps = 0.f;
; #pragma unroll
;                 for (int g = 0; g < 2; ++g) {
; #pragma unroll
;                     for (int ab = 0; ab < 2; ++ab)
; #pragma unroll
;                         for (int e = 0; e < 4; ++e) { const float p = fexp2(sa[qb][g][ab][e] - mn); sa[qb][g][ab][e] = p; ps += p; }
;                     Pf[qb][g] = pack8(sa[qb][g][0], sa[qb][g][1]);
;                 }
;                 l_run[qb] = l_run[qb] * alpha[qb] + ps; m_run[qb] = mn;
;             }
;             if (__any(moved)) {
; #pragma unroll
;                 for (int qb = 0; qb < 2; ++qb)
; #pragma unroll
;                     for (int db = 0; db < 8; ++db) O[qb][db] *= alpha[qb];
;             }
.LBB0_546:
	s_nop 4
	ds_bpermute_b32 v64, v202, v128
	v_max_f32_e32 v65, v128, v128
	v_max_f32_e32 v66, v129, v129
	s_waitcnt lgkmcnt(0)
	v_max_f32_e32 v64, v64, v64
	v_max_f32_e32 v64, v65, v64
	v_mov_b32_e32 v65, v64
	s_nop 1
	v_permlane32_swap_b32_e32 v65, v64
	s_waitcnt lgkmcnt(0)
	v_max3_f32 v64, v130, v64, v65
	v_sub_f32_e32 v65, v130, v64
	v_exp_f32_e32 v97, v65
	ds_bpermute_b32 v65, v202, v129
	v_cmp_gt_f32_e32 vcc, v64, v130
	s_waitcnt lgkmcnt(0)
	v_max_f32_e32 v65, v65, v65
	v_max_f32_e32 v65, v66, v65
	v_mov_b32_e32 v66, v65
	s_nop 1
	v_permlane32_swap_b32_e32 v66, v65
	s_waitcnt lgkmcnt(0)
	v_max3_f32 v68, v232, v65, v66
	v_sub_f32_e32 v65, v232, v68
	v_exp_f32_e32 v96, v65
	v_cmp_gt_f32_e64 s[34:35], v68, v232
	s_or_b64 vcc, vcc, s[34:35]
	s_cbranch_vccz .LBB0_516
	v_mov_b32_e32 v66, v97
	v_pk_mul_f32 v[34:35], v[34:35], v[66:67] op_sel_hi:[1,0]
	v_pk_mul_f32 v[32:33], v[32:33], v[66:67] op_sel_hi:[1,0]
	v_pk_mul_f32 v[38:39], v[38:39], v[66:67] op_sel_hi:[1,0]
	v_pk_mul_f32 v[36:37], v[36:37], v[66:67] op_sel_hi:[1,0]
	v_pk_mul_f32 v[42:43], v[42:43], v[66:67] op_sel_hi:[1,0]
	v_pk_mul_f32 v[40:41], v[40:41], v[66:67] op_sel_hi:[1,0]
	v_pk_mul_f32 v[46:47], v[46:47], v[66:67] op_sel_hi:[1,0]
	v_pk_mul_f32 v[44:45], v[44:45], v[66:67] op_sel_hi:[1,0]
	v_pk_mul_f32 v[50:51], v[50:51], v[66:67] op_sel_hi:[1,0]
	v_pk_mul_f32 v[48:49], v[48:49], v[66:67] op_sel_hi:[1,0]
	v_pk_mul_f32 v[54:55], v[54:55], v[66:67] op_sel_hi:[1,0]
	v_pk_mul_f32 v[52:53], v[52:53], v[66:67] op_sel_hi:[1,0]
	v_pk_mul_f32 v[58:59], v[58:59], v[66:67] op_sel_hi:[1,0]
	v_pk_mul_f32 v[56:57], v[56:57], v[66:67] op_sel_hi:[1,0]
	v_pk_mul_f32 v[62:63], v[62:63], v[66:67] op_sel_hi:[1,0]
	v_pk_mul_f32 v[60:61], v[60:61], v[66:67] op_sel_hi:[1,0]
	v_pk_mul_f32 v[6:7], v[6:7], v[96:97] op_sel_hi:[1,0]
	v_pk_mul_f32 v[4:5], v[4:5], v[96:97] op_sel_hi:[1,0]
	v_pk_mul_f32 v[10:11], v[10:11], v[96:97] op_sel_hi:[1,0]
	v_pk_mul_f32 v[8:9], v[8:9], v[96:97] op_sel_hi:[1,0]
	v_pk_mul_f32 v[2:3], v[2:3], v[96:97] op_sel_hi:[1,0]
	v_pk_mul_f32 v[0:1], v[0:1], v[96:97] op_sel_hi:[1,0]
	v_pk_mul_f32 v[14:15], v[14:15], v[96:97] op_sel_hi:[1,0]
	v_pk_mul_f32 v[12:13], v[12:13], v[96:97] op_sel_hi:[1,0]
	v_pk_mul_f32 v[18:19], v[18:19], v[96:97] op_sel_hi:[1,0]
	v_pk_mul_f32 v[16:17], v[16:17], v[96:97] op_sel_hi:[1,0]
	v_pk_mul_f32 v[22:23], v[22:23], v[96:97] op_sel_hi:[1,0]
	v_pk_mul_f32 v[20:21], v[20:21], v[96:97] op_sel_hi:[1,0]
	v_pk_mul_f32 v[26:27], v[26:27], v[96:97] op_sel_hi:[1,0]
	v_pk_mul_f32 v[24:25], v[24:25], v[96:97] op_sel_hi:[1,0]
	v_pk_mul_f32 v[30:31], v[30:31], v[96:97] op_sel_hi:[1,0]
	v_pk_mul_f32 v[28:29], v[28:29], v[96:97] op_sel_hi:[1,0]
	s_branch .LBB0_516

; __device__ __forceinline__ unsigned pk2(float lo, float hi) { return f2bf(lo) | (f2bf(hi) << 16); }
; __device__ __forceinline__ float rq_sum(float v) { v += __shfl_xor(v, 16); v += __shfl_xor(v, 32); return v; }
; __device__ __forceinline__ float frsq(float x) { return __builtin_amdgcn_rsqf(x); }
; __device__ __forceinline__ void attn_wg_task(const Frame& F, int l, int task) {
;     ...
;     for (int qb = 0; qb < 2; ++qb) {
;         const int tq = tq0 + qb * 16;
;         const float inv = 1.0f / rq_sum(l_run[qb]);
;         float ss = 0.f;
; #pragma unroll
;         for (int db = 0; db < 8; ++db) { O[qb][db] *= inv; ss += (O[qb][db][0] * O[qb][db][0] + O[qb][db][1] * O[qb][db][1]) + (O[qb][db][2] * O[qb][db][2] + O[qb][db][3] * O[qb][db][3]); }
;         const float rstd = frsq(rq_sum(ss) * (1.f / HD) + EPS);
; #pragma unroll
;         for (int db = 0; db < 8; ++db) {
;             const int d0 = h * HD + db * 16 + rq * 4;
;             const f32x4 g4 = ld_f4(F.attn_g + l * 1024 + d0);
;             u32x2 o; o.x = pk2(O[qb][db][0] * rstd * g4[0], O[qb][db][1] * rstd * g4[1]); o.y = pk2(O[qb][db][2] * rstd * g4[2], O[qb][db][3] * rstd * g4[3]);
;             st_u2(MIX + (size_t)tq * D + d0, o);
.LBB0_549:
	v_mov_b32_e32 v64, v151
	v_lshl_or_b32 v82, v204, 2, s19
	v_readlane_b32 s2, v251, 53
	v_readlane_b32 s3, v251, 54
	s_nop 1
	v_permlane16_swap_b32_e32 v64, v151
	s_waitcnt lgkmcnt(0)
	v_add_f32_e32 v64, v151, v64
	ds_bpermute_b32 v65, v203, v64
	s_barrier
	s_waitcnt lgkmcnt(0)
	v_lshlrev_b32_e32 v184, 1, v82
	s_add_i32 s18, s18, s87
	v_add_f32_e32 v64, v64, v65
	v_div_scale_f32 v65, s[0:1], v64, v64, 1.0
	v_rcp_f32_e32 v66, v65
	s_nop 0
	v_fma_f32 v67, -v65, v66, 1.0
	v_fmac_f32_e32 v66, v67, v66
	v_div_scale_f32 v67, vcc, 1.0, v64, 1.0
	v_mul_f32_e32 v68, v67, v66
	v_fma_f32 v69, -v65, v68, v67
	v_fmac_f32_e32 v68, v69, v66
	v_fma_f32 v65, -v65, v68, v67
	v_div_fmas_f32 v65, v65, v66, v68
	v_div_fixup_f32 v84, v65, v64, 1.0
	v_pk_mul_f32 v[80:81], v[32:33], v[84:85] op_sel_hi:[1,0]
	v_pk_mul_f32 v[76:77], v[36:37], v[84:85] op_sel_hi:[1,0]
	v_pk_mul_f32 v[78:79], v[34:35], v[84:85] op_sel_hi:[1,0]
	v_pk_mul_f32 v[74:75], v[38:39], v[84:85] op_sel_hi:[1,0]
	v_mov_b32_e32 v34, v81
	v_mov_b32_e32 v35, v77
	v_mov_b32_e32 v32, v80
	v_mov_b32_e32 v33, v76
	v_pk_mul_f32 v[34:35], v[34:35], v[34:35]
	v_mov_b32_e32 v36, v79
	v_mov_b32_e32 v37, v75
	v_pk_fma_f32 v[32:33], v[32:33], v[32:33], v[34:35]
	v_mov_b32_e32 v34, v78
	v_mov_b32_e32 v35, v74
	v_pk_mul_f32 v[36:37], v[36:37], v[36:37]
	v_pk_mul_f32 v[72:73], v[40:41], v[84:85] op_sel_hi:[1,0]
	v_pk_fma_f32 v[34:35], v[34:35], v[34:35], v[36:37]
	v_pk_mul_f32 v[70:71], v[42:43], v[84:85] op_sel_hi:[1,0]
	v_pk_add_f32 v[32:33], v[32:33], v[34:35]
	v_pk_mul_f32 v[34:35], v[70:71], v[70:71]
	v_pk_add_f32 v[32:33], v[32:33], v[32:33] op_sel_hi:[0,1]
	v_pk_mul_f32 v[36:37], v[72:73], v[72:73]
	v_pk_mul_f32 v[68:69], v[44:45], v[84:85] op_sel_hi:[1,0]
	v_pk_mov_b32 v[38:39], v[36:37], v[34:35] op_sel:[1,0]
	v_mov_b32_e32 v37, v35
	v_pk_mul_f32 v[66:67], v[46:47], v[84:85] op_sel_hi:[1,0]
	v_mul_f32_e32 v32, v68, v68
	v_pk_add_f32 v[34:35], v[38:39], v[36:37]
	v_pk_fma_f32 v[36:37], v[68:69], v[68:69], v[32:33] op_sel_hi:[1,1,0]
	v_mul_f32_e32 v32, v66, v66
	v_pk_add_f32 v[34:35], v[34:35], v[34:35] op_sel_hi:[0,1]
	v_pk_fma_f32 v[38:39], v[66:67], v[66:67], v[32:33] op_sel_hi:[1,1,0]
	v_pk_mul_f32 v[50:51], v[50:51], v[84:85] op_sel_hi:[1,0]
	v_pk_mul_f32 v[64:65], v[48:49], v[84:85] op_sel_hi:[1,0]
	v_mul_f32_e32 v34, v50, v50
	v_mul_f32_e32 v36, v64, v64
	v_mul_f32_e32 v38, v65, v65
	v_mul_f32_e32 v32, v51, v51
	v_pk_add_f32 v[36:37], v[36:37], v[38:39]
	v_pk_add_f32 v[32:33], v[34:35], v[32:33]
	v_pk_mul_f32 v[48:49], v[52:53], v[84:85] op_sel_hi:[1,0]
	v_pk_add_f32 v[32:33], v[36:37], v[32:33]
	v_pk_mul_f32 v[46:47], v[54:55], v[84:85] op_sel_hi:[1,0]
	v_pk_add_f32 v[32:33], v[32:33], v[32:33] op_sel_hi:[0,1]
	v_pk_mul_f32 v[34:35], v[46:47], v[46:47]
	v_pk_mul_f32 v[36:37], v[48:49], v[48:49]
	v_pk_mul_f32 v[44:45], v[56:57], v[84:85] op_sel_hi:[1,0]
	v_pk_mov_b32 v[38:39], v[36:37], v[34:35] op_sel:[1,0]
	v_mov_b32_e32 v37, v35
	v_pk_mul_f32 v[42:43], v[58:59], v[84:85] op_sel_hi:[1,0]
	v_mul_f32_e32 v32, v44, v44
	v_pk_add_f32 v[34:35], v[38:39], v[36:37]
	v_pk_fma_f32 v[40:41], v[44:45], v[44:45], v[32:33] op_sel_hi:[1,1,0]
	v_mul_f32_e32 v32, v42, v42
	v_pk_add_f32 v[34:35], v[34:35], v[34:35] op_sel_hi:[0,1]
	v_pk_fma_f32 v[52:53], v[42:43], v[42:43], v[32:33] op_sel_hi:[1,1,0]
	v_pk_mul_f32 v[36:37], v[62:63], v[84:85] op_sel_hi:[1,0]
	v_pk_mul_f32 v[38:39], v[60:61], v[84:85] op_sel_hi:[1,0]
	v_mul_f32_e32 v34, v36, v36
	v_mul_f32_e32 v40, v38, v38
	v_mul_f32_e32 v52, v39, v39
	v_mul_f32_e32 v32, v37, v37
	v_pk_add_f32 v[40:41], v[40:41], v[52:53]
	v_pk_add_f32 v[32:33], v[34:35], v[32:33]
	v_lshlrev_b32_e32 v54, 2, v82
	global_load_dwordx4 v[96:99], v54, s[42:43]
	global_load_dwordx4 v[100:103], v54, s[42:43] offset:64
	global_load_dwordx4 v[104:107], v54, s[42:43] offset:128
	global_load_dwordx4 v[108:111], v54, s[42:43] offset:192
	global_load_dwordx4 v[112:115], v54, s[42:43] offset:256
	global_load_dwordx4 v[116:119], v54, s[42:43] offset:320
	global_load_dwordx4 v[120:123], v54, s[42:43] offset:384
	global_load_dwordx4 v[124:127], v54, s[42:43] offset:448
	v_pk_add_f32 v[32:33], v[40:41], v[32:33]
	v_mov_b32_e32 v56, v80
	v_add_f32_e32 v32, v32, v33
	v_mov_b32_e32 v33, v32
	v_mov_b32_e32 v57, v78
	v_mov_b32_e32 v78, v81
	s_nop 1
	v_permlane16_swap_b32_e32 v33, v32
	s_waitcnt lgkmcnt(0)
	v_add_f32_e32 v32, v32, v33
	v_mov_b32_e32 v33, v32
	s_nop 1
	v_permlane32_swap_b32_e32 v33, v32
	s_waitcnt lgkmcnt(0)
	v_add_f32_e32 v32, v32, v33
	v_fmamk_f32 v32, v32, 0x3c000000, v214
	v_rsq_f32_e32 v40, v32
	v_lshlrev_b64 v[32:33], 12, v[152:153]
	v_lshl_add_u64 v[52:53], s[2:3], 0, v[32:33]
	s_waitcnt vmcnt(0)
; __device__ __forceinline__ unsigned pk2(float lo, float hi) { return f2bf(lo) | (f2bf(hi) << 16); }
; __device__ __forceinline__ void attn_wg_task(const Frame& F, int l, int task) {
;     ...
; #pragma unroll
;         for (int db = 0; db < 8; ++db) {
;             const int d0 = h * HD + db * 16 + rq * 4;
;             const f32x4 g4 = ld_f4(F.attn_g + l * 1024 + d0);
;             u32x2 o; o.x = pk2(O[qb][db][0] * rstd * g4[0], O[qb][db][1] * rstd * g4[1]); o.y = pk2(O[qb][db][2] * rstd * g4[2], O[qb][db][3] * rstd * g4[3]);
;             st_u2(MIX + (size_t)tq * D + d0, o);
;         }
	v_mov_b32_e32 v32, v96
	v_mov_b32_e32 v33, v97
	v_mov_b32_e32 v34, v98
	v_mov_b32_e32 v35, v99
	v_pk_mul_f32 v[56:57], v[56:57], v[40:41] op_sel_hi:[1,0]
	v_mov_b32_e32 v58, v32
	v_mov_b32_e32 v59, v34
	v_pk_mul_f32 v[56:57], v[58:59], v[56:57]
	v_pk_mul_f32 v[58:59], v[78:79], v[40:41] op_sel_hi:[1,0]
	v_mov_b32_e32 v34, v33
	v_pk_mul_f32 v[32:33], v[34:35], v[58:59]
	v_and_b32_sdwa v35, v56, v213 dst_sel:DWORD dst_unused:UNUSED_PAD src0_sel:WORD_1 src1_sel:DWORD
	v_add3_u32 v41, v56, v35, s76
	v_and_b32_sdwa v35, v33, v213 dst_sel:DWORD dst_unused:UNUSED_PAD src0_sel:WORD_1 src1_sel:DWORD
	v_and_b32_sdwa v55, v32, v213 dst_sel:DWORD dst_unused:UNUSED_PAD src0_sel:WORD_1 src1_sel:DWORD
	v_and_b32_sdwa v34, v57, v213 dst_sel:DWORD dst_unused:UNUSED_PAD src0_sel:WORD_1 src1_sel:DWORD
	v_add3_u32 v33, v33, v35, s76
	v_add3_u32 v32, v32, v55, s76
	v_add3_u32 v34, v57, v34, s76
	v_and_b32_e32 v33, 0xffff0000, v33
	v_and_b32_e32 v32, 0xffff0000, v32
	v_or_b32_sdwa v35, v33, v34 dst_sel:DWORD dst_unused:UNUSED_PAD src0_sel:DWORD src1_sel:WORD_1
	v_or_b32_sdwa v34, v32, v41 dst_sel:DWORD dst_unused:UNUSED_PAD src0_sel:DWORD src1_sel:WORD_1
	v_lshl_add_u64 v[32:33], v[52:53], 0, v[184:185]
	global_store_dwordx2 v[32:33], v[34:35], off
	v_mov_b32_e32 v56, v100
	v_mov_b32_e32 v57, v101
	v_mov_b32_e32 v58, v102
	v_mov_b32_e32 v59, v103
	v_mov_b32_e32 v34, v76
	v_mov_b32_e32 v35, v74
	v_pk_mul_f32 v[34:35], v[34:35], v[40:41] op_sel_hi:[1,0]
	v_mov_b32_e32 v74, v77
	v_mov_b32_e32 v52, v56
	v_mov_b32_e32 v53, v58
	v_pk_mul_f32 v[34:35], v[52:53], v[34:35]
	v_pk_mul_f32 v[52:53], v[74:75], v[40:41] op_sel_hi:[1,0]
	v_mov_b32_e32 v58, v57
	v_pk_mul_f32 v[52:53], v[58:59], v[52:53]
	v_and_b32_sdwa v41, v35, v213 dst_sel:DWORD dst_unused:UNUSED_PAD src0_sel:WORD_1 src1_sel:DWORD
	v_and_b32_sdwa v55, v34, v213 dst_sel:DWORD dst_unused:UNUSED_PAD src0_sel:WORD_1 src1_sel:DWORD
	v_add3_u32 v34, v34, v55, s76
	v_add3_u32 v35, v35, v41, s76
	v_and_b32_sdwa v41, v53, v213 dst_sel:DWORD dst_unused:UNUSED_PAD src0_sel:WORD_1 src1_sel:DWORD
	v_and_b32_sdwa v55, v52, v213 dst_sel:DWORD dst_unused:UNUSED_PAD src0_sel:WORD_1 src1_sel:DWORD
	v_add3_u32 v41, v53, v41, s76
	v_add3_u32 v52, v52, v55, s76
	v_and_b32_e32 v41, 0xffff0000, v41
	v_and_b32_e32 v52, 0xffff0000, v52
	v_or_b32_sdwa v35, v41, v35 dst_sel:DWORD dst_unused:UNUSED_PAD src0_sel:DWORD src1_sel:WORD_1
	v_or_b32_sdwa v34, v52, v34 dst_sel:DWORD dst_unused:UNUSED_PAD src0_sel:DWORD src1_sel:WORD_1
	global_store_dwordx2 v[32:33], v[34:35], off offset:32
	v_mov_b32_e32 v56, v104
	v_mov_b32_e32 v57, v105
	v_mov_b32_e32 v58, v106
	v_mov_b32_e32 v59, v107
	v_mov_b32_e32 v34, v72
	v_mov_b32_e32 v35, v70
	v_pk_mul_f32 v[34:35], v[34:35], v[40:41] op_sel_hi:[1,0]
	v_mov_b32_e32 v70, v73
	v_mov_b32_e32 v52, v56
	v_mov_b32_e32 v53, v58
	v_pk_mul_f32 v[34:35], v[52:53], v[34:35]
	v_pk_mul_f32 v[52:53], v[70:71], v[40:41] op_sel_hi:[1,0]
	v_mov_b32_e32 v58, v57
	v_pk_mul_f32 v[52:53], v[58:59], v[52:53]
	v_and_b32_sdwa v41, v35, v213 dst_sel:DWORD dst_unused:UNUSED_PAD src0_sel:WORD_1 src1_sel:DWORD
	v_and_b32_sdwa v55, v34, v213 dst_sel:DWORD dst_unused:UNUSED_PAD src0_sel:WORD_1 src1_sel:DWORD
	v_add3_u32 v34, v34, v55, s76
	v_add3_u32 v35, v35, v41, s76
	v_and_b32_sdwa v41, v53, v213 dst_sel:DWORD dst_unused:UNUSED_PAD src0_sel:WORD_1 src1_sel:DWORD
	v_and_b32_sdwa v55, v52, v213 dst_sel:DWORD dst_unused:UNUSED_PAD src0_sel:WORD_1 src1_sel:DWORD
	v_add3_u32 v41, v53, v41, s76
	v_add3_u32 v52, v52, v55, s76
	v_and_b32_e32 v41, 0xffff0000, v41
	v_and_b32_e32 v52, 0xffff0000, v52
	v_or_b32_sdwa v35, v41, v35 dst_sel:DWORD dst_unused:UNUSED_PAD src0_sel:DWORD src1_sel:WORD_1
	v_or_b32_sdwa v34, v52, v34 dst_sel:DWORD dst_unused:UNUSED_PAD src0_sel:DWORD src1_sel:WORD_1
	global_store_dwordx2 v[32:33], v[34:35], off offset:64
	v_mov_b32_e32 v56, v108
	v_mov_b32_e32 v57, v109
	v_mov_b32_e32 v58, v110
	v_mov_b32_e32 v59, v111
	v_mov_b32_e32 v34, v68
	v_mov_b32_e32 v35, v66
	v_pk_mul_f32 v[34:35], v[34:35], v[40:41] op_sel_hi:[1,0]
	v_mov_b32_e32 v66, v69
	v_mov_b32_e32 v52, v56
	v_mov_b32_e32 v53, v58
	v_pk_mul_f32 v[34:35], v[52:53], v[34:35]
	v_pk_mul_f32 v[52:53], v[66:67], v[40:41] op_sel_hi:[1,0]
	v_mov_b32_e32 v58, v57
	v_pk_mul_f32 v[52:53], v[58:59], v[52:53]
	v_and_b32_sdwa v41, v35, v213 dst_sel:DWORD dst_unused:UNUSED_PAD src0_sel:WORD_1 src1_sel:DWORD
	v_and_b32_sdwa v55, v34, v213 dst_sel:DWORD dst_unused:UNUSED_PAD src0_sel:WORD_1 src1_sel:DWORD
	v_add3_u32 v34, v34, v55, s76
	v_add3_u32 v35, v35, v41, s76
	v_and_b32_sdwa v41, v53, v213 dst_sel:DWORD dst_unused:UNUSED_PAD src0_sel:WORD_1 src1_sel:DWORD
	v_and_b32_sdwa v55, v52, v213 dst_sel:DWORD dst_unused:UNUSED_PAD src0_sel:WORD_1 src1_sel:DWORD
	v_add3_u32 v41, v53, v41, s76
	v_add3_u32 v52, v52, v55, s76
	v_and_b32_e32 v41, 0xffff0000, v41
	v_and_b32_e32 v52, 0xffff0000, v52
	v_or_b32_sdwa v35, v41, v35 dst_sel:DWORD dst_unused:UNUSED_PAD src0_sel:DWORD src1_sel:WORD_1
	v_or_b32_sdwa v34, v52, v34 dst_sel:DWORD dst_unused:UNUSED_PAD src0_sel:DWORD src1_sel:WORD_1
	global_store_dwordx2 v[32:33], v[34:35], off offset:96
	v_mov_b32_e32 v56, v112
	v_mov_b32_e32 v57, v113
	v_mov_b32_e32 v58, v114
	v_mov_b32_e32 v59, v115
	v_mov_b32_e32 v34, v64
	v_mov_b32_e32 v35, v50
	v_pk_mul_f32 v[34:35], v[34:35], v[40:41] op_sel_hi:[1,0]
	v_mov_b32_e32 v50, v65
	v_pk_mul_f32 v[50:51], v[50:51], v[40:41] op_sel_hi:[1,0]
	v_mov_b32_e32 v52, v56
	v_mov_b32_e32 v53, v58
	v_pk_mul_f32 v[34:35], v[52:53], v[34:35]
	v_mov_b32_e32 v58, v57
	v_pk_mul_f32 v[50:51], v[58:59], v[50:51]
	v_and_b32_sdwa v41, v35, v213 dst_sel:DWORD dst_unused:UNUSED_PAD src0_sel:WORD_1 src1_sel:DWORD
; __device__ __forceinline__ unsigned pk2(float lo, float hi) { return f2bf(lo) | (f2bf(hi) << 16); }
; __device__ __forceinline__ float rq_sum(float v) { v += __shfl_xor(v, 16); v += __shfl_xor(v, 32); return v; }
; __device__ __forceinline__ float frsq(float x) { return __builtin_amdgcn_rsqf(x); }
; __device__ __forceinline__ void attn_wg_task(const Frame& F, int l, int task) {
;     ...
;     for (int qb = 0; qb < 2; ++qb) {
;         const int tq = tq0 + qb * 16;
;         const float inv = 1.0f / rq_sum(l_run[qb]);
;         float ss = 0.f;
; #pragma unroll
;         for (int db = 0; db < 8; ++db) { O[qb][db] *= inv; ss += (O[qb][db][0] * O[qb][db][0] + O[qb][db][1] * O[qb][db][1]) + (O[qb][db][2] * O[qb][db][2] + O[qb][db][3] * O[qb][db][3]); }
;         const float rstd = frsq(rq_sum(ss) * (1.f / HD) + EPS);
; #pragma unroll
;         for (int db = 0; db < 8; ++db) {
;             const int d0 = h * HD + db * 16 + rq * 4;
;             const f32x4 g4 = ld_f4(F.attn_g + l * 1024 + d0);
;             u32x2 o; o.x = pk2(O[qb][db][0] * rstd * g4[0], O[qb][db][1] * rstd * g4[1]); o.y = pk2(O[qb][db][2] * rstd * g4[2], O[qb][db][3] * rstd * g4[3]);
;             st_u2(MIX + (size_t)tq * D + d0, o);
;         }
	v_and_b32_sdwa v52, v34, v213 dst_sel:DWORD dst_unused:UNUSED_PAD src0_sel:WORD_1 src1_sel:DWORD
	v_add3_u32 v34, v34, v52, s76
	v_add3_u32 v35, v35, v41, s76
	v_and_b32_sdwa v41, v51, v213 dst_sel:DWORD dst_unused:UNUSED_PAD src0_sel:WORD_1 src1_sel:DWORD
	v_and_b32_sdwa v52, v50, v213 dst_sel:DWORD dst_unused:UNUSED_PAD src0_sel:WORD_1 src1_sel:DWORD
	v_add3_u32 v41, v51, v41, s76
	v_add3_u32 v50, v50, v52, s76
	v_and_b32_e32 v41, 0xffff0000, v41
	v_and_b32_e32 v50, 0xffff0000, v50
	v_or_b32_sdwa v35, v41, v35 dst_sel:DWORD dst_unused:UNUSED_PAD src0_sel:DWORD src1_sel:WORD_1
	v_or_b32_sdwa v34, v50, v34 dst_sel:DWORD dst_unused:UNUSED_PAD src0_sel:DWORD src1_sel:WORD_1
	global_store_dwordx2 v[32:33], v[34:35], off offset:128
	v_mov_b32_e32 v50, v116
	v_mov_b32_e32 v51, v117
	v_mov_b32_e32 v52, v118
	v_mov_b32_e32 v53, v119
	v_mov_b32_e32 v34, v48
	v_mov_b32_e32 v35, v46
	v_pk_mul_f32 v[34:35], v[34:35], v[40:41] op_sel_hi:[1,0]
	v_mov_b32_e32 v46, v49
	v_pk_mul_f32 v[46:47], v[46:47], v[40:41] op_sel_hi:[1,0]
	v_mov_b32_e32 v56, v50
	v_mov_b32_e32 v57, v52
	v_pk_mul_f32 v[34:35], v[56:57], v[34:35]
	v_mov_b32_e32 v52, v51
	v_pk_mul_f32 v[46:47], v[52:53], v[46:47]
	v_and_b32_sdwa v41, v35, v213 dst_sel:DWORD dst_unused:UNUSED_PAD src0_sel:WORD_1 src1_sel:DWORD
	v_and_b32_sdwa v48, v34, v213 dst_sel:DWORD dst_unused:UNUSED_PAD src0_sel:WORD_1 src1_sel:DWORD
	v_add3_u32 v34, v34, v48, s76
	v_add3_u32 v35, v35, v41, s76
	v_and_b32_sdwa v41, v47, v213 dst_sel:DWORD dst_unused:UNUSED_PAD src0_sel:WORD_1 src1_sel:DWORD
	v_and_b32_sdwa v48, v46, v213 dst_sel:DWORD dst_unused:UNUSED_PAD src0_sel:WORD_1 src1_sel:DWORD
	v_add3_u32 v41, v47, v41, s76
	v_add3_u32 v46, v46, v48, s76
	v_and_b32_e32 v41, 0xffff0000, v41
	v_and_b32_e32 v46, 0xffff0000, v46
	v_or_b32_sdwa v35, v41, v35 dst_sel:DWORD dst_unused:UNUSED_PAD src0_sel:DWORD src1_sel:WORD_1
	v_or_b32_sdwa v34, v46, v34 dst_sel:DWORD dst_unused:UNUSED_PAD src0_sel:DWORD src1_sel:WORD_1
	global_store_dwordx2 v[32:33], v[34:35], off offset:160
	v_mov_b32_e32 v46, v120
	v_mov_b32_e32 v47, v121
	v_mov_b32_e32 v48, v122
	v_mov_b32_e32 v49, v123
	v_mov_b32_e32 v34, v44
	v_mov_b32_e32 v35, v42
	v_pk_mul_f32 v[34:35], v[34:35], v[40:41] op_sel_hi:[1,0]
	v_mov_b32_e32 v42, v45
	v_pk_mul_f32 v[42:43], v[42:43], v[40:41] op_sel_hi:[1,0]
	v_mov_b32_e32 v50, v46
	v_mov_b32_e32 v51, v48
	v_pk_mul_f32 v[34:35], v[50:51], v[34:35]
	v_mov_b32_e32 v48, v47
	v_pk_mul_f32 v[42:43], v[48:49], v[42:43]
	v_and_b32_sdwa v41, v35, v213 dst_sel:DWORD dst_unused:UNUSED_PAD src0_sel:WORD_1 src1_sel:DWORD
	v_and_b32_sdwa v44, v34, v213 dst_sel:DWORD dst_unused:UNUSED_PAD src0_sel:WORD_1 src1_sel:DWORD
	v_add3_u32 v34, v34, v44, s76
	v_add3_u32 v35, v35, v41, s76
	v_and_b32_sdwa v41, v43, v213 dst_sel:DWORD dst_unused:UNUSED_PAD src0_sel:WORD_1 src1_sel:DWORD
	v_and_b32_sdwa v44, v42, v213 dst_sel:DWORD dst_unused:UNUSED_PAD src0_sel:WORD_1 src1_sel:DWORD
	v_add3_u32 v41, v43, v41, s76
	v_add3_u32 v42, v42, v44, s76
	v_and_b32_e32 v41, 0xffff0000, v41
	v_and_b32_e32 v42, 0xffff0000, v42
	v_or_b32_sdwa v35, v41, v35 dst_sel:DWORD dst_unused:UNUSED_PAD src0_sel:DWORD src1_sel:WORD_1
	v_or_b32_sdwa v34, v42, v34 dst_sel:DWORD dst_unused:UNUSED_PAD src0_sel:DWORD src1_sel:WORD_1
	global_store_dwordx2 v[32:33], v[34:35], off offset:192
	v_mov_b32_e32 v42, v124
	v_mov_b32_e32 v43, v125
	v_mov_b32_e32 v44, v126
	v_mov_b32_e32 v45, v127
	v_mov_b32_e32 v34, v38
	v_mov_b32_e32 v35, v36
	v_pk_mul_f32 v[34:35], v[34:35], v[40:41] op_sel_hi:[1,0]
	v_mov_b32_e32 v36, v39
	v_pk_mul_f32 v[36:37], v[36:37], v[40:41] op_sel_hi:[1,0]
	v_mov_b32_e32 v46, v42
	v_mov_b32_e32 v47, v44
	v_pk_mul_f32 v[34:35], v[46:47], v[34:35]
	v_mov_b32_e32 v44, v43
	v_pk_mul_f32 v[36:37], v[44:45], v[36:37]
	v_and_b32_sdwa v38, v35, v213 dst_sel:DWORD dst_unused:UNUSED_PAD src0_sel:WORD_1 src1_sel:DWORD
	v_and_b32_sdwa v39, v34, v213 dst_sel:DWORD dst_unused:UNUSED_PAD src0_sel:WORD_1 src1_sel:DWORD
	v_add3_u32 v34, v34, v39, s76
	v_add3_u32 v35, v35, v38, s76
	v_and_b32_sdwa v38, v37, v213 dst_sel:DWORD dst_unused:UNUSED_PAD src0_sel:WORD_1 src1_sel:DWORD
	v_and_b32_sdwa v39, v36, v213 dst_sel:DWORD dst_unused:UNUSED_PAD src0_sel:WORD_1 src1_sel:DWORD
	v_add3_u32 v37, v37, v38, s76
	v_add3_u32 v36, v36, v39, s76
	v_and_b32_e32 v37, 0xffff0000, v37
	v_and_b32_e32 v36, 0xffff0000, v36
	v_or_b32_sdwa v35, v37, v35 dst_sel:DWORD dst_unused:UNUSED_PAD src0_sel:DWORD src1_sel:WORD_1
	v_or_b32_sdwa v34, v36, v34 dst_sel:DWORD dst_unused:UNUSED_PAD src0_sel:DWORD src1_sel:WORD_1
	global_store_dwordx2 v[32:33], v[34:35], off offset:224
	v_mov_b32_e32 v32, v150
	s_nop 1
	v_permlane16_swap_b32_e32 v32, v150
	s_waitcnt lgkmcnt(0)
	v_add_f32_e32 v32, v150, v32
	v_mov_b32_e32 v33, v32
	s_nop 1
	v_permlane32_swap_b32_e32 v33, v32
	s_waitcnt lgkmcnt(0)
; __device__ __forceinline__ unsigned pk2(float lo, float hi) { return f2bf(lo) | (f2bf(hi) << 16); }
; __device__ __forceinline__ float rq_sum(float v) { v += __shfl_xor(v, 16); v += __shfl_xor(v, 32); return v; }
; __device__ __forceinline__ float frsq(float x) { return __builtin_amdgcn_rsqf(x); }
; __device__ __forceinline__ void attn_wg_task(const Frame& F, int l, int task) {
;     ...
;         const float inv = 1.0f / rq_sum(l_run[qb]);
;         float ss = 0.f;
; #pragma unroll
;         for (int db = 0; db < 8; ++db) { O[qb][db] *= inv; ss += (O[qb][db][0] * O[qb][db][0] + O[qb][db][1] * O[qb][db][1]) + (O[qb][db][2] * O[qb][db][2] + O[qb][db][3] * O[qb][db][3]); }
;         const float rstd = frsq(rq_sum(ss) * (1.f / HD) + EPS);
; #pragma unroll
;         for (int db = 0; db < 8; ++db) {
;             const int d0 = h * HD + db * 16 + rq * 4;
;             const f32x4 g4 = ld_f4(F.attn_g + l * 1024 + d0);
;             u32x2 o; o.x = pk2(O[qb][db][0] * rstd * g4[0], O[qb][db][1] * rstd * g4[1]); o.y = pk2(O[qb][db][2] * rstd * g4[2], O[qb][db][3] * rstd * g4[3]);
;             st_u2(MIX + (size_t)tq * D + d0, o);
;         }
	v_add_f32_e32 v32, v32, v33
	v_div_scale_f32 v33, s[0:1], v32, v32, 1.0
	v_rcp_f32_e32 v34, v33
	v_readlane_b32 s0, v250, 0
	s_add_i32 s17, s17, s0
	v_readlane_b32 s0, v250, 2
	v_fma_f32 v35, -v33, v34, 1.0
	v_fmac_f32_e32 v34, v35, v34
	v_div_scale_f32 v35, vcc, 1.0, v32, 1.0
	v_mul_f32_e32 v36, v35, v34
	v_fma_f32 v37, -v33, v36, v35
	v_fmac_f32_e32 v36, v37, v34
	v_fma_f32 v33, -v33, v36, v35
	v_div_fmas_f32 v33, v33, v34, v36
	v_div_fixup_f32 v48, v33, v32, 1.0
	v_pk_mul_f32 v[46:47], v[4:5], v[48:49] op_sel_hi:[1,0]
	v_pk_mul_f32 v[42:43], v[8:9], v[48:49] op_sel_hi:[1,0]
	v_pk_mul_f32 v[44:45], v[6:7], v[48:49] op_sel_hi:[1,0]
	v_pk_mul_f32 v[36:37], v[10:11], v[48:49] op_sel_hi:[1,0]
	v_mov_b32_e32 v6, v47
	v_mov_b32_e32 v7, v43
	v_mov_b32_e32 v4, v46
	v_mov_b32_e32 v5, v42
	v_pk_mul_f32 v[6:7], v[6:7], v[6:7]
	v_mov_b32_e32 v8, v45
	v_mov_b32_e32 v9, v37
	v_pk_fma_f32 v[4:5], v[4:5], v[4:5], v[6:7]
	v_mov_b32_e32 v6, v44
	v_mov_b32_e32 v7, v36
	v_pk_mul_f32 v[8:9], v[8:9], v[8:9]
	v_pk_mul_f32 v[40:41], v[0:1], v[48:49] op_sel_hi:[1,0]
	v_pk_mul_f32 v[38:39], v[2:3], v[48:49] op_sel_hi:[1,0]
	v_pk_fma_f32 v[6:7], v[6:7], v[6:7], v[8:9]
	v_pk_mul_f32 v[0:1], v[38:39], v[38:39]
	v_pk_mul_f32 v[2:3], v[40:41], v[40:41]
	v_pk_add_f32 v[4:5], v[4:5], v[6:7]
	v_pk_mov_b32 v[6:7], v[2:3], v[0:1] op_sel:[1,0]
	v_mov_b32_e32 v3, v1
	v_pk_add_f32 v[0:1], v[6:7], v[2:3]
	v_pk_mul_f32 v[34:35], v[12:13], v[48:49] op_sel_hi:[1,0]
	v_pk_add_f32 v[0:1], v[0:1], v[0:1] op_sel_hi:[0,1]
	v_pk_mul_f32 v[32:33], v[14:15], v[48:49] op_sel_hi:[1,0]
	v_mul_f32_e32 v0, v34, v34
	v_pk_fma_f32 v[2:3], v[34:35], v[34:35], v[0:1] op_sel_hi:[1,1,0]
	v_mul_f32_e32 v0, v32, v32
	v_pk_add_f32 v[4:5], v[4:5], v[4:5] op_sel_hi:[0,1]
	v_pk_fma_f32 v[6:7], v[32:33], v[32:33], v[0:1] op_sel_hi:[1,1,0]
	v_pk_mul_f32 v[14:15], v[18:19], v[48:49] op_sel_hi:[1,0]
	v_pk_mul_f32 v[16:17], v[16:17], v[48:49] op_sel_hi:[1,0]
	v_mul_f32_e32 v0, v14, v14
	v_mul_f32_e32 v2, v16, v16
	v_mul_f32_e32 v6, v17, v17
	v_mul_f32_e32 v4, v15, v15
	v_pk_add_f32 v[2:3], v[2:3], v[6:7]
	v_pk_add_f32 v[0:1], v[0:1], v[4:5]
	v_pk_mul_f32 v[12:13], v[20:21], v[48:49] op_sel_hi:[1,0]
	v_pk_add_f32 v[0:1], v[2:3], v[0:1]
	v_pk_mul_f32 v[10:11], v[22:23], v[48:49] op_sel_hi:[1,0]
	v_pk_add_f32 v[4:5], v[0:1], v[0:1] op_sel_hi:[0,1]
	v_pk_mul_f32 v[0:1], v[10:11], v[10:11]
	v_pk_mul_f32 v[2:3], v[12:13], v[12:13]
	v_pk_mul_f32 v[8:9], v[24:25], v[48:49] op_sel_hi:[1,0]
	v_pk_mov_b32 v[6:7], v[2:3], v[0:1] op_sel:[1,0]
	v_mov_b32_e32 v3, v1
	v_pk_add_f32 v[0:1], v[6:7], v[2:3]
	v_pk_mul_f32 v[6:7], v[26:27], v[48:49] op_sel_hi:[1,0]
	v_pk_add_f32 v[18:19], v[0:1], v[0:1] op_sel_hi:[0,1]
	v_mul_f32_e32 v0, v8, v8
	v_pk_fma_f32 v[20:21], v[8:9], v[8:9], v[0:1] op_sel_hi:[1,1,0]
	v_mul_f32_e32 v0, v6, v6
	v_pk_fma_f32 v[22:23], v[6:7], v[6:7], v[0:1] op_sel_hi:[1,1,0]
	v_pk_mul_f32 v[0:1], v[30:31], v[48:49] op_sel_hi:[1,0]
	v_pk_mul_f32 v[2:3], v[28:29], v[48:49] op_sel_hi:[1,0]
	v_mul_f32_e32 v18, v0, v0
	v_mul_f32_e32 v20, v2, v2
	v_mul_f32_e32 v22, v3, v3
	v_mul_f32_e32 v4, v1, v1
	v_pk_add_f32 v[20:21], v[20:21], v[22:23]
	v_pk_add_f32 v[4:5], v[18:19], v[4:5]
	v_mov_b32_e32 v24, v46
	v_pk_add_f32 v[4:5], v[20:21], v[4:5]
	v_mov_b32_e32 v20, v96
	v_mov_b32_e32 v21, v97
	v_mov_b32_e32 v22, v98
	v_mov_b32_e32 v23, v99
	v_add_f32_e32 v4, v4, v5
	v_mov_b32_e32 v5, v4
	v_mov_b32_e32 v25, v44
	v_mov_b32_e32 v44, v47
	v_lshlrev_b64 v[18:19], 12, v[148:149]
	v_lshl_add_u64 v[18:19], s[2:3], 0, v[18:19]
	s_nop 1
	v_permlane16_swap_b32_e32 v5, v4
	s_waitcnt lgkmcnt(0)
	v_add_f32_e32 v4, v4, v5
	v_mov_b32_e32 v5, v4
	v_lshl_add_u64 v[18:19], v[18:19], 0, v[184:185]
	s_add_i32 s16, s16, s0
	s_cmpk_lt_i32 s18, 0x200
	s_nop 1
	v_permlane32_swap_b32_e32 v5, v4
	s_waitcnt lgkmcnt(0)
	v_add_f32_e32 v4, v4, v5
	v_fmamk_f32 v4, v4, 0x3c000000, v214
	v_rsq_f32_e32 v4, v4
	v_mov_b32_e32 v26, v20
	v_pk_mul_f32 v[24:25], v[24:25], v[4:5] op_sel_hi:[1,0]
	v_mov_b32_e32 v27, v22
	v_pk_mul_f32 v[24:25], v[26:27], v[24:25]
	v_pk_mul_f32 v[26:27], v[44:45], v[4:5] op_sel_hi:[1,0]
	v_mov_b32_e32 v22, v21
	v_pk_mul_f32 v[20:21], v[22:23], v[26:27]
	v_and_b32_sdwa v22, v24, v213 dst_sel:DWORD dst_unused:UNUSED_PAD src0_sel:WORD_1 src1_sel:DWORD
	v_add3_u32 v22, v24, v22, s76
	v_and_b32_sdwa v23, v21, v213 dst_sel:DWORD dst_unused:UNUSED_PAD src0_sel:WORD_1 src1_sel:DWORD
	v_and_b32_sdwa v24, v20, v213 dst_sel:DWORD dst_unused:UNUSED_PAD src0_sel:WORD_1 src1_sel:DWORD
	v_and_b32_sdwa v5, v25, v213 dst_sel:DWORD dst_unused:UNUSED_PAD src0_sel:WORD_1 src1_sel:DWORD
	v_add3_u32 v21, v21, v23, s76
	v_add3_u32 v20, v20, v24, s76
	v_add3_u32 v5, v25, v5, s76
	v_and_b32_e32 v21, 0xffff0000, v21
	v_and_b32_e32 v20, 0xffff0000, v20
	v_or_b32_sdwa v21, v21, v5 dst_sel:DWORD dst_unused:UNUSED_PAD src0_sel:DWORD src1_sel:WORD_1
	v_or_b32_sdwa v20, v20, v22 dst_sel:DWORD dst_unused:UNUSED_PAD src0_sel:DWORD src1_sel:WORD_1
	global_store_dwordx2 v[18:19], v[20:21], off
	v_mov_b32_e32 v20, v100
	v_mov_b32_e32 v21, v101
	v_mov_b32_e32 v22, v102
	v_mov_b32_e32 v23, v103
	v_mov_b32_e32 v24, v42
	v_mov_b32_e32 v25, v36
	v_pk_mul_f32 v[24:25], v[24:25], v[4:5] op_sel_hi:[1,0]
	v_mov_b32_e32 v36, v43
	v_mov_b32_e32 v26, v20
	v_mov_b32_e32 v27, v22
	v_pk_mul_f32 v[24:25], v[26:27], v[24:25]
	v_pk_mul_f32 v[26:27], v[36:37], v[4:5] op_sel_hi:[1,0]
	v_mov_b32_e32 v22, v21
	v_pk_mul_f32 v[20:21], v[22:23], v[26:27]
	v_and_b32_sdwa v22, v24, v213 dst_sel:DWORD dst_unused:UNUSED_PAD src0_sel:WORD_1 src1_sel:DWORD
	v_add3_u32 v22, v24, v22, s76
	v_and_b32_sdwa v23, v21, v213 dst_sel:DWORD dst_unused:UNUSED_PAD src0_sel:WORD_1 src1_sel:DWORD
; __device__ __forceinline__ unsigned pk2(float lo, float hi) { return f2bf(lo) | (f2bf(hi) << 16); }
; __device__ __forceinline__ void attn_wg_task(const Frame& F, int l, int task) {
;     ...
; #pragma unroll
;         for (int db = 0; db < 8; ++db) {
;             const int d0 = h * HD + db * 16 + rq * 4;
;             const f32x4 g4 = ld_f4(F.attn_g + l * 1024 + d0);
;             u32x2 o; o.x = pk2(O[qb][db][0] * rstd * g4[0], O[qb][db][1] * rstd * g4[1]); o.y = pk2(O[qb][db][2] * rstd * g4[2], O[qb][db][3] * rstd * g4[3]);
;             st_u2(MIX + (size_t)tq * D + d0, o);
;         }
	v_and_b32_sdwa v24, v20, v213 dst_sel:DWORD dst_unused:UNUSED_PAD src0_sel:WORD_1 src1_sel:DWORD
	v_and_b32_sdwa v5, v25, v213 dst_sel:DWORD dst_unused:UNUSED_PAD src0_sel:WORD_1 src1_sel:DWORD
	v_add3_u32 v21, v21, v23, s76
	v_add3_u32 v20, v20, v24, s76
	v_add3_u32 v5, v25, v5, s76
	v_and_b32_e32 v21, 0xffff0000, v21
	v_and_b32_e32 v20, 0xffff0000, v20
	v_or_b32_sdwa v21, v21, v5 dst_sel:DWORD dst_unused:UNUSED_PAD src0_sel:DWORD src1_sel:WORD_1
	v_or_b32_sdwa v20, v20, v22 dst_sel:DWORD dst_unused:UNUSED_PAD src0_sel:DWORD src1_sel:WORD_1
	global_store_dwordx2 v[18:19], v[20:21], off offset:32
	v_mov_b32_e32 v20, v104
	v_mov_b32_e32 v21, v105
	v_mov_b32_e32 v22, v106
	v_mov_b32_e32 v23, v107
	v_mov_b32_e32 v24, v40
	v_mov_b32_e32 v25, v38
	v_pk_mul_f32 v[24:25], v[24:25], v[4:5] op_sel_hi:[1,0]
	v_mov_b32_e32 v38, v41
	v_mov_b32_e32 v26, v20
	v_mov_b32_e32 v27, v22
	v_pk_mul_f32 v[24:25], v[26:27], v[24:25]
	v_pk_mul_f32 v[26:27], v[38:39], v[4:5] op_sel_hi:[1,0]
	v_mov_b32_e32 v22, v21
	v_pk_mul_f32 v[20:21], v[22:23], v[26:27]
	v_and_b32_sdwa v22, v24, v213 dst_sel:DWORD dst_unused:UNUSED_PAD src0_sel:WORD_1 src1_sel:DWORD
	v_add3_u32 v22, v24, v22, s76
	v_and_b32_sdwa v23, v21, v213 dst_sel:DWORD dst_unused:UNUSED_PAD src0_sel:WORD_1 src1_sel:DWORD
	v_and_b32_sdwa v24, v20, v213 dst_sel:DWORD dst_unused:UNUSED_PAD src0_sel:WORD_1 src1_sel:DWORD
	v_and_b32_sdwa v5, v25, v213 dst_sel:DWORD dst_unused:UNUSED_PAD src0_sel:WORD_1 src1_sel:DWORD
	v_add3_u32 v21, v21, v23, s76
	v_add3_u32 v20, v20, v24, s76
	v_add3_u32 v5, v25, v5, s76
	v_and_b32_e32 v21, 0xffff0000, v21
	v_and_b32_e32 v20, 0xffff0000, v20
	v_or_b32_sdwa v21, v21, v5 dst_sel:DWORD dst_unused:UNUSED_PAD src0_sel:DWORD src1_sel:WORD_1
	v_or_b32_sdwa v20, v20, v22 dst_sel:DWORD dst_unused:UNUSED_PAD src0_sel:DWORD src1_sel:WORD_1
	global_store_dwordx2 v[18:19], v[20:21], off offset:64
	v_mov_b32_e32 v20, v108
	v_mov_b32_e32 v21, v109
	v_mov_b32_e32 v22, v110
	v_mov_b32_e32 v23, v111
	v_mov_b32_e32 v24, v34
	v_mov_b32_e32 v25, v32
	v_pk_mul_f32 v[24:25], v[24:25], v[4:5] op_sel_hi:[1,0]
	v_mov_b32_e32 v32, v35
	v_mov_b32_e32 v26, v20
	v_mov_b32_e32 v27, v22
	v_pk_mul_f32 v[24:25], v[26:27], v[24:25]
	v_pk_mul_f32 v[26:27], v[32:33], v[4:5] op_sel_hi:[1,0]
	v_mov_b32_e32 v22, v21
	v_pk_mul_f32 v[20:21], v[22:23], v[26:27]
	v_and_b32_sdwa v22, v24, v213 dst_sel:DWORD dst_unused:UNUSED_PAD src0_sel:WORD_1 src1_sel:DWORD
	v_add3_u32 v22, v24, v22, s76
	v_and_b32_sdwa v23, v21, v213 dst_sel:DWORD dst_unused:UNUSED_PAD src0_sel:WORD_1 src1_sel:DWORD
	v_and_b32_sdwa v24, v20, v213 dst_sel:DWORD dst_unused:UNUSED_PAD src0_sel:WORD_1 src1_sel:DWORD
	v_and_b32_sdwa v5, v25, v213 dst_sel:DWORD dst_unused:UNUSED_PAD src0_sel:WORD_1 src1_sel:DWORD
	v_add3_u32 v21, v21, v23, s76
	v_add3_u32 v20, v20, v24, s76
	v_add3_u32 v5, v25, v5, s76
	v_and_b32_e32 v21, 0xffff0000, v21
	v_and_b32_e32 v20, 0xffff0000, v20
	v_or_b32_sdwa v21, v21, v5 dst_sel:DWORD dst_unused:UNUSED_PAD src0_sel:DWORD src1_sel:WORD_1
	v_or_b32_sdwa v20, v20, v22 dst_sel:DWORD dst_unused:UNUSED_PAD src0_sel:DWORD src1_sel:WORD_1
	global_store_dwordx2 v[18:19], v[20:21], off offset:96
	v_mov_b32_e32 v20, v112
	v_mov_b32_e32 v21, v113
	v_mov_b32_e32 v22, v114
	v_mov_b32_e32 v23, v115
	v_mov_b32_e32 v25, v14
	v_mov_b32_e32 v14, v17
	v_mov_b32_e32 v24, v16
	v_pk_mul_f32 v[14:15], v[14:15], v[4:5] op_sel_hi:[1,0]
	v_pk_mul_f32 v[24:25], v[24:25], v[4:5] op_sel_hi:[1,0]
	v_mov_b32_e32 v27, v22
	v_mov_b32_e32 v22, v21
	v_mov_b32_e32 v26, v20
	v_pk_mul_f32 v[14:15], v[22:23], v[14:15]
	v_pk_mul_f32 v[24:25], v[26:27], v[24:25]
	v_and_b32_sdwa v17, v15, v213 dst_sel:DWORD dst_unused:UNUSED_PAD src0_sel:WORD_1 src1_sel:DWORD
	v_and_b32_sdwa v20, v14, v213 dst_sel:DWORD dst_unused:UNUSED_PAD src0_sel:WORD_1 src1_sel:DWORD
	v_and_b32_sdwa v5, v25, v213 dst_sel:DWORD dst_unused:UNUSED_PAD src0_sel:WORD_1 src1_sel:DWORD
	v_and_b32_sdwa v16, v24, v213 dst_sel:DWORD dst_unused:UNUSED_PAD src0_sel:WORD_1 src1_sel:DWORD
	v_add3_u32 v15, v15, v17, s76
	v_add3_u32 v14, v14, v20, s76
	v_add3_u32 v16, v24, v16, s76
	v_add3_u32 v5, v25, v5, s76
; __device__ __forceinline__ unsigned pk2(float lo, float hi) { return f2bf(lo) | (f2bf(hi) << 16); }
; __device__ __forceinline__ void attn_wg_task(const Frame& F, int l, int task) {
;     ...
; #pragma unroll
;         for (int db = 0; db < 8; ++db) {
;             const int d0 = h * HD + db * 16 + rq * 4;
;             const f32x4 g4 = ld_f4(F.attn_g + l * 1024 + d0);
;             u32x2 o; o.x = pk2(O[qb][db][0] * rstd * g4[0], O[qb][db][1] * rstd * g4[1]); o.y = pk2(O[qb][db][2] * rstd * g4[2], O[qb][db][3] * rstd * g4[3]);
;             st_u2(MIX + (size_t)tq * D + d0, o);
;         }
	v_and_b32_e32 v15, 0xffff0000, v15
	v_and_b32_e32 v14, 0xffff0000, v14
	v_or_b32_sdwa v15, v15, v5 dst_sel:DWORD dst_unused:UNUSED_PAD src0_sel:DWORD src1_sel:WORD_1
	v_or_b32_sdwa v14, v14, v16 dst_sel:DWORD dst_unused:UNUSED_PAD src0_sel:DWORD src1_sel:WORD_1
	global_store_dwordx2 v[18:19], v[14:15], off offset:128
	v_mov_b32_e32 v14, v116
	v_mov_b32_e32 v15, v117
	v_mov_b32_e32 v16, v118
	v_mov_b32_e32 v17, v119
	v_mov_b32_e32 v21, v10
	v_mov_b32_e32 v10, v13
	v_mov_b32_e32 v20, v12
	v_pk_mul_f32 v[10:11], v[10:11], v[4:5] op_sel_hi:[1,0]
	v_pk_mul_f32 v[20:21], v[20:21], v[4:5] op_sel_hi:[1,0]
	v_mov_b32_e32 v23, v16
	v_mov_b32_e32 v16, v15
	v_mov_b32_e32 v22, v14
	v_pk_mul_f32 v[10:11], v[16:17], v[10:11]
	v_pk_mul_f32 v[20:21], v[22:23], v[20:21]
	v_and_b32_sdwa v13, v11, v213 dst_sel:DWORD dst_unused:UNUSED_PAD src0_sel:WORD_1 src1_sel:DWORD
	v_and_b32_sdwa v14, v10, v213 dst_sel:DWORD dst_unused:UNUSED_PAD src0_sel:WORD_1 src1_sel:DWORD
	v_and_b32_sdwa v5, v21, v213 dst_sel:DWORD dst_unused:UNUSED_PAD src0_sel:WORD_1 src1_sel:DWORD
	v_and_b32_sdwa v12, v20, v213 dst_sel:DWORD dst_unused:UNUSED_PAD src0_sel:WORD_1 src1_sel:DWORD
	v_add3_u32 v11, v11, v13, s76
	v_add3_u32 v10, v10, v14, s76
	v_add3_u32 v12, v20, v12, s76
	v_add3_u32 v5, v21, v5, s76
	v_and_b32_e32 v11, 0xffff0000, v11
	v_and_b32_e32 v10, 0xffff0000, v10
	v_or_b32_sdwa v11, v11, v5 dst_sel:DWORD dst_unused:UNUSED_PAD src0_sel:DWORD src1_sel:WORD_1
	v_or_b32_sdwa v10, v10, v12 dst_sel:DWORD dst_unused:UNUSED_PAD src0_sel:DWORD src1_sel:WORD_1
	global_store_dwordx2 v[18:19], v[10:11], off offset:160
	v_mov_b32_e32 v10, v120
	v_mov_b32_e32 v11, v121
	v_mov_b32_e32 v12, v122
	v_mov_b32_e32 v13, v123
	v_mov_b32_e32 v15, v6
	v_mov_b32_e32 v6, v9
	v_mov_b32_e32 v14, v8
	v_pk_mul_f32 v[6:7], v[6:7], v[4:5] op_sel_hi:[1,0]
	v_pk_mul_f32 v[14:15], v[14:15], v[4:5] op_sel_hi:[1,0]
	v_mov_b32_e32 v17, v12
	v_mov_b32_e32 v12, v11
	v_mov_b32_e32 v16, v10
	v_pk_mul_f32 v[6:7], v[12:13], v[6:7]
	v_pk_mul_f32 v[14:15], v[16:17], v[14:15]
	v_and_b32_sdwa v9, v7, v213 dst_sel:DWORD dst_unused:UNUSED_PAD src0_sel:WORD_1 src1_sel:DWORD
	v_and_b32_sdwa v10, v6, v213 dst_sel:DWORD dst_unused:UNUSED_PAD src0_sel:WORD_1 src1_sel:DWORD
	v_and_b32_sdwa v5, v15, v213 dst_sel:DWORD dst_unused:UNUSED_PAD src0_sel:WORD_1 src1_sel:DWORD
	v_and_b32_sdwa v8, v14, v213 dst_sel:DWORD dst_unused:UNUSED_PAD src0_sel:WORD_1 src1_sel:DWORD
	v_add3_u32 v7, v7, v9, s76
	v_add3_u32 v6, v6, v10, s76
	v_add3_u32 v8, v14, v8, s76
	v_add3_u32 v5, v15, v5, s76
	v_and_b32_e32 v7, 0xffff0000, v7
	v_and_b32_e32 v6, 0xffff0000, v6
	v_or_b32_sdwa v7, v7, v5 dst_sel:DWORD dst_unused:UNUSED_PAD src0_sel:DWORD src1_sel:WORD_1
	v_or_b32_sdwa v6, v6, v8 dst_sel:DWORD dst_unused:UNUSED_PAD src0_sel:DWORD src1_sel:WORD_1
	global_store_dwordx2 v[18:19], v[6:7], off offset:192
	v_mov_b32_e32 v6, v124
	v_mov_b32_e32 v7, v125
	v_mov_b32_e32 v8, v126
	v_mov_b32_e32 v9, v127
	v_mov_b32_e32 v11, v0
	v_mov_b32_e32 v0, v3
	v_mov_b32_e32 v10, v2
	v_pk_mul_f32 v[0:1], v[0:1], v[4:5] op_sel_hi:[1,0]
	v_pk_mul_f32 v[10:11], v[10:11], v[4:5] op_sel_hi:[1,0]
	v_mov_b32_e32 v13, v8
	v_mov_b32_e32 v8, v7
	v_mov_b32_e32 v12, v6
	v_pk_mul_f32 v[0:1], v[8:9], v[0:1]
	v_pk_mul_f32 v[10:11], v[12:13], v[10:11]
	v_and_b32_sdwa v4, v1, v213 dst_sel:DWORD dst_unused:UNUSED_PAD src0_sel:WORD_1 src1_sel:DWORD
	v_and_b32_sdwa v5, v0, v213 dst_sel:DWORD dst_unused:UNUSED_PAD src0_sel:WORD_1 src1_sel:DWORD
	v_and_b32_sdwa v2, v11, v213 dst_sel:DWORD dst_unused:UNUSED_PAD src0_sel:WORD_1 src1_sel:DWORD
	v_and_b32_sdwa v3, v10, v213 dst_sel:DWORD dst_unused:UNUSED_PAD src0_sel:WORD_1 src1_sel:DWORD
	v_add3_u32 v1, v1, v4, s76
	v_add3_u32 v0, v0, v5, s76
	v_add3_u32 v3, v10, v3, s76
	v_add3_u32 v2, v11, v2, s76
	v_and_b32_e32 v1, 0xffff0000, v1
	v_and_b32_e32 v0, 0xffff0000, v0
	v_or_b32_sdwa v1, v1, v2 dst_sel:DWORD dst_unused:UNUSED_PAD src0_sel:DWORD src1_sel:WORD_1
	v_or_b32_sdwa v0, v0, v3 dst_sel:DWORD dst_unused:UNUSED_PAD src0_sel:DWORD src1_sel:WORD_1
	global_store_dwordx2 v[18:19], v[0:1], off offset:224
	s_cbranch_scc0 .LBB0_479

; __device__ __forceinline__ unsigned pk2(float lo, float hi) { return f2bf(lo) | (f2bf(hi) << 16); }
; __device__ __forceinline__ float rq_sum(float v) { v += __shfl_xor(v, 16); v += __shfl_xor(v, 32); return v; }
; __device__ __forceinline__ float frsq(float x) { return __builtin_amdgcn_rsqf(x); }
; __device__ __forceinline__ void ret_task(const Frame& F, int l, int task) {
;     ...
; #pragma unroll
;     for (int eb = 0; eb < 8; ++eb) g4[eb] = ld_f4(F.ret_g + l * 1024 + h * HD + eb * 16 + rq * 4);
; #pragma unroll
;     for (int qb = 0; qb < 2; ++qb) {
;         const int t = tq0 + qb * 16 + c;
;         float ss = 0.f;
; #pragma unroll
;         for (int eb = 0; eb < 8; ++eb) ss += (acc[qb][eb][0] * acc[qb][eb][0] + acc[qb][eb][1] * acc[qb][eb][1]) + (acc[qb][eb][2] * acc[qb][eb][2] + acc[qb][eb][3] * acc[qb][eb][3]);
;         const float rstd = frsq(rq_sum(ss) * (1.f / HD) + EPS);
; #pragma unroll
;         for (int eb = 0; eb < 8; ++eb) {
;             const int e0 = h * HD + eb * 16 + rq * 4;
;             const f32x4 gg = g4[eb]; const u32x2 gw = gwq[qb][eb];
;             u32x2 o; o.x = pk2(acc[qb][eb][0] * rstd * gg[0] * bf_lo(gw.x), acc[qb][eb][1] * rstd * gg[1] * bf_hi(gw.x));
;             o.y = pk2(acc[qb][eb][2] * rstd * gg[2] * bf_lo(gw.y), acc[qb][eb][3] * rstd * gg[3] * bf_hi(gw.y));
;             st_u2(MIX + (size_t)t * D + 1024 + e0, o);
;         }
.LBB0_633:
	s_lshl_b32 s0, s9, 2
	s_add_u32 s0, s2, s0
	s_addc_u32 s1, s3, 0
	v_ashrrev_i32_e32 v209, 31, v208
	v_lshl_add_u64 v[24:25], v[208:209], 2, s[0:1]
	global_load_dwordx4 v[20:23], v[24:25], off
	v_pk_mul_f32 v[58:59], v[90:91], v[90:91]
	v_pk_mul_f32 v[64:65], v[88:89], v[88:89]
	v_mul_f32_e32 v60, v84, v84
	v_mul_f32_e32 v62, v86, v86
	s_waitcnt vmcnt(17)
	v_pk_mov_b32 v[78:79], v[64:65], v[58:59] op_sel:[1,0]
	v_mov_b32_e32 v65, v59
	v_pk_fma_f32 v[58:59], v[84:85], v[84:85], v[60:61] op_sel_hi:[1,1,0]
	v_pk_fma_f32 v[82:83], v[86:87], v[86:87], v[62:63] op_sel_hi:[1,1,0]
	global_load_dwordx4 v[60:63], v[24:25], off offset:64
	v_mov_b32_e32 v52, v97
	v_mov_b32_e32 v53, v109
	v_mov_b32_e32 v56, v99
	v_mov_b32_e32 v57, v111
	v_mov_b32_e32 v26, v96
	v_mov_b32_e32 v27, v108
	v_mov_b32_e32 v54, v98
	v_mov_b32_e32 v55, v110
	v_pk_mul_f32 v[52:53], v[52:53], v[52:53]
	v_pk_mul_f32 v[56:57], v[56:57], v[56:57]
	v_pk_fma_f32 v[26:27], v[26:27], v[26:27], v[52:53]
	v_pk_fma_f32 v[52:53], v[54:55], v[54:55], v[56:57]
	v_pk_add_f32 v[54:55], v[78:79], v[64:65]
	v_pk_add_f32 v[26:27], v[26:27], v[52:53]
	v_pk_mul_f32 v[66:67], v[50:51], v[50:51]
	v_pk_mul_f32 v[72:73], v[48:49], v[48:49]
	v_pk_add_f32 v[52:53], v[54:55], v[54:55] op_sel_hi:[0,1]
	v_pk_add_f32 v[26:27], v[26:27], v[26:27] op_sel_hi:[0,1]
	v_pk_mov_b32 v[92:93], v[72:73], v[66:67] op_sel:[1,0]
	v_mov_b32_e32 v73, v67
	v_mul_f32_e32 v58, v68, v68
	v_mul_f32_e32 v82, v69, v69
	v_mul_f32_e32 v52, v70, v70
	v_mul_f32_e32 v26, v71, v71
	v_pk_add_f32 v[56:57], v[92:93], v[72:73]
	v_pk_add_f32 v[54:55], v[58:59], v[82:83]
	v_pk_add_f32 v[26:27], v[52:53], v[26:27]
	v_mul_f32_e32 v74, v44, v44
	v_mul_f32_e32 v76, v46, v46
	v_pk_add_f32 v[64:65], v[56:57], v[56:57] op_sel_hi:[0,1]
	global_load_dwordx4 v[56:59], v[24:25], off offset:128
	v_pk_add_f32 v[26:27], v[54:55], v[26:27]
	v_pk_fma_f32 v[66:67], v[44:45], v[44:45], v[74:75] op_sel_hi:[1,1,0]
	v_pk_fma_f32 v[74:75], v[46:47], v[46:47], v[76:77] op_sel_hi:[1,1,0]
	v_pk_add_f32 v[26:27], v[26:27], v[26:27] op_sel_hi:[0,1]
	v_mul_f32_e32 v66, v40, v40
	v_mul_f32_e32 v74, v41, v41
	v_mul_f32_e32 v64, v42, v42
	v_mul_f32_e32 v26, v43, v43
	v_pk_add_f32 v[66:67], v[66:67], v[74:75]
	v_pk_add_f32 v[26:27], v[64:65], v[26:27]
	global_load_dwordx4 v[76:79], v[24:25], off offset:192
	v_pk_add_f32 v[26:27], v[66:67], v[26:27]
	v_ashrrev_i32_e32 v197, 31, v196
	v_add_f32_e32 v26, v26, v27
	ds_bpermute_b32 v27, v226, v26
	v_mov_b32_e32 v80, v108
	v_mov_b32_e32 v81, v110
	v_mov_b32_e32 v110, v109
	s_waitcnt vmcnt(11)
	v_lshlrev_b32_e32 v83, 16, v207
	s_waitcnt lgkmcnt(0)
	v_add_f32_e32 v52, v26, v27
	v_mov_b32_e32 v53, v52
	v_lshlrev_b64 v[26:27], 12, v[196:197]
	v_lshl_add_u64 v[100:101], s[62:63], 0, v[26:27]
	v_lshlrev_b32_e32 v82, 16, v206
	v_and_b32_e32 v95, 0xffff0000, v207
	s_nop 1
	v_permlane32_swap_b32_e32 v53, v52
	s_waitcnt lgkmcnt(0)
	v_add_f32_e32 v26, v52, v53
	v_fmamk_f32 v26, v26, 0x3c000000, v214
	v_rsq_f32_e32 v92, v26
	global_load_dwordx4 v[72:75], v[24:25], off offset:256
	global_load_dwordx4 v[64:67], v[24:25], off offset:320
	global_load_dwordx4 v[52:55], v[24:25], off offset:384
	s_nop 0
	global_load_dwordx4 v[24:27], v[24:25], off offset:448
	v_and_b32_e32 v94, 0xffff0000, v206
	s_mov_b64 s[4:5], 0x26c00800
	v_pk_mul_f32 v[102:103], v[80:81], v[92:93] op_sel_hi:[1,0]
	v_pk_mul_f32 v[104:105], v[110:111], v[92:93] op_sel_hi:[1,0]
	s_mov_b32 s0, 0x26c00000
	v_ashrrev_i32_e32 v195, 31, v194
	s_add_i32 s8, s8, s82
	s_cmpk_gt_i32 s8, 0xfff
	s_waitcnt vmcnt(7)
	v_mov_b32_e32 v80, v20
	v_mov_b32_e32 v81, v22
	v_mov_b32_e32 v22, v21
	v_pk_mul_f32 v[20:21], v[80:81], v[102:103]
	v_pk_mul_f32 v[102:103], v[22:23], v[104:105]
	v_pk_mul_f32 v[20:21], v[20:21], v[82:83]
	v_pk_mul_f32 v[82:83], v[102:103], v[94:95]
	v_and_b32_sdwa v93, v21, v213 dst_sel:DWORD dst_unused:UNUSED_PAD src0_sel:WORD_1 src1_sel:DWORD
	v_and_b32_sdwa v94, v20, v213 dst_sel:DWORD dst_unused:UNUSED_PAD src0_sel:WORD_1 src1_sel:DWORD
	v_add3_u32 v20, v20, v94, s76
	v_add3_u32 v21, v21, v93, s76
	v_and_b32_sdwa v93, v83, v213 dst_sel:DWORD dst_unused:UNUSED_PAD src0_sel:WORD_1 src1_sel:DWORD
	v_and_b32_sdwa v94, v82, v213 dst_sel:DWORD dst_unused:UNUSED_PAD src0_sel:WORD_1 src1_sel:DWORD
	v_add3_u32 v83, v83, v93, s76
	v_add3_u32 v82, v82, v94, s76
	v_and_b32_e32 v83, 0xffff0000, v83
	v_and_b32_e32 v82, 0xffff0000, v82
	v_lshl_add_u64 v[94:95], v[100:101], 0, v[156:157]
	v_or_b32_sdwa v21, v83, v21 dst_sel:DWORD dst_unused:UNUSED_PAD src0_sel:DWORD src1_sel:WORD_1
	v_or_b32_sdwa v20, v82, v20 dst_sel:DWORD dst_unused:UNUSED_PAD src0_sel:DWORD src1_sel:WORD_1
	v_lshl_add_u64 v[82:83], v[94:95], 0, s[4:5]
	v_add_co_u32_e32 v94, vcc, s0, v94
	v_lshlrev_b32_e32 v101, 16, v205
	s_nop 0
	v_addc_co_u32_e32 v95, vcc, 0, v95, vcc
	global_store_dwordx2 v[94:95], v[20:21], off offset:2048
	v_mov_b32_e32 v20, v96
	v_mov_b32_e32 v21, v98
	v_pk_mul_f32 v[94:95], v[20:21], v[92:93] op_sel_hi:[1,0]
	s_waitcnt vmcnt(7)
; __device__ __forceinline__ unsigned pk2(float lo, float hi) { return f2bf(lo) | (f2bf(hi) << 16); }
; __device__ __forceinline__ void ret_task(const Frame& F, int l, int task) {
;     ...
;         for (int eb = 0; eb < 8; ++eb) {
;             const int e0 = h * HD + eb * 16 + rq * 4;
;             const f32x4 gg = g4[eb]; const u32x2 gw = gwq[qb][eb];
;             u32x2 o; o.x = pk2(acc[qb][eb][0] * rstd * gg[0] * bf_lo(gw.x), acc[qb][eb][1] * rstd * gg[1] * bf_hi(gw.x));
;             o.y = pk2(acc[qb][eb][2] * rstd * gg[2] * bf_lo(gw.y), acc[qb][eb][3] * rstd * gg[3] * bf_hi(gw.y));
;             st_u2(MIX + (size_t)t * D + 1024 + e0, o);
;         }
	v_mov_b32_e32 v20, v60
	v_mov_b32_e32 v21, v62
	v_mov_b32_e32 v98, v97
	v_pk_mul_f32 v[94:95], v[20:21], v[94:95]
	v_lshlrev_b32_e32 v100, 16, v204
	v_pk_mul_f32 v[96:97], v[98:99], v[92:93] op_sel_hi:[1,0]
	v_mov_b32_e32 v62, v61
	v_pk_mul_f32 v[94:95], v[94:95], v[100:101]
	v_pk_mul_f32 v[60:61], v[62:63], v[96:97]
	v_and_b32_e32 v97, 0xffff0000, v205
	v_and_b32_e32 v96, 0xffff0000, v204
	v_pk_mul_f32 v[60:61], v[60:61], v[96:97]
	v_and_b32_sdwa v93, v95, v213 dst_sel:DWORD dst_unused:UNUSED_PAD src0_sel:WORD_1 src1_sel:DWORD
	v_and_b32_sdwa v96, v94, v213 dst_sel:DWORD dst_unused:UNUSED_PAD src0_sel:WORD_1 src1_sel:DWORD
	v_add3_u32 v94, v94, v96, s76
	v_add3_u32 v93, v95, v93, s76
	v_and_b32_sdwa v95, v61, v213 dst_sel:DWORD dst_unused:UNUSED_PAD src0_sel:WORD_1 src1_sel:DWORD
	v_and_b32_sdwa v96, v60, v213 dst_sel:DWORD dst_unused:UNUSED_PAD src0_sel:WORD_1 src1_sel:DWORD
	v_add3_u32 v61, v61, v95, s76
	v_add3_u32 v60, v60, v96, s76
	v_and_b32_e32 v61, 0xffff0000, v61
	v_and_b32_e32 v60, 0xffff0000, v60
	v_or_b32_sdwa v61, v61, v93 dst_sel:DWORD dst_unused:UNUSED_PAD src0_sel:DWORD src1_sel:WORD_1
	v_or_b32_sdwa v60, v60, v94 dst_sel:DWORD dst_unused:UNUSED_PAD src0_sel:DWORD src1_sel:WORD_1
	global_store_dwordx2 v[82:83], v[60:61], off offset:32
	v_mov_b32_e32 v60, v88
	v_mov_b32_e32 v61, v90
	v_mov_b32_e32 v90, v89
	v_pk_mul_f32 v[94:95], v[60:61], v[92:93] op_sel_hi:[1,0]
	s_waitcnt vmcnt(7)
	v_mov_b32_e32 v61, v58
	v_pk_mul_f32 v[88:89], v[90:91], v[92:93] op_sel_hi:[1,0]
	v_mov_b32_e32 v58, v57
	v_mov_b32_e32 v60, v56
	v_pk_mul_f32 v[56:57], v[58:59], v[88:89]
	v_and_b32_e32 v89, 0xffff0000, v203
	v_and_b32_e32 v88, 0xffff0000, v202
	v_pk_mul_f32 v[94:95], v[60:61], v[94:95]
	v_lshlrev_b32_e32 v97, 16, v203
	v_lshlrev_b32_e32 v96, 16, v202
	v_pk_mul_f32 v[56:57], v[56:57], v[88:89]
	v_pk_mul_f32 v[94:95], v[94:95], v[96:97]
	v_and_b32_sdwa v90, v57, v213 dst_sel:DWORD dst_unused:UNUSED_PAD src0_sel:WORD_1 src1_sel:DWORD
	v_and_b32_sdwa v91, v56, v213 dst_sel:DWORD dst_unused:UNUSED_PAD src0_sel:WORD_1 src1_sel:DWORD
	v_and_b32_sdwa v88, v95, v213 dst_sel:DWORD dst_unused:UNUSED_PAD src0_sel:WORD_1 src1_sel:DWORD
	v_and_b32_sdwa v89, v94, v213 dst_sel:DWORD dst_unused:UNUSED_PAD src0_sel:WORD_1 src1_sel:DWORD
	v_add3_u32 v57, v57, v90, s76
	v_add3_u32 v56, v56, v91, s76
	v_add3_u32 v89, v94, v89, s76
	v_add3_u32 v88, v95, v88, s76
	v_and_b32_e32 v57, 0xffff0000, v57
	v_and_b32_e32 v56, 0xffff0000, v56
	v_or_b32_sdwa v57, v57, v88 dst_sel:DWORD dst_unused:UNUSED_PAD src0_sel:DWORD src1_sel:WORD_1
	v_or_b32_sdwa v56, v56, v89 dst_sel:DWORD dst_unused:UNUSED_PAD src0_sel:DWORD src1_sel:WORD_1
	global_store_dwordx2 v[82:83], v[56:57], off offset:64
	v_mov_b32_e32 v56, v84
	v_mov_b32_e32 v57, v86
	v_mov_b32_e32 v86, v85
	v_pk_mul_f32 v[88:89], v[56:57], v[92:93] op_sel_hi:[1,0]
	s_waitcnt vmcnt(7)
	v_mov_b32_e32 v57, v78
	v_pk_mul_f32 v[84:85], v[86:87], v[92:93] op_sel_hi:[1,0]
	v_mov_b32_e32 v78, v77
	v_mov_b32_e32 v56, v76
	v_pk_mul_f32 v[76:77], v[78:79], v[84:85]
	v_and_b32_e32 v85, 0xffff0000, v201
	v_and_b32_e32 v84, 0xffff0000, v200
	v_pk_mul_f32 v[88:89], v[56:57], v[88:89]
	v_lshlrev_b32_e32 v91, 16, v201
	v_lshlrev_b32_e32 v90, 16, v200
	v_pk_mul_f32 v[76:77], v[76:77], v[84:85]
	v_pk_mul_f32 v[88:89], v[88:89], v[90:91]
	v_and_b32_sdwa v86, v77, v213 dst_sel:DWORD dst_unused:UNUSED_PAD src0_sel:WORD_1 src1_sel:DWORD
	v_and_b32_sdwa v87, v76, v213 dst_sel:DWORD dst_unused:UNUSED_PAD src0_sel:WORD_1 src1_sel:DWORD
	v_and_b32_sdwa v84, v89, v213 dst_sel:DWORD dst_unused:UNUSED_PAD src0_sel:WORD_1 src1_sel:DWORD
	v_and_b32_sdwa v85, v88, v213 dst_sel:DWORD dst_unused:UNUSED_PAD src0_sel:WORD_1 src1_sel:DWORD
	v_add3_u32 v77, v77, v86, s76
	v_add3_u32 v76, v76, v87, s76
	v_add3_u32 v85, v88, v85, s76
	v_add3_u32 v84, v89, v84, s76
	v_and_b32_e32 v77, 0xffff0000, v77
	v_and_b32_e32 v76, 0xffff0000, v76
	v_or_b32_sdwa v77, v77, v84 dst_sel:DWORD dst_unused:UNUSED_PAD src0_sel:DWORD src1_sel:WORD_1
	v_or_b32_sdwa v76, v76, v85 dst_sel:DWORD dst_unused:UNUSED_PAD src0_sel:DWORD src1_sel:WORD_1
	global_store_dwordx2 v[82:83], v[76:77], off offset:96
	v_mov_b32_e32 v76, v68
	v_mov_b32_e32 v77, v70
	v_mov_b32_e32 v70, v69
	v_pk_mul_f32 v[84:85], v[76:77], v[92:93] op_sel_hi:[1,0]
	s_waitcnt vmcnt(7)
	v_mov_b32_e32 v77, v74
	v_pk_mul_f32 v[68:69], v[70:71], v[92:93] op_sel_hi:[1,0]
	v_mov_b32_e32 v74, v73
	v_mov_b32_e32 v76, v72
	v_pk_mul_f32 v[68:69], v[74:75], v[68:69]
	v_and_b32_e32 v71, 0xffff0000, v199
	v_and_b32_e32 v70, 0xffff0000, v198
	v_pk_mul_f32 v[84:85], v[76:77], v[84:85]
	v_lshlrev_b32_e32 v87, 16, v199
	v_lshlrev_b32_e32 v86, 16, v198
	v_pk_mul_f32 v[68:69], v[68:69], v[70:71]
	v_pk_mul_f32 v[84:85], v[84:85], v[86:87]
	v_and_b32_sdwa v72, v69, v213 dst_sel:DWORD dst_unused:UNUSED_PAD src0_sel:WORD_1 src1_sel:DWORD
	v_and_b32_sdwa v73, v68, v213 dst_sel:DWORD dst_unused:UNUSED_PAD src0_sel:WORD_1 src1_sel:DWORD
	v_and_b32_sdwa v70, v85, v213 dst_sel:DWORD dst_unused:UNUSED_PAD src0_sel:WORD_1 src1_sel:DWORD
	v_and_b32_sdwa v71, v84, v213 dst_sel:DWORD dst_unused:UNUSED_PAD src0_sel:WORD_1 src1_sel:DWORD
	v_add3_u32 v69, v69, v72, s76
	v_add3_u32 v68, v68, v73, s76
	v_add3_u32 v71, v84, v71, s76
	v_add3_u32 v70, v85, v70, s76
	v_and_b32_e32 v69, 0xffff0000, v69
	v_and_b32_e32 v68, 0xffff0000, v68
	v_or_b32_sdwa v69, v69, v70 dst_sel:DWORD dst_unused:UNUSED_PAD src0_sel:DWORD src1_sel:WORD_1
	v_or_b32_sdwa v68, v68, v71 dst_sel:DWORD dst_unused:UNUSED_PAD src0_sel:DWORD src1_sel:WORD_1
	global_store_dwordx2 v[82:83], v[68:69], off offset:128
	v_mov_b32_e32 v68, v48
	v_mov_b32_e32 v69, v50
	v_mov_b32_e32 v50, v49
	v_pk_mul_f32 v[70:71], v[68:69], v[92:93] op_sel_hi:[1,0]
	s_waitcnt vmcnt(7)
; __device__ __forceinline__ unsigned pk2(float lo, float hi) { return f2bf(lo) | (f2bf(hi) << 16); }
; __device__ __forceinline__ float rq_sum(float v) { v += __shfl_xor(v, 16); v += __shfl_xor(v, 32); return v; }
; __device__ __forceinline__ float frsq(float x) { return __builtin_amdgcn_rsqf(x); }
; __device__ __forceinline__ void ret_task(const Frame& F, int l, int task) {
;     ...
;     for (int qb = 0; qb < 2; ++qb) {
;         const int t = tq0 + qb * 16 + c;
;         float ss = 0.f;
; #pragma unroll
;         for (int eb = 0; eb < 8; ++eb) ss += (acc[qb][eb][0] * acc[qb][eb][0] + acc[qb][eb][1] * acc[qb][eb][1]) + (acc[qb][eb][2] * acc[qb][eb][2] + acc[qb][eb][3] * acc[qb][eb][3]);
;         const float rstd = frsq(rq_sum(ss) * (1.f / HD) + EPS);
; #pragma unroll
;         for (int eb = 0; eb < 8; ++eb) {
;             const int e0 = h * HD + eb * 16 + rq * 4;
;             const f32x4 gg = g4[eb]; const u32x2 gw = gwq[qb][eb];
;             u32x2 o; o.x = pk2(acc[qb][eb][0] * rstd * gg[0] * bf_lo(gw.x), acc[qb][eb][1] * rstd * gg[1] * bf_hi(gw.x));
;             o.y = pk2(acc[qb][eb][2] * rstd * gg[2] * bf_lo(gw.y), acc[qb][eb][3] * rstd * gg[3] * bf_hi(gw.y));
;             st_u2(MIX + (size_t)t * D + 1024 + e0, o);
;         }
	v_mov_b32_e32 v69, v66
	v_pk_mul_f32 v[48:49], v[50:51], v[92:93] op_sel_hi:[1,0]
	v_mov_b32_e32 v66, v65
	v_mov_b32_e32 v68, v64
	v_pk_mul_f32 v[48:49], v[66:67], v[48:49]
	v_and_b32_e32 v51, 0xffff0000, v167
	v_and_b32_e32 v50, 0xffff0000, v166
	v_pk_mul_f32 v[70:71], v[68:69], v[70:71]
	v_lshlrev_b32_e32 v73, 16, v167
	v_lshlrev_b32_e32 v72, 16, v166
	v_pk_mul_f32 v[48:49], v[48:49], v[50:51]
	v_pk_mul_f32 v[70:71], v[70:71], v[72:73]
	v_and_b32_sdwa v64, v49, v213 dst_sel:DWORD dst_unused:UNUSED_PAD src0_sel:WORD_1 src1_sel:DWORD
	v_and_b32_sdwa v65, v48, v213 dst_sel:DWORD dst_unused:UNUSED_PAD src0_sel:WORD_1 src1_sel:DWORD
	v_and_b32_sdwa v50, v71, v213 dst_sel:DWORD dst_unused:UNUSED_PAD src0_sel:WORD_1 src1_sel:DWORD
	v_and_b32_sdwa v51, v70, v213 dst_sel:DWORD dst_unused:UNUSED_PAD src0_sel:WORD_1 src1_sel:DWORD
	v_add3_u32 v49, v49, v64, s76
	v_add3_u32 v48, v48, v65, s76
	v_add3_u32 v51, v70, v51, s76
	v_add3_u32 v50, v71, v50, s76
	v_and_b32_e32 v49, 0xffff0000, v49
	v_and_b32_e32 v48, 0xffff0000, v48
	v_or_b32_sdwa v49, v49, v50 dst_sel:DWORD dst_unused:UNUSED_PAD src0_sel:DWORD src1_sel:WORD_1
	v_or_b32_sdwa v48, v48, v51 dst_sel:DWORD dst_unused:UNUSED_PAD src0_sel:DWORD src1_sel:WORD_1
	global_store_dwordx2 v[82:83], v[48:49], off offset:160
	v_mov_b32_e32 v48, v44
	v_mov_b32_e32 v49, v46
	v_pk_mul_f32 v[50:51], v[48:49], v[92:93] op_sel_hi:[1,0]
	s_waitcnt vmcnt(7)
	v_mov_b32_e32 v48, v52
	v_mov_b32_e32 v49, v54
	v_mov_b32_e32 v46, v45
	v_pk_mul_f32 v[50:51], v[48:49], v[50:51]
	v_lshlrev_b32_e32 v65, 16, v165
	v_lshlrev_b32_e32 v64, 16, v164
	v_pk_mul_f32 v[44:45], v[46:47], v[92:93] op_sel_hi:[1,0]
	v_mov_b32_e32 v54, v53
	v_pk_mul_f32 v[50:51], v[50:51], v[64:65]
	v_pk_mul_f32 v[44:45], v[54:55], v[44:45]
	v_and_b32_e32 v47, 0xffff0000, v165
	v_and_b32_e32 v46, 0xffff0000, v164
	v_pk_mul_f32 v[44:45], v[44:45], v[46:47]
	v_and_b32_sdwa v46, v51, v213 dst_sel:DWORD dst_unused:UNUSED_PAD src0_sel:WORD_1 src1_sel:DWORD
	v_and_b32_sdwa v47, v50, v213 dst_sel:DWORD dst_unused:UNUSED_PAD src0_sel:WORD_1 src1_sel:DWORD
	v_add3_u32 v47, v50, v47, s76
	v_add3_u32 v46, v51, v46, s76
	v_and_b32_sdwa v50, v45, v213 dst_sel:DWORD dst_unused:UNUSED_PAD src0_sel:WORD_1 src1_sel:DWORD
	v_and_b32_sdwa v51, v44, v213 dst_sel:DWORD dst_unused:UNUSED_PAD src0_sel:WORD_1 src1_sel:DWORD
	v_add3_u32 v45, v45, v50, s76
	v_add3_u32 v44, v44, v51, s76
	v_and_b32_e32 v45, 0xffff0000, v45
	v_and_b32_e32 v44, 0xffff0000, v44
	v_or_b32_sdwa v45, v45, v46 dst_sel:DWORD dst_unused:UNUSED_PAD src0_sel:DWORD src1_sel:WORD_1
	v_or_b32_sdwa v44, v44, v47 dst_sel:DWORD dst_unused:UNUSED_PAD src0_sel:DWORD src1_sel:WORD_1
	global_store_dwordx2 v[82:83], v[44:45], off offset:192
	v_mov_b32_e32 v44, v40
	v_mov_b32_e32 v45, v42
	v_pk_mul_f32 v[46:47], v[44:45], v[92:93] op_sel_hi:[1,0]
	s_waitcnt vmcnt(7)
	v_mov_b32_e32 v44, v24
	v_mov_b32_e32 v45, v26
	v_mov_b32_e32 v42, v41
	v_pk_mul_f32 v[46:47], v[44:45], v[46:47]
	v_lshlrev_b32_e32 v51, 16, v163
	v_lshlrev_b32_e32 v50, 16, v162
	v_pk_mul_f32 v[40:41], v[42:43], v[92:93] op_sel_hi:[1,0]
	v_mov_b32_e32 v26, v25
	v_pk_mul_f32 v[46:47], v[46:47], v[50:51]
	v_pk_mul_f32 v[24:25], v[26:27], v[40:41]
	v_and_b32_e32 v41, 0xffff0000, v163
	v_and_b32_e32 v40, 0xffff0000, v162
	v_pk_mul_f32 v[24:25], v[24:25], v[40:41]
	v_and_b32_sdwa v40, v47, v213 dst_sel:DWORD dst_unused:UNUSED_PAD src0_sel:WORD_1 src1_sel:DWORD
	v_and_b32_sdwa v41, v46, v213 dst_sel:DWORD dst_unused:UNUSED_PAD src0_sel:WORD_1 src1_sel:DWORD
	v_mov_b32_e32 v42, v37
	v_mov_b32_e32 v43, v33
	v_add3_u32 v52, v46, v41, s76
	v_add3_u32 v53, v47, v40, s76
	v_mov_b32_e32 v40, v36
	v_mov_b32_e32 v41, v32
	v_pk_mul_f32 v[42:43], v[42:43], v[42:43]
	v_mov_b32_e32 v46, v39
	v_mov_b32_e32 v47, v35
	v_pk_fma_f32 v[40:41], v[40:41], v[40:41], v[42:43]
	v_mov_b32_e32 v42, v38
	v_mov_b32_e32 v43, v34
	v_pk_mul_f32 v[46:47], v[46:47], v[46:47]
	v_and_b32_sdwa v64, v25, v213 dst_sel:DWORD dst_unused:UNUSED_PAD src0_sel:WORD_1 src1_sel:DWORD
	v_pk_fma_f32 v[42:43], v[42:43], v[42:43], v[46:47]
	v_pk_mul_f32 v[46:47], v[28:29], v[28:29]
	v_pk_add_f32 v[40:41], v[40:41], v[42:43]
	v_pk_mul_f32 v[42:43], v[30:31], v[30:31]
	v_pk_add_f32 v[40:41], v[40:41], v[40:41] op_sel:[0,1] op_sel_hi:[1,0]
	v_pk_mov_b32 v[50:51], v[46:47], v[42:43] op_sel:[1,0]
	v_mov_b32_e32 v47, v43
	v_pk_add_f32 v[42:43], v[50:51], v[46:47]
	v_mul_f32_e32 v46, v12, v12
	v_mul_f32_e32 v47, v13, v13
	v_pk_add_f32 v[42:43], v[42:43], v[42:43] op_sel:[0,1] op_sel_hi:[1,0]
	v_mov_b32_e32 v41, v46
	v_mov_b32_e32 v43, v47
	v_pk_add_f32 v[40:41], v[40:41], v[42:43]
	v_mul_f32_e32 v42, v17, v17
	v_mul_f32_e32 v46, v19, v19
	v_mul_f32_e32 v50, v14, v14
	v_mul_f32_e32 v51, v15, v15
	v_pk_fma_f32 v[42:43], v[16:17], v[16:17], v[42:43] op_sel_hi:[1,1,0]
	v_pk_fma_f32 v[46:47], v[18:19], v[18:19], v[46:47] op_sel_hi:[1,1,0]
	v_mov_b32_e32 v43, v50
	v_mov_b32_e32 v47, v51
	v_pk_add_f32 v[42:43], v[42:43], v[46:47]
	v_pk_mul_f32 v[46:47], v[8:9], v[8:9]
	v_pk_add_f32 v[40:41], v[40:41], v[42:43]
	v_pk_mul_f32 v[42:43], v[10:11], v[10:11]
	v_pk_add_f32 v[40:41], v[40:41], v[40:41] op_sel:[0,1] op_sel_hi:[1,0]
	v_pk_mov_b32 v[50:51], v[46:47], v[42:43] op_sel:[1,0]
	v_mov_b32_e32 v47, v43
	v_pk_add_f32 v[42:43], v[50:51], v[46:47]
	v_mul_f32_e32 v46, v0, v0
	v_mul_f32_e32 v47, v1, v1
	v_pk_add_f32 v[42:43], v[42:43], v[42:43] op_sel:[0,1] op_sel_hi:[1,0]
	v_mov_b32_e32 v41, v46
	v_mov_b32_e32 v43, v47
	v_pk_add_f32 v[40:41], v[40:41], v[42:43]
	v_mul_f32_e32 v42, v5, v5
	v_mul_f32_e32 v46, v7, v7
	v_mul_f32_e32 v50, v2, v2
	v_mul_f32_e32 v51, v3, v3
	v_pk_fma_f32 v[42:43], v[4:5], v[4:5], v[42:43] op_sel_hi:[1,1,0]
	v_pk_fma_f32 v[46:47], v[6:7], v[6:7], v[46:47] op_sel_hi:[1,1,0]
	v_mov_b32_e32 v43, v50
	v_mov_b32_e32 v47, v51
	v_pk_add_f32 v[42:43], v[42:43], v[46:47]
	v_add3_u32 v25, v25, v64, s76
	v_pk_add_f32 v[40:41], v[40:41], v[42:43]
	v_and_b32_sdwa v42, v24, v213 dst_sel:DWORD dst_unused:UNUSED_PAD src0_sel:WORD_1 src1_sel:DWORD
	v_add_f32_e32 v40, v40, v41
	v_mov_b32_e32 v41, v40
	v_add3_u32 v24, v24, v42, s76
	v_and_b32_e32 v25, 0xffff0000, v25
	v_and_b32_e32 v24, 0xffff0000, v24
	v_or_b32_sdwa v25, v25, v53 dst_sel:DWORD dst_unused:UNUSED_PAD src0_sel:DWORD src1_sel:WORD_1
	s_nop 1
	v_permlane16_swap_b32_e32 v41, v40
	s_waitcnt lgkmcnt(0)
; __device__ __forceinline__ unsigned pk2(float lo, float hi) { return f2bf(lo) | (f2bf(hi) << 16); }
; __device__ __forceinline__ float rq_sum(float v) { v += __shfl_xor(v, 16); v += __shfl_xor(v, 32); return v; }
; __device__ __forceinline__ float frsq(float x) { return __builtin_amdgcn_rsqf(x); }
; __device__ __forceinline__ void ret_task(const Frame& F, int l, int task) {
;     ...
;         const float rstd = frsq(rq_sum(ss) * (1.f / HD) + EPS);
; #pragma unroll
;         for (int eb = 0; eb < 8; ++eb) {
;             const int e0 = h * HD + eb * 16 + rq * 4;
;             const f32x4 gg = g4[eb]; const u32x2 gw = gwq[qb][eb];
;             u32x2 o; o.x = pk2(acc[qb][eb][0] * rstd * gg[0] * bf_lo(gw.x), acc[qb][eb][1] * rstd * gg[1] * bf_hi(gw.x));
;             o.y = pk2(acc[qb][eb][2] * rstd * gg[2] * bf_lo(gw.y), acc[qb][eb][3] * rstd * gg[3] * bf_hi(gw.y));
;             st_u2(MIX + (size_t)t * D + 1024 + e0, o);
;         }
	v_add_f32_e32 v40, v40, v41
	ds_bpermute_b32 v41, v227, v40
	v_or_b32_sdwa v24, v24, v52 dst_sel:DWORD dst_unused:UNUSED_PAD src0_sel:DWORD src1_sel:WORD_1
	global_store_dwordx2 v[82:83], v[24:25], off offset:224
	v_mov_b32_e32 v43, v38
	v_mov_b32_e32 v38, v37
	s_waitcnt lgkmcnt(0)
	v_add_f32_e32 v24, v40, v41
	v_fmamk_f32 v24, v24, 0x3c000000, v214
	v_rsq_f32_e32 v24, v24
	v_mov_b32_e32 v42, v36
	v_lshlrev_b32_e32 v47, 16, v161
	v_lshlrev_b32_e32 v46, 16, v160
	v_pk_mul_f32 v[36:37], v[38:39], v[24:25] op_sel_hi:[1,0]
	v_pk_mul_f32 v[42:43], v[42:43], v[24:25] op_sel_hi:[1,0]
	v_pk_mul_f32 v[22:23], v[22:23], v[36:37]
	v_and_b32_e32 v37, 0xffff0000, v161
	v_and_b32_e32 v36, 0xffff0000, v160
	v_pk_mul_f32 v[42:43], v[80:81], v[42:43]
	v_pk_mul_f32 v[22:23], v[22:23], v[36:37]
	v_pk_mul_f32 v[42:43], v[42:43], v[46:47]
	v_and_b32_sdwa v38, v22, v213 dst_sel:DWORD dst_unused:UNUSED_PAD src0_sel:WORD_1 src1_sel:DWORD
	v_lshlrev_b64 v[40:41], 12, v[194:195]
	v_and_b32_sdwa v36, v42, v213 dst_sel:DWORD dst_unused:UNUSED_PAD src0_sel:WORD_1 src1_sel:DWORD
	v_add3_u32 v22, v22, v38, s76
	v_lshl_add_u64 v[40:41], s[62:63], 0, v[40:41]
	v_add3_u32 v36, v42, v36, s76
	v_and_b32_sdwa v37, v23, v213 dst_sel:DWORD dst_unused:UNUSED_PAD src0_sel:WORD_1 src1_sel:DWORD
	v_and_b32_e32 v22, 0xffff0000, v22
	v_and_b32_sdwa v25, v43, v213 dst_sel:DWORD dst_unused:UNUSED_PAD src0_sel:WORD_1 src1_sel:DWORD
	v_add3_u32 v23, v23, v37, s76
	v_or_b32_sdwa v22, v22, v36 dst_sel:DWORD dst_unused:UNUSED_PAD src0_sel:DWORD src1_sel:WORD_1
	v_lshl_add_u64 v[36:37], v[40:41], 0, v[156:157]
	v_add3_u32 v25, v43, v25, s76
	v_and_b32_e32 v23, 0xffff0000, v23
	v_lshl_add_u64 v[38:39], v[36:37], 0, s[4:5]
	v_add_co_u32_e32 v36, vcc, s0, v36
	v_or_b32_sdwa v23, v23, v25 dst_sel:DWORD dst_unused:UNUSED_PAD src0_sel:DWORD src1_sel:WORD_1
	s_nop 0
	v_addc_co_u32_e32 v37, vcc, 0, v37, vcc
	global_store_dwordx2 v[36:37], v[22:23], off offset:2048
	v_mov_b32_e32 v22, v32
	v_mov_b32_e32 v23, v34
	v_pk_mul_f32 v[22:23], v[22:23], v[24:25] op_sel_hi:[1,0]
	v_mov_b32_e32 v34, v33
	v_pk_mul_f32 v[20:21], v[20:21], v[22:23]
	v_lshlrev_b32_e32 v23, 16, v159
	v_lshlrev_b32_e32 v22, 16, v158
	v_pk_mul_f32 v[20:21], v[20:21], v[22:23]
	v_pk_mul_f32 v[22:23], v[34:35], v[24:25] op_sel_hi:[1,0]
	v_and_b32_e32 v33, 0xffff0000, v159
	v_pk_mul_f32 v[22:23], v[62:63], v[22:23]
	v_and_b32_e32 v32, 0xffff0000, v158
	v_pk_mul_f32 v[22:23], v[22:23], v[32:33]
	v_and_b32_sdwa v25, v21, v213 dst_sel:DWORD dst_unused:UNUSED_PAD src0_sel:WORD_1 src1_sel:DWORD
	v_and_b32_sdwa v32, v20, v213 dst_sel:DWORD dst_unused:UNUSED_PAD src0_sel:WORD_1 src1_sel:DWORD
	v_add3_u32 v20, v20, v32, s76
	v_add3_u32 v21, v21, v25, s76
	v_and_b32_sdwa v25, v23, v213 dst_sel:DWORD dst_unused:UNUSED_PAD src0_sel:WORD_1 src1_sel:DWORD
	v_and_b32_sdwa v32, v22, v213 dst_sel:DWORD dst_unused:UNUSED_PAD src0_sel:WORD_1 src1_sel:DWORD
	v_add3_u32 v23, v23, v25, s76
	v_add3_u32 v22, v22, v32, s76
	v_and_b32_e32 v23, 0xffff0000, v23
	v_and_b32_e32 v22, 0xffff0000, v22
	v_or_b32_sdwa v21, v23, v21 dst_sel:DWORD dst_unused:UNUSED_PAD src0_sel:DWORD src1_sel:WORD_1
	v_or_b32_sdwa v20, v22, v20 dst_sel:DWORD dst_unused:UNUSED_PAD src0_sel:DWORD src1_sel:WORD_1
	global_store_dwordx2 v[38:39], v[20:21], off offset:32
	v_mov_b32_e32 v20, v28
	v_mov_b32_e32 v21, v30
	v_pk_mul_f32 v[20:21], v[20:21], v[24:25] op_sel_hi:[1,0]
	v_lshlrev_b32_e32 v23, 16, v155
	v_pk_mul_f32 v[20:21], v[60:61], v[20:21]
	v_lshlrev_b32_e32 v22, 16, v154
	v_mov_b32_e32 v30, v29
	v_pk_mul_f32 v[20:21], v[20:21], v[22:23]
	v_pk_mul_f32 v[22:23], v[30:31], v[24:25] op_sel_hi:[1,0]
	v_and_b32_e32 v29, 0xffff0000, v155
	v_pk_mul_f32 v[22:23], v[58:59], v[22:23]
	v_and_b32_e32 v28, 0xffff0000, v154
	v_pk_mul_f32 v[22:23], v[22:23], v[28:29]
	v_and_b32_sdwa v25, v21, v213 dst_sel:DWORD dst_unused:UNUSED_PAD src0_sel:WORD_1 src1_sel:DWORD
	v_and_b32_sdwa v28, v20, v213 dst_sel:DWORD dst_unused:UNUSED_PAD src0_sel:WORD_1 src1_sel:DWORD
	v_add3_u32 v20, v20, v28, s76
	v_add3_u32 v21, v21, v25, s76
	v_and_b32_sdwa v25, v23, v213 dst_sel:DWORD dst_unused:UNUSED_PAD src0_sel:WORD_1 src1_sel:DWORD
	v_and_b32_sdwa v28, v22, v213 dst_sel:DWORD dst_unused:UNUSED_PAD src0_sel:WORD_1 src1_sel:DWORD
	v_add3_u32 v23, v23, v25, s76
	v_add3_u32 v22, v22, v28, s76
	v_and_b32_e32 v23, 0xffff0000, v23
	v_and_b32_e32 v22, 0xffff0000, v22
	v_or_b32_sdwa v21, v23, v21 dst_sel:DWORD dst_unused:UNUSED_PAD src0_sel:DWORD src1_sel:WORD_1
	v_or_b32_sdwa v20, v22, v20 dst_sel:DWORD dst_unused:UNUSED_PAD src0_sel:DWORD src1_sel:WORD_1
	global_store_dwordx2 v[38:39], v[20:21], off offset:64
	v_mov_b32_e32 v20, v16
	v_mov_b32_e32 v21, v18
	v_pk_mul_f32 v[20:21], v[20:21], v[24:25] op_sel_hi:[1,0]
	v_mov_b32_e32 v18, v17
	v_pk_mul_f32 v[20:21], v[56:57], v[20:21]
	v_lshlrev_b32_e32 v23, 16, v153
	v_lshlrev_b32_e32 v22, 16, v152
	v_pk_mul_f32 v[16:17], v[18:19], v[24:25] op_sel_hi:[1,0]
	v_pk_mul_f32 v[20:21], v[20:21], v[22:23]
	v_pk_mul_f32 v[16:17], v[78:79], v[16:17]
	v_and_b32_e32 v19, 0xffff0000, v153
	v_and_b32_e32 v18, 0xffff0000, v152
	v_pk_mul_f32 v[16:17], v[16:17], v[18:19]
	v_and_b32_sdwa v18, v21, v213 dst_sel:DWORD dst_unused:UNUSED_PAD src0_sel:WORD_1 src1_sel:DWORD
	v_and_b32_sdwa v19, v20, v213 dst_sel:DWORD dst_unused:UNUSED_PAD src0_sel:WORD_1 src1_sel:DWORD
	v_add3_u32 v19, v20, v19, s76
	v_add3_u32 v18, v21, v18, s76
	v_and_b32_sdwa v20, v17, v213 dst_sel:DWORD dst_unused:UNUSED_PAD src0_sel:WORD_1 src1_sel:DWORD
	v_and_b32_sdwa v21, v16, v213 dst_sel:DWORD dst_unused:UNUSED_PAD src0_sel:WORD_1 src1_sel:DWORD
; __device__ __forceinline__ unsigned pk2(float lo, float hi) { return f2bf(lo) | (f2bf(hi) << 16); }
; __device__ __forceinline__ void ret_task(const Frame& F, int l, int task) {
;     ...
;         for (int eb = 0; eb < 8; ++eb) {
;             const int e0 = h * HD + eb * 16 + rq * 4;
;             const f32x4 gg = g4[eb]; const u32x2 gw = gwq[qb][eb];
;             u32x2 o; o.x = pk2(acc[qb][eb][0] * rstd * gg[0] * bf_lo(gw.x), acc[qb][eb][1] * rstd * gg[1] * bf_hi(gw.x));
;             o.y = pk2(acc[qb][eb][2] * rstd * gg[2] * bf_lo(gw.y), acc[qb][eb][3] * rstd * gg[3] * bf_hi(gw.y));
;             st_u2(MIX + (size_t)t * D + 1024 + e0, o);
;         }
	v_add3_u32 v17, v17, v20, s76
	v_add3_u32 v16, v16, v21, s76
	v_and_b32_e32 v17, 0xffff0000, v17
	v_and_b32_e32 v16, 0xffff0000, v16
	v_or_b32_sdwa v17, v17, v18 dst_sel:DWORD dst_unused:UNUSED_PAD src0_sel:DWORD src1_sel:WORD_1
	v_or_b32_sdwa v16, v16, v19 dst_sel:DWORD dst_unused:UNUSED_PAD src0_sel:DWORD src1_sel:WORD_1
	global_store_dwordx2 v[38:39], v[16:17], off offset:96
	v_mov_b32_e32 v16, v12
	v_mov_b32_e32 v17, v14
	v_pk_mul_f32 v[16:17], v[16:17], v[24:25] op_sel_hi:[1,0]
	v_mov_b32_e32 v14, v13
	v_pk_mul_f32 v[16:17], v[76:77], v[16:17]
	v_lshlrev_b32_e32 v19, 16, v151
	v_lshlrev_b32_e32 v18, 16, v150
	v_pk_mul_f32 v[12:13], v[14:15], v[24:25] op_sel_hi:[1,0]
	v_pk_mul_f32 v[16:17], v[16:17], v[18:19]
	v_pk_mul_f32 v[12:13], v[74:75], v[12:13]
	v_and_b32_e32 v15, 0xffff0000, v151
	v_and_b32_e32 v14, 0xffff0000, v150
	v_pk_mul_f32 v[12:13], v[12:13], v[14:15]
	v_and_b32_sdwa v14, v17, v213 dst_sel:DWORD dst_unused:UNUSED_PAD src0_sel:WORD_1 src1_sel:DWORD
	v_and_b32_sdwa v15, v16, v213 dst_sel:DWORD dst_unused:UNUSED_PAD src0_sel:WORD_1 src1_sel:DWORD
	v_add3_u32 v15, v16, v15, s76
	v_add3_u32 v14, v17, v14, s76
	v_and_b32_sdwa v16, v13, v213 dst_sel:DWORD dst_unused:UNUSED_PAD src0_sel:WORD_1 src1_sel:DWORD
	v_and_b32_sdwa v17, v12, v213 dst_sel:DWORD dst_unused:UNUSED_PAD src0_sel:WORD_1 src1_sel:DWORD
	v_add3_u32 v13, v13, v16, s76
	v_add3_u32 v12, v12, v17, s76
	v_and_b32_e32 v13, 0xffff0000, v13
	v_and_b32_e32 v12, 0xffff0000, v12
	v_or_b32_sdwa v13, v13, v14 dst_sel:DWORD dst_unused:UNUSED_PAD src0_sel:DWORD src1_sel:WORD_1
	v_or_b32_sdwa v12, v12, v15 dst_sel:DWORD dst_unused:UNUSED_PAD src0_sel:DWORD src1_sel:WORD_1
	global_store_dwordx2 v[38:39], v[12:13], off offset:128
	v_mov_b32_e32 v12, v8
	v_mov_b32_e32 v13, v10
	v_pk_mul_f32 v[12:13], v[12:13], v[24:25] op_sel_hi:[1,0]
	v_mov_b32_e32 v10, v9
	v_pk_mul_f32 v[12:13], v[68:69], v[12:13]
	v_lshlrev_b32_e32 v15, 16, v149
	v_lshlrev_b32_e32 v14, 16, v148
	v_pk_mul_f32 v[8:9], v[10:11], v[24:25] op_sel_hi:[1,0]
	v_pk_mul_f32 v[12:13], v[12:13], v[14:15]
	v_pk_mul_f32 v[8:9], v[66:67], v[8:9]
	v_and_b32_e32 v11, 0xffff0000, v149
	v_and_b32_e32 v10, 0xffff0000, v148
	v_pk_mul_f32 v[8:9], v[8:9], v[10:11]
	v_and_b32_sdwa v10, v13, v213 dst_sel:DWORD dst_unused:UNUSED_PAD src0_sel:WORD_1 src1_sel:DWORD
	v_and_b32_sdwa v11, v12, v213 dst_sel:DWORD dst_unused:UNUSED_PAD src0_sel:WORD_1 src1_sel:DWORD
	v_add3_u32 v11, v12, v11, s76
	v_add3_u32 v10, v13, v10, s76
	v_and_b32_sdwa v12, v9, v213 dst_sel:DWORD dst_unused:UNUSED_PAD src0_sel:WORD_1 src1_sel:DWORD
	v_and_b32_sdwa v13, v8, v213 dst_sel:DWORD dst_unused:UNUSED_PAD src0_sel:WORD_1 src1_sel:DWORD
	v_add3_u32 v9, v9, v12, s76
	v_add3_u32 v8, v8, v13, s76
	v_and_b32_e32 v9, 0xffff0000, v9
	v_and_b32_e32 v8, 0xffff0000, v8
	v_or_b32_sdwa v9, v9, v10 dst_sel:DWORD dst_unused:UNUSED_PAD src0_sel:DWORD src1_sel:WORD_1
	v_or_b32_sdwa v8, v8, v11 dst_sel:DWORD dst_unused:UNUSED_PAD src0_sel:DWORD src1_sel:WORD_1
	global_store_dwordx2 v[38:39], v[8:9], off offset:160
	v_mov_b32_e32 v8, v4
	v_mov_b32_e32 v9, v6
	v_pk_mul_f32 v[8:9], v[8:9], v[24:25] op_sel_hi:[1,0]
	v_mov_b32_e32 v6, v5
	v_pk_mul_f32 v[8:9], v[48:49], v[8:9]
	v_lshlrev_b32_e32 v11, 16, v147
	v_lshlrev_b32_e32 v10, 16, v146
	v_pk_mul_f32 v[4:5], v[6:7], v[24:25] op_sel_hi:[1,0]
	v_pk_mul_f32 v[8:9], v[8:9], v[10:11]
	v_pk_mul_f32 v[4:5], v[54:55], v[4:5]
	v_and_b32_e32 v7, 0xffff0000, v147
	v_and_b32_e32 v6, 0xffff0000, v146
	v_pk_mul_f32 v[4:5], v[4:5], v[6:7]
	v_and_b32_sdwa v6, v9, v213 dst_sel:DWORD dst_unused:UNUSED_PAD src0_sel:WORD_1 src1_sel:DWORD
	v_and_b32_sdwa v7, v8, v213 dst_sel:DWORD dst_unused:UNUSED_PAD src0_sel:WORD_1 src1_sel:DWORD
	v_add3_u32 v7, v8, v7, s76
	v_add3_u32 v6, v9, v6, s76
	v_and_b32_sdwa v8, v5, v213 dst_sel:DWORD dst_unused:UNUSED_PAD src0_sel:WORD_1 src1_sel:DWORD
	v_and_b32_sdwa v9, v4, v213 dst_sel:DWORD dst_unused:UNUSED_PAD src0_sel:WORD_1 src1_sel:DWORD
	v_add3_u32 v5, v5, v8, s76
	v_add3_u32 v4, v4, v9, s76
	v_and_b32_e32 v5, 0xffff0000, v5
	v_and_b32_e32 v4, 0xffff0000, v4
	v_or_b32_sdwa v5, v5, v6 dst_sel:DWORD dst_unused:UNUSED_PAD src0_sel:DWORD src1_sel:WORD_1
	v_or_b32_sdwa v4, v4, v7 dst_sel:DWORD dst_unused:UNUSED_PAD src0_sel:DWORD src1_sel:WORD_1
	global_store_dwordx2 v[38:39], v[4:5], off offset:192
	v_mov_b32_e32 v4, v0
	v_mov_b32_e32 v5, v2
	v_pk_mul_f32 v[4:5], v[4:5], v[24:25] op_sel_hi:[1,0]
	v_mov_b32_e32 v2, v1
	v_pk_mul_f32 v[4:5], v[44:45], v[4:5]
	v_lshlrev_b32_e32 v7, 16, v145
	v_lshlrev_b32_e32 v6, 16, v144
	v_pk_mul_f32 v[0:1], v[2:3], v[24:25] op_sel_hi:[1,0]
	v_pk_mul_f32 v[4:5], v[4:5], v[6:7]
	v_pk_mul_f32 v[0:1], v[26:27], v[0:1]
	v_and_b32_e32 v3, 0xffff0000, v145
	v_and_b32_e32 v2, 0xffff0000, v144
	v_pk_mul_f32 v[0:1], v[0:1], v[2:3]
	v_and_b32_sdwa v2, v5, v213 dst_sel:DWORD dst_unused:UNUSED_PAD src0_sel:WORD_1 src1_sel:DWORD
	v_and_b32_sdwa v3, v4, v213 dst_sel:DWORD dst_unused:UNUSED_PAD src0_sel:WORD_1 src1_sel:DWORD
	v_add3_u32 v3, v4, v3, s76
	v_add3_u32 v2, v5, v2, s76
	v_and_b32_sdwa v4, v1, v213 dst_sel:DWORD dst_unused:UNUSED_PAD src0_sel:WORD_1 src1_sel:DWORD
	v_and_b32_sdwa v5, v0, v213 dst_sel:DWORD dst_unused:UNUSED_PAD src0_sel:WORD_1 src1_sel:DWORD
	v_add3_u32 v1, v1, v4, s76
	v_add3_u32 v0, v0, v5, s76
	v_and_b32_e32 v1, 0xffff0000, v1
	v_and_b32_e32 v0, 0xffff0000, v0
	v_or_b32_sdwa v1, v1, v2 dst_sel:DWORD dst_unused:UNUSED_PAD src0_sel:DWORD src1_sel:WORD_1
	v_or_b32_sdwa v0, v0, v3 dst_sel:DWORD dst_unused:UNUSED_PAD src0_sel:DWORD src1_sel:WORD_1
	global_store_dwordx2 v[38:39], v[0:1], off offset:224
	s_cbranch_scc1 .LBB0_659

; __device__ __forceinline__ unsigned cvt_pk_bf16(float lo, float hi) { unsigned r; asm volatile("v_cvt_pk_bf16_f32 %0, %1, %2" : "=v"(r) : "v"(lo), "v"(hi)); return r; }
;     __device__ __forceinline__ void operator()(const f32x4 (&acc)[2][2][4][2], const Unit& u, int wr, int wc, int fr, int fq) const {
;     ...
;                         const f32x4 v = acc[ai][bj][m][n] + r;
;                         typedef unsigned u32x2_s __attribute__((ext_vector_type(2))); u32x2_s w; w.x = cvt_pk_bf16(v[0], v[1]); w.y = cvt_pk_bf16(v[2], v[3]);
;                         *(u32x2_s*)(XB + ro + bj * HALF + n * 16) = w;
;                         s += (v[0] * v[0] + v[1] * v[1]) + (v[2] * v[2] + v[3] * v[3]); }
;                 s += __shfl_xor(s, 16); s += __shfl_xor(s, 32);
;                 if (fq == 0) ss2[(size_t)(u.pn * 4 + wc) * MT + row] = s; }
.LBB0_744:
	v_mul_f32_e32 v125, v125, v125
	v_mul_f32_e32 v144, v149, v149
	v_mul_f32_e32 v131, v131, v131
	v_fmac_f32_e32 v125, v124, v124
	v_mul_f32_e32 v124, v127, v127
	v_mul_f32_e32 v121, v121, v121
	v_fmac_f32_e32 v144, v148, v148
	v_fmac_f32_e32 v131, v130, v130
	v_fmac_f32_e32 v124, v126, v126
	v_fmac_f32_e32 v121, v120, v120
	v_mul_f32_e32 v120, v123, v123
	v_pk_add_f32 v[114:115], v[114:115], v[118:119]
	v_pk_add_f32 v[116:117], v[112:113], v[116:117]
	v_add_f32_e32 v130, v144, v131
	v_add_f32_e32 v124, v125, v124
	v_fmac_f32_e32 v120, v122, v122
	v_mul_f32_e32 v112, v117, v117
	v_mul_f32_e32 v113, v115, v115
	v_add_f32_e32 v124, v130, v124
	v_add_f32_e32 v120, v121, v120
	v_fmac_f32_e32 v112, v116, v116
	v_fmac_f32_e32 v113, v114, v114
	v_add_f32_e32 v120, v124, v120
	v_add_f32_e32 v112, v112, v113
	v_add_f32_e32 v112, v120, v112
	v_mov_b32_e32 v113, v112
	s_lshl_b32 s2, s64, 2
	s_or_b32 s2, s2, s53
	s_ashr_i32 s3, s2, 31
	s_lshl_b64 s[24:25], s[2:3], 16
	s_nop 1
	v_permlane16_swap_b32_e32 v113, v112
	s_waitcnt lgkmcnt(0)
	v_add_f32_e32 v112, v112, v113
	ds_bpermute_b32 v113, v151, v112
	v_cvt_pk_bf16_f32 v116, v116, v117
	v_cvt_pk_bf16_f32 v117, v114, v115
	global_store_dwordx2 v[128:129], v[116:117], off offset:288
	s_and_saveexec_b64 s[2:3], s[36:37]
	s_cbranch_execz .LBB0_746
	v_readlane_b32 s4, v250, 32
	v_readlane_b32 s5, v250, 33
	s_add_u32 s4, s4, s24
	s_addc_u32 s5, s5, s25
	v_lshl_add_u64 v[114:115], v[138:139], 2, s[4:5]
	s_waitcnt lgkmcnt(0)
	v_add_f32_e32 v112, v112, v113
	global_store_dword v[114:115], v112, off

; template <int N> __device__ __forceinline__ void sortdesc(float (&v)[N]) {
; #pragma unroll
;     for (int k = 2; k <= N; k <<= 1)
; #pragma unroll
;         for (int j = k >> 1; j > 0; j >>= 1)
; #pragma unroll
;             for (int i = 0; i < N; ++i) { const int p = i ^ j;
;                 if (p > i) { const bool desc = ((i & k) == 0); const float a = v[i], b = v[p], hi = fmaxf(a, b), lo = fminf(a, b); v[i] = desc ? hi : lo; v[p] = desc ? lo : hi; } }
; }
; __device__ __forceinline__ void merge16(float (&v)[16]) {
; #pragma unroll
;     for (int j = 8; j > 0; j >>= 1)
; #pragma unroll
;         for (int i = 0; i < 16; ++i) { const int p = i ^ j; if (p > i) { const float a = v[i], b = v[p]; v[i] = fmaxf(a, b); v[p] = fminf(a, b); } }
; }
; __device__ __forceinline__ void top16_of_group(float (&a)[16]) {
; #pragma unroll
;     for (int sh = 16; sh <= 32; sh <<= 1) {
;         float cc[16];
; #pragma unroll
;         for (int i = 0; i < 16; ++i) cc[i] = fmaxf(a[i], __shfl_xor(a[15 - i], sh));
;         merge16(cc);
; #pragma unroll
;         for (int i = 0; i < 16; ++i) a[i] = cc[i];
;     }
; }
; __device__ __forceinline__ void topk_task(const Frame& F, int l, int tb, int h, const LAS unsigned char* kl, LAS float* tl, const LAS unsigned char* cab) {
;     ...
;     sortdesc<16>(res);
;     top16_of_group(res);
.LBB0_1039:
	s_or_b64 exec, exec, s[0:1]
	v_max_f32_e32 v2, v2, v2
	v_max_f32_e32 v0, v0, v0
	v_max_f32_e32 v14, v0, v2
	v_min_f32_e32 v0, v0, v2
	v_max_f32_e32 v2, v4, v4
	v_max_f32_e32 v3, v3, v3
	v_max_f32_e32 v4, v3, v2
	v_min_f32_e32 v2, v3, v2
	v_max_f32_e32 v3, v6, v6
	v_max_f32_e32 v5, v5, v5
	v_max_f32_e32 v6, v5, v3
	v_min_f32_e32 v3, v5, v3
	v_max_f32_e32 v5, v8, v8
	v_max_f32_e32 v7, v7, v7
	v_max_f32_e32 v8, v7, v5
	v_min_f32_e32 v5, v7, v5
	v_max_f32_e32 v7, v10, v10
	v_max_f32_e32 v9, v9, v9
	v_max_f32_e32 v10, v9, v7
	v_min_f32_e32 v7, v9, v7
	v_max_f32_e32 v9, v12, v12
	v_max_f32_e32 v11, v11, v11
	v_max_f32_e32 v12, v11, v9
	v_min_f32_e32 v9, v11, v9
	v_max_f32_e32 v11, v14, v2
	v_min_f32_e32 v2, v14, v2
	v_max_f32_e32 v14, v0, v4
	v_min_f32_e32 v0, v0, v4
	v_max_f32_e32 v4, v6, v5
	v_min_f32_e32 v5, v6, v5
	v_max_f32_e32 v6, v3, v8
	v_min_f32_e32 v3, v3, v8
	v_max_f32_e32 v8, v10, v9
	v_min_f32_e32 v9, v10, v9
	v_max_f32_e32 v10, v7, v12
	v_min_f32_e32 v7, v7, v12
	v_max_f32_e32 v12, v11, v14
	v_min_f32_e32 v11, v11, v14
	v_max_f32_e32 v14, v2, v0
	v_min_f32_e32 v0, v2, v0
	v_max_f32_e32 v2, v5, v3
	v_min_f32_e32 v3, v5, v3
	v_max_f32_e32 v5, v4, v6
	v_min_f32_e32 v4, v4, v6
	v_min_f32_e32 v6, v8, v10
	v_min_f32_e32 v15, v9, v7
	v_max_f32_e32 v16, v12, v3
	v_min_f32_e32 v3, v12, v3
	v_max_f32_e32 v12, v11, v2
	v_min_f32_e32 v2, v11, v2
	v_max_f32_e32 v11, v14, v4
	v_min_f32_e32 v4, v14, v4
	v_max_f32_e32 v14, v0, v5
	v_min_f32_e32 v0, v0, v5
	v_max3_f32 v5, v8, v10, s59
	v_max_f32_e32 v8, v13, v13
	v_max_f32_e32 v6, 0xff800000, v6
	v_max3_f32 v7, v9, v7, s59
	v_max_f32_e32 v9, v15, v8
	v_min_f32_e32 v8, v15, v8
	v_max_f32_e32 v10, v16, v11
	v_min_f32_e32 v11, v16, v11
	v_max_f32_e32 v13, v12, v14
	v_min_f32_e32 v12, v12, v14
	v_max_f32_e32 v14, v3, v4
	v_min_f32_e32 v3, v3, v4
	v_max_f32_e32 v4, v2, v0
	v_min_f32_e32 v0, v2, v0
	v_max_f32_e32 v2, 0xff800000, v8
	v_max_f32_e32 v8, v5, v7
	v_min_f32_e32 v5, v5, v7
	v_max_f32_e32 v7, v6, v9
	v_min_f32_e32 v6, v6, v9
	v_min_f32_e32 v9, v10, v13
	v_min_f32_e32 v15, v11, v12
	v_max_f32_e32 v16, v14, v4
	v_min_f32_e32 v4, v14, v4
	v_max_f32_e32 v14, v3, v0
	v_min_f32_e32 v0, v3, v0
	v_max_f32_e32 v3, v5, v6
	v_min_f32_e32 v5, v5, v6
	v_max_f32_e32 v6, v8, v7
	v_min_f32_e32 v7, v8, v7
	v_max3_f32 v8, v10, v13, s59
	v_max_f32_e32 v9, 0xff800000, v9
	v_max3_f32 v10, v11, v12, s59
	v_max_f32_e32 v11, v15, v2
	v_min_f32_e32 v2, v15, v2
	v_max_f32_e32 v12, v16, v5
	v_min_f32_e32 v5, v16, v5
	v_max_f32_e32 v13, v4, v3
	v_min_f32_e32 v3, v4, v3
	v_max_f32_e32 v4, v14, v7
	v_min_f32_e32 v7, v14, v7
	v_max_f32_e32 v14, v0, v6
	v_min_f32_e32 v0, v0, v6
	v_max_f32_e32 v6, v8, v12
	v_min_f32_e32 v8, v8, v12
	v_max_f32_e32 v12, v9, v13
	v_min_f32_e32 v9, v9, v13
	v_max_f32_e32 v13, v10, v4
	v_min_f32_e32 v4, v10, v4
	v_max_f32_e32 v10, v11, v14
	v_min_f32_e32 v11, v11, v14
	v_max_f32_e32 v5, 0xff800000, v5
	v_max_f32_e32 v3, 0xff800000, v3
	v_max_f32_e32 v7, 0xff800000, v7
	v_max_f32_e32 v14, v2, v0
	v_min_f32_e32 v0, v2, v0
	v_max_f32_e32 v2, v6, v13
	v_min_f32_e32 v6, v6, v13
	v_max_f32_e32 v13, v12, v10
	v_min_f32_e32 v10, v12, v10
	v_max_f32_e32 v12, v8, v4
	v_min_f32_e32 v4, v8, v4
	v_max_f32_e32 v8, v9, v11
	v_min_f32_e32 v9, v9, v11
	v_max_f32_e32 v11, v5, v7
	v_min_f32_e32 v5, v5, v7
	v_max_f32_e32 v7, v3, v14
	v_min_f32_e32 v3, v3, v14
	v_max_f32_e32 v0, 0xff800000, v0
	v_max_f32_e32 v14, v2, v13
	v_min_f32_e32 v2, v2, v13
	v_max_f32_e32 v13, v6, v10
	v_min_f32_e32 v6, v6, v10
	v_max_f32_e32 v10, v12, v8
	v_min_f32_e32 v8, v12, v8
	v_max_f32_e32 v12, v4, v9
	v_min_f32_e32 v4, v4, v9
	v_max_f32_e32 v9, v11, v7
	v_min_f32_e32 v7, v11, v7
	v_max_f32_e32 v11, v5, v3
	v_min_f32_e32 v3, v5, v3
	ds_bpermute_b32 v5, v70, v0
	ds_bpermute_b32 v17, v70, v3
	ds_bpermute_b32 v19, v70, v11
	ds_bpermute_b32 v20, v70, v7
	ds_bpermute_b32 v21, v70, v9
	s_waitcnt lgkmcnt(4)
	v_max_f32_e32 v5, v5, v5
	s_waitcnt lgkmcnt(3)
	v_max_f32_e32 v17, v17, v17
	v_max_f32_e32 v5, v6, v5
	v_max_f32_e32 v17, v10, v17
	ds_bpermute_b32 v10, v70, v10
	ds_bpermute_b32 v6, v70, v6
	s_waitcnt lgkmcnt(4)
	v_max_f32_e32 v19, v19, v19
	s_waitcnt lgkmcnt(3)
	v_max_f32_e32 v20, v20, v20
	v_max_f32_e32 v16, 0xff800000, v2
	s_waitcnt lgkmcnt(1)
	v_max_f32_e32 v10, v10, v10
	s_waitcnt lgkmcnt(0)
	v_max_f32_e32 v6, v6, v6
	v_max_f32_e32 v19, v8, v19
	ds_bpermute_b32 v22, v70, v4
	v_max_f32_e32 v20, v12, v20
	ds_bpermute_b32 v12, v70, v12
	ds_bpermute_b32 v8, v70, v8
	v_max_f32_e32 v3, v3, v10
	ds_bpermute_b32 v10, v70, v13
	ds_bpermute_b32 v2, v70, v2
	v_max_f32_e32 v0, v0, v6
	ds_bpermute_b32 v6, v70, v14
	v_max_f32_e32 v21, v21, v21
	v_max_f32_e32 v4, v4, v21
	s_waitcnt lgkmcnt(5)
	v_max_f32_e32 v21, v22, v22
	s_waitcnt lgkmcnt(4)
	v_max_f32_e32 v12, v12, v12
	s_waitcnt lgkmcnt(3)
	v_max_f32_e32 v8, v8, v8
	s_waitcnt lgkmcnt(2)
	v_max_f32_e32 v10, v10, v10
	s_waitcnt lgkmcnt(1)
	v_max_f32_e32 v2, v2, v2
	s_waitcnt lgkmcnt(0)
; __device__ __forceinline__ float rq_sum(float v) { v += __shfl_xor(v, 16); v += __shfl_xor(v, 32); return v; }
; __device__ __forceinline__ float frsq(float x) { return __builtin_amdgcn_rsqf(x); }
; __device__ __forceinline__ void top16_of_group(float (&a)[16]) {
; #pragma unroll
;     for (int sh = 16; sh <= 32; sh <<= 1) {
;         float cc[16];
; #pragma unroll
;         for (int i = 0; i < 16; ++i) cc[i] = fmaxf(a[i], __shfl_xor(a[15 - i], sh));
;         merge16(cc);
; #pragma unroll
;         for (int i = 0; i < 16; ++i) a[i] = cc[i];
;     }
; }
; __device__ __forceinline__ void topk_task(const Frame& F, int l, int tb, int h, const LAS unsigned char* kl, LAS float* tl, const LAS unsigned char* cab) {
;     ...
;     float rs2 = 0.f;
; #pragma unroll
;     for (int i = 0; i < 8; ++i) rs2 += rsp[i];
;     const float lsc = frsq(rq_sum(rs2) * (1.f / D) + EPS) * LOG2E;
	v_max_f32_e32 v6, v6, v6
	v_max_f32_e32 v15, 0xff800000, v14
	v_max_f32_e32 v18, 0xff800000, v13
	v_max_f32_e32 v9, v9, v21
	v_max_f32_e32 v7, v7, v12
	v_max_f32_e32 v8, v11, v8
	v_max_f32_e32 v10, 0xff800000, v10
	v_max_f32_e32 v2, 0xff800000, v2
	v_max_f32_e32 v6, 0xff800000, v6
	v_max_f32_e32 v11, v15, v9
	v_min_f32_e32 v9, v15, v9
	v_max_f32_e32 v12, v16, v7
	v_min_f32_e32 v7, v16, v7
	v_max_f32_e32 v13, v18, v8
	v_min_f32_e32 v8, v18, v8
	v_max_f32_e32 v14, v5, v3
	v_min_f32_e32 v3, v5, v3
	v_max_f32_e32 v5, v17, v0
	v_min_f32_e32 v0, v17, v0
	v_max_f32_e32 v15, v19, v10
	v_min_f32_e32 v10, v19, v10
	v_max_f32_e32 v16, v20, v2
	v_min_f32_e32 v2, v20, v2
	v_max_f32_e32 v17, v4, v6
	v_min_f32_e32 v4, v4, v6
	v_max_f32_e32 v6, v11, v5
	v_min_f32_e32 v5, v11, v5
	v_max_f32_e32 v11, v12, v15
	v_min_f32_e32 v12, v12, v15
	v_max_f32_e32 v15, v13, v16
	v_min_f32_e32 v13, v13, v16
	v_max_f32_e32 v16, v14, v17
	v_min_f32_e32 v14, v14, v17
	v_max_f32_e32 v17, v9, v0
	v_min_f32_e32 v0, v9, v0
	v_max_f32_e32 v9, v7, v10
	v_min_f32_e32 v7, v7, v10
	v_max_f32_e32 v10, v8, v2
	v_min_f32_e32 v2, v8, v2
	v_max_f32_e32 v8, v3, v4
	v_min_f32_e32 v3, v3, v4
	v_max_f32_e32 v4, v6, v15
	v_min_f32_e32 v6, v6, v15
	v_max_f32_e32 v15, v11, v16
	v_min_f32_e32 v11, v11, v16
	v_max_f32_e32 v16, v5, v13
	v_min_f32_e32 v5, v5, v13
	v_max_f32_e32 v13, v12, v14
	v_min_f32_e32 v12, v12, v14
	v_max_f32_e32 v14, v17, v10
	v_min_f32_e32 v10, v17, v10
	v_max_f32_e32 v17, v9, v8
	v_min_f32_e32 v8, v9, v8
	v_max_f32_e32 v9, v0, v2
	v_min_f32_e32 v0, v0, v2
	v_max_f32_e32 v2, v7, v3
	v_min_f32_e32 v3, v7, v3
	v_max_f32_e32 v7, v4, v15
	v_min_f32_e32 v4, v4, v15
	v_max_f32_e32 v15, v6, v11
	v_min_f32_e32 v6, v6, v11
	v_max_f32_e32 v11, v16, v13
	v_min_f32_e32 v13, v16, v13
	v_max_f32_e32 v16, v5, v12
	v_min_f32_e32 v5, v5, v12
	v_max_f32_e32 v12, v14, v17
	v_min_f32_e32 v14, v14, v17
	v_max_f32_e32 v17, v10, v8
	v_min_f32_e32 v8, v10, v8
	ds_bpermute_b32 v21, v71, v8
	v_min_f32_e32 v10, v0, v3
	v_max_f32_e32 v0, v0, v3
	v_max_f32_e32 v19, v9, v2
	ds_bpermute_b32 v3, v71, v0
	s_waitcnt lgkmcnt(1)
	v_max_f32_e32 v21, v21, v21
	ds_bpermute_b32 v18, v71, v10
	ds_bpermute_b32 v20, v71, v19
	ds_bpermute_b32 v22, v71, v17
	ds_bpermute_b32 v23, v71, v14
	v_max_f32_e32 v21, v11, v21
	ds_bpermute_b32 v11, v71, v11
	s_waitcnt lgkmcnt(5)
	v_max_f32_e32 v3, v3, v3
	v_min_f32_e32 v2, v9, v2
	s_waitcnt lgkmcnt(4)
	v_max_f32_e32 v9, v18, v18
	v_max_f32_e32 v3, v4, v3
	s_waitcnt lgkmcnt(3)
	v_max_f32_e32 v20, v20, v20
	s_waitcnt lgkmcnt(2)
	v_max_f32_e32 v22, v22, v22
	ds_bpermute_b32 v24, v71, v12
	s_waitcnt lgkmcnt(2)
	v_max_f32_e32 v23, v23, v23
	s_waitcnt lgkmcnt(1)
	v_max_f32_e32 v11, v11, v11
	ds_bpermute_b32 v4, v71, v4
	ds_bpermute_b32 v18, v71, v2
	v_max_f32_e32 v9, v7, v9
	v_max_f32_e32 v20, v6, v20
	v_max_f32_e32 v22, v13, v22
	ds_bpermute_b32 v25, v71, v5
	v_max_f32_e32 v23, v16, v23
	ds_bpermute_b32 v16, v71, v16
	ds_bpermute_b32 v13, v71, v13
	ds_bpermute_b32 v6, v71, v6
	v_max_f32_e32 v8, v8, v11
	ds_bpermute_b32 v11, v71, v15
	ds_bpermute_b32 v7, v71, v7
	s_waitcnt lgkmcnt(8)
	v_max_f32_e32 v24, v24, v24
	s_waitcnt lgkmcnt(7)
	v_max_f32_e32 v4, v4, v4
	s_waitcnt lgkmcnt(6)
	v_max_f32_e32 v18, v18, v18
	v_max_f32_e32 v5, v5, v24
	s_waitcnt lgkmcnt(5)
	v_max_f32_e32 v24, v25, v25
	s_waitcnt lgkmcnt(4)
	v_max_f32_e32 v16, v16, v16
	s_waitcnt lgkmcnt(3)
	v_max_f32_e32 v13, v13, v13
	s_waitcnt lgkmcnt(2)
	v_max_f32_e32 v6, v6, v6
	s_waitcnt lgkmcnt(1)
	v_max_f32_e32 v11, v11, v11
	v_max_f32_e32 v0, v0, v4
	s_waitcnt lgkmcnt(0)
	v_max_f32_e32 v4, v7, v7
	v_max_f32_e32 v18, v15, v18
	v_max_f32_e32 v12, v12, v24
	v_max_f32_e32 v14, v14, v16
	v_max_f32_e32 v13, v17, v13
	v_max_f32_e32 v6, v19, v6
	v_max_f32_e32 v2, v2, v11
	v_max_f32_e32 v4, v10, v4
	v_max_f32_e32 v7, v9, v12
	v_min_f32_e32 v9, v9, v12
	v_max_f32_e32 v10, v3, v14
	v_min_f32_e32 v3, v3, v14
	v_max_f32_e32 v11, v18, v13
	v_min_f32_e32 v12, v18, v13
	v_max_f32_e32 v13, v20, v8
	v_min_f32_e32 v8, v20, v8
	v_max_f32_e32 v14, v21, v6
	v_min_f32_e32 v6, v21, v6
	v_max_f32_e32 v15, v22, v2
	v_min_f32_e32 v2, v22, v2
	v_max_f32_e32 v16, v23, v0
	v_min_f32_e32 v0, v23, v0
	v_max_f32_e32 v17, v5, v4
	v_min_f32_e32 v4, v5, v4
	v_max_f32_e32 v5, v7, v14
	v_min_f32_e32 v7, v7, v14
	v_max_f32_e32 v14, v10, v15
	v_min_f32_e32 v10, v10, v15
	v_max_f32_e32 v15, v11, v16
	v_min_f32_e32 v11, v11, v16
	v_max_f32_e32 v16, v13, v17
	v_min_f32_e32 v13, v13, v17
	v_max_f32_e32 v17, v9, v6
	v_min_f32_e32 v6, v9, v6
	v_max_f32_e32 v9, v3, v2
	v_min_f32_e32 v2, v3, v2
	v_max_f32_e32 v3, v12, v0
	v_min_f32_e32 v0, v12, v0
	v_max_f32_e32 v12, v8, v4
	v_min_f32_e32 v4, v8, v4
	v_max_f32_e32 v23, v2, v4
	v_min_f32_e32 v24, v2, v4
	s_waitcnt vmcnt(7)
	v_add_f32_e32 v2, 0, v69
	s_waitcnt vmcnt(6)
	v_add_f32_e32 v2, v2, v81
	s_waitcnt vmcnt(5)
	v_add_f32_e32 v2, v2, v82
	s_waitcnt vmcnt(4)
	v_add_f32_e32 v2, v2, v83
	s_waitcnt vmcnt(3)
	v_add_f32_e32 v2, v2, v84
	s_waitcnt vmcnt(2)
	v_add_f32_e32 v2, v2, v85
	v_max_f32_e32 v8, v5, v15
	v_min_f32_e32 v5, v5, v15
	v_max_f32_e32 v15, v14, v16
	s_waitcnt vmcnt(1)
	v_add_f32_e32 v2, v2, v86
	v_min_f32_e32 v14, v14, v16
	v_max_f32_e32 v20, v8, v15
	v_min_f32_e32 v21, v8, v15
	s_waitcnt vmcnt(0)
	v_add_f32_e32 v8, v2, v87
	v_max_f32_e32 v18, v5, v14
	v_min_f32_e32 v19, v5, v14
	ds_bpermute_b32 v14, v70, v8
	v_max_f32_e32 v16, v7, v11
	v_min_f32_e32 v7, v7, v11
	v_max_f32_e32 v11, v10, v13
	v_max_f32_e32 v4, v16, v11
	v_min_f32_e32 v5, v16, v11
	s_waitcnt lgkmcnt(0)
	v_add_f32_e32 v11, v8, v14
	v_mov_b32_e32 v14, v11
	v_min_f32_e32 v10, v10, v13
	v_max_f32_e32 v13, v17, v3
	v_max_f32_e32 v22, v9, v12
	v_min_f32_e32 v9, v9, v12
	s_nop 1
	v_permlane32_swap_b32_e32 v14, v11
	s_waitcnt lgkmcnt(0)
; #define GAS __attribute__((address_space(1)))
; __device__ __forceinline__ float rq_sum(float v) { v += __shfl_xor(v, 16); v += __shfl_xor(v, 32); return v; }
; __device__ __forceinline__ float fexp2(float x) { return __builtin_amdgcn_exp2f(x); }
; __device__ __forceinline__ float frsq(float x) { return __builtin_amdgcn_rsqf(x); }
; __device__ __forceinline__ void topk_task(const Frame& F, int l, int tb, int h, const LAS unsigned char* kl, LAS float* tl, const LAS unsigned char* cab) {
;     ...
;     const float lsc = frsq(rq_sum(rs2) * (1.f / D) + EPS) * LOG2E;
;     float den = 0.f;
; #pragma unroll
;     for (int it = 0; it < 16; ++it) den += fexp2((res[it] - res[0]) * lsc);
;     const float rden = 1.0f / den;
; #pragma unroll
;     for (int it = 0; it < 16; ++it) {
;         if ((it >> 2) == rq) {
;             const unsigned cid = decode_idx<63u>(res[it]); const unsigned ab = cab[cid];
;             const unsigned i1 = decode_idx<127u>(t0l[ab >> 4]), i2 = decode_idx<127u>(t1l[ab & 15]);
;             const size_t o = (size_t)(t0 + c) * 128 + h * 16 + it;
;             *(GAS int*)(EXPI + o) = (int)(i1 * 128u + i2);
;             *(GAS float*)(GATE + o) = fexp2((res[it] - res[0]) * lsc) * rden;
;         }
;     }
	v_add_f32_e32 v11, v11, v14
	v_fmamk_f32 v11, v11, 0x3a000000, v214
	v_rsq_f32_e32 v14, v11
	v_max_f32_e32 v12, v6, v0
	v_min_f32_e32 v0, v6, v0
	v_min_f32_e32 v17, v17, v3
	v_max_f32_e32 v2, v7, v10
	v_min_f32_e32 v3, v7, v10
	v_max_f32_e32 v6, v13, v22
	v_min_f32_e32 v7, v13, v22
	v_max_f32_e32 v10, v12, v23
	v_min_f32_e32 v11, v12, v23
	v_max_f32_e32 v12, v0, v24
	v_min_f32_e32 v13, v0, v24
	v_mul_f32_e32 v0, 0x3fb8aa3b, v14
	v_sub_f32_e32 v23, v4, v20
	v_sub_f32_e32 v14, v20, v20
	v_mul_f32_e32 v23, v23, v0
	v_mul_f32_e32 v14, v14, v0
	v_exp_f32_e32 v26, v23
	v_sub_f32_e32 v23, v5, v20
	v_exp_f32_e32 v16, v14
	v_sub_f32_e32 v14, v21, v20
	v_mul_f32_e32 v23, v23, v0
	v_mul_f32_e32 v14, v14, v0
	v_exp_f32_e32 v27, v23
	v_sub_f32_e32 v23, v2, v20
	v_max_f32_e32 v8, v17, v9
	v_min_f32_e32 v9, v17, v9
	v_exp_f32_e32 v17, v14
	v_sub_f32_e32 v14, v18, v20
	v_mul_f32_e32 v23, v23, v0
	v_mul_f32_e32 v14, v14, v0
	v_sub_f32_e32 v15, v19, v20
	v_exp_f32_e32 v29, v23
	v_sub_f32_e32 v23, v3, v20
	v_exp_f32_e32 v14, v14
	v_mul_f32_e32 v15, v15, v0
	v_mul_f32_e32 v23, v23, v0
	v_exp_f32_e32 v15, v15
	v_exp_f32_e32 v32, v23
	v_sub_f32_e32 v23, v6, v20
	v_add_f32_e32 v22, 0, v16
	v_mul_f32_e32 v23, v23, v0
	v_add_f32_e32 v22, v17, v22
	v_exp_f32_e32 v28, v23
	v_sub_f32_e32 v23, v7, v20
	v_add_f32_e32 v22, v14, v22
	v_mul_f32_e32 v23, v23, v0
	v_add_f32_e32 v22, v15, v22
	v_exp_f32_e32 v30, v23
	v_sub_f32_e32 v23, v8, v20
	v_add_f32_e32 v22, v26, v22
	v_mul_f32_e32 v23, v23, v0
	v_add_f32_e32 v22, v27, v22
	v_exp_f32_e32 v31, v23
	v_sub_f32_e32 v23, v9, v20
	v_add_f32_e32 v22, v29, v22
	v_mul_f32_e32 v23, v23, v0
	v_add_f32_e32 v22, v32, v22
	v_exp_f32_e32 v33, v23
	v_add_f32_e32 v22, v28, v22
	v_add_f32_e32 v22, v30, v22
	v_add_f32_e32 v22, v31, v22
	v_add_f32_e32 v34, v33, v22
	v_sub_f32_e32 v22, v10, v20
	v_mul_f32_e32 v22, v22, v0
	v_exp_f32_e32 v25, v22
	v_sub_f32_e32 v22, v11, v20
	v_mul_f32_e32 v22, v22, v0
	v_exp_f32_e32 v24, v22
	v_sub_f32_e32 v22, v12, v20
	v_mul_f32_e32 v22, v22, v0
	v_exp_f32_e32 v23, v22
	v_sub_f32_e32 v22, v13, v20
	v_mul_f32_e32 v0, v22, v0
	v_exp_f32_e32 v22, v0
	v_add_f32_e32 v0, v25, v34
	v_add_f32_e32 v0, v24, v0
	v_add_f32_e32 v0, v23, v0
	v_add_f32_e32 v0, v22, v0
	v_div_scale_f32 v34, s[0:1], v0, v0, 1.0
	v_rcp_f32_e32 v35, v34
	v_ashrrev_i32_e32 v69, 31, v68
	v_fma_f32 v81, -v34, v35, 1.0
	v_fmac_f32_e32 v35, v81, v35
	v_div_scale_f32 v81, vcc, 1.0, v0, 1.0
	v_mul_f32_e32 v82, v81, v35
	v_fma_f32 v83, -v34, v82, v81
	v_fmac_f32_e32 v82, v83, v35
	v_fma_f32 v34, -v34, v82, v81
	v_div_fmas_f32 v34, v34, v35, v82
	v_div_fixup_f32 v0, v34, v0, 1.0
	s_and_saveexec_b64 s[0:1], s[34:35]
	s_cbranch_execz .LBB0_1041
	v_and_b32_e32 v81, 63, v21
	v_and_b32_e32 v82, 63, v20
	v_xor_b32_e32 v83, 63, v81
	v_cmp_gt_i32_e32 vcc, 0, v21
	v_xor_b32_e32 v84, 63, v82
	s_add_u32 s2, s62, s20
	v_cndmask_b32_e32 v21, v83, v81, vcc
	v_cmp_gt_i32_e32 vcc, 0, v20
	v_and_b32_e32 v81, 63, v19
	v_xor_b32_e32 v83, 63, v81
	v_cndmask_b32_e32 v20, v84, v82, vcc
	v_and_b32_e32 v82, 63, v18
	v_cmp_gt_i32_e32 vcc, 0, v19
	v_lshlrev_b64 v[34:35], 9, v[68:69]
	s_addc_u32 s3, s63, s21
	v_xor_b32_e32 v84, 63, v82
	v_cndmask_b32_e32 v19, v83, v81, vcc
	v_cmp_gt_i32_e32 vcc, 0, v18
	v_lshl_add_u64 v[34:35], s[2:3], 0, v[34:35]
	s_add_i32 s2, 0, 0x15400
	v_cndmask_b32_e32 v18, v84, v82, vcc
	v_add_u32_e32 v20, s2, v20
	v_add_u32_e32 v21, s2, v21
	v_add_u32_e32 v18, s2, v18
	v_add_u32_e32 v19, s2, v19
	ds_read_u8 v20, v20
	ds_read_u8 v21, v21
	ds_read_u8 v18, v18
	ds_read_u8 v19, v19
	v_pk_mul_f32 v[16:17], v[16:17], v[0:1] op_sel_hi:[1,0]
	s_waitcnt lgkmcnt(2)
	v_lshrrev_b32_e32 v82, 2, v21
	v_lshrrev_b32_e32 v81, 2, v20
	s_waitcnt lgkmcnt(0)
	v_lshrrev_b32_e32 v84, 2, v19
	v_and_b32_e32 v81, 60, v81
	v_and_b32_e32 v20, 15, v20
	v_and_b32_e32 v82, 60, v82
	v_and_b32_e32 v21, 15, v21
	v_lshrrev_b32_e32 v83, 2, v18
	v_and_b32_e32 v84, 60, v84
	v_add_u32_e32 v81, v1, v81
	v_lshl_add_u32 v20, v20, 2, v1
	v_add_u32_e32 v82, v1, v82
	v_lshl_add_u32 v21, v21, 2, v1
	v_and_b32_e32 v83, 60, v83
	v_and_b32_e32 v18, 15, v18
	v_add_u32_e32 v84, v1, v84
	v_and_b32_e32 v19, 15, v19
	v_add_u32_e32 v83, v1, v83
	v_lshl_add_u32 v18, v18, 2, v1
	v_lshl_add_u32 v19, v19, 2, v1
	ds_read_b32 v81, v81
	ds_read_b32 v20, v20 offset:1088
	ds_read_b32 v82, v82
	ds_read_b32 v21, v21 offset:1088
	ds_read_b32 v85, v83
	ds_read_b32 v86, v18 offset:1088
	ds_read_b32 v84, v84
	ds_read_b32 v87, v19 offset:1088
	s_waitcnt lgkmcnt(4)
	v_and_b32_e32 v18, 0x7f, v21
	v_xor_b32_e32 v83, 0x7f, v18
	v_cmp_gt_i32_e32 vcc, 0, v21
	v_and_b32_e32 v19, 0x7f, v20
	v_xor_b32_e32 v88, 0x7f, v19
	v_cndmask_b32_e32 v18, v83, v18, vcc
	v_cmp_gt_i32_e32 vcc, 0, v20
	v_lshlrev_b32_e32 v20, 7, v82
	v_lshlrev_b32_e32 v21, 7, v81
	v_and_b32_e32 v20, 0x3f80, v20
	v_cndmask_b32_e32 v19, v88, v19, vcc
	v_and_b32_e32 v21, 0x3f80, v21
	v_xor_b32_e32 v83, 0x3f80, v20
	v_cmp_gt_i32_e32 vcc, 0, v82
	v_xor_b32_e32 v88, 0x3f80, v21
	s_nop 0
	v_cndmask_b32_e32 v20, v83, v20, vcc
	v_cmp_gt_i32_e32 vcc, 0, v81
	v_or_b32_e32 v83, v20, v18
	s_nop 0
	v_cndmask_b32_e32 v21, v88, v21, vcc
	v_or_b32_e32 v82, v21, v19
	v_pk_mul_f32 v[18:19], v[14:15], v[0:1] op_sel_hi:[1,0]
	s_waitcnt lgkmcnt(0)
	v_and_b32_e32 v14, 0x7f, v87
	v_and_b32_e32 v15, 0x7f, v86
	v_xor_b32_e32 v20, 0x7f, v14
	v_cmp_gt_i32_e32 vcc, 0, v87
	v_xor_b32_e32 v21, 0x7f, v15
	s_nop 0
	v_cndmask_b32_e32 v14, v20, v14, vcc
	v_cmp_gt_i32_e32 vcc, 0, v86
	v_lshlrev_b32_e32 v20, 7, v84
	v_and_b32_e32 v20, 0x3f80, v20
	v_cndmask_b32_e32 v15, v21, v15, vcc
	v_lshlrev_b32_e32 v21, 7, v85
	v_and_b32_e32 v21, 0x3f80, v21
	v_xor_b32_e32 v81, 0x3f80, v20
	v_cmp_gt_i32_e32 vcc, 0, v84
	v_xor_b32_e32 v86, 0x3f80, v21
	s_nop 0
	v_cndmask_b32_e32 v20, v81, v20, vcc
	v_cmp_gt_i32_e32 vcc, 0, v85
	v_or_b32_e32 v85, v20, v14
	s_nop 0
	v_cndmask_b32_e32 v21, v86, v21, vcc
	v_add_co_u32_e32 v14, vcc, 0x900000, v34
	v_or_b32_e32 v84, v21, v15
	s_nop 0
	v_addc_co_u32_e32 v15, vcc, 0, v35, vcc
	global_store_dwordx4 v[14:15], v[82:85], off
	v_add_co_u32_e32 v14, vcc, 0x1100000, v34
	s_nop 1
	v_addc_co_u32_e32 v15, vcc, 0, v35, vcc
	global_store_dwordx4 v[14:15], v[16:19], off
